# v5 + accumulator clearing with v_pk_mov_b32 pairs + K-loop back-edge SALU issued before the loop's last barrier (all ten GEMM loops)
# speedup vs baseline: 1.0021x; 1.0021x over previous
; #define PG8_LDA(dst, b, h) do { _Pragma("unroll") for (int m = 0; m < 4; ++m) _Pragma("unroll") for (int k = 0; k < 2; ++k) dst[m][k] = *(const PG8_LAS bf16x8*)(lds + PG8_SA(b, h) + aoff + m * 2048 + k * 1024); } while (0)
; #define PG8_LDB(dst, b, h) do { _Pragma("unroll") for (int n = 0; n < 2; ++n) _Pragma("unroll") for (int k = 0; k < 2; ++k) dst[n][k] = *(const PG8_LAS bf16x8*)(lds + PG8_SB(b, h) + boff + n * 2048 + k * 1024); } while (0)
; #define PG8_WAIT_V(n) asm volatile("s_waitcnt vmcnt(" #n ")" ::: "memory")
; #define PG8_WAIT_L(n) asm volatile("s_waitcnt lgkmcnt(" #n ")" ::: "memory")
; #define PG8_BAR __builtin_amdgcn_s_barrier()
; #define PG8_SCHED __builtin_amdgcn_sched_barrier(0)
; template <class Epi, class Sched, bool ALIGN_EPI = false, bool SP2 = false, bool F8 = false, bool I8 = false, bool PF = false>
; __device__ __forceinline__ void gemm_phase(PG8_LAS unsigned char* lds, const Gemm g, const Sched& S, const Epi& E, const int wave_) {
;     ...
;             if constexpr (SP2) {
;             PG8_LDB(B0, 0, 0); PG8_LDB(B1, 0, 1); PG8_SCHED; PG8_LDA(At, 0, 0); PG8_STAGE(PG8_SA(1, 1), a1 + hstep, voffA);
;             PG8_WAIT_V(8); PG8_WAIT_L(0); PG8_BAR; PG8_MMA(0, 0, At, B0); PG8_MMA(0, 1, At, B1); PG8_BAR; PG8_SCHED;
;     ...
;         for (int a = 0; a < 2; ++a)
; #pragma unroll
;             for (int b = 0; b < 2; ++b)
; #pragma unroll
;                 for (int m = 0; m < 4; ++m)
; #pragma unroll
;                     for (int n = 0; n < 2; ++n) acc[a][b][m][n] = (f32x4){0.f, 0.f, 0.f, 0.f};
.LBB0_241:
	s_ashr_i32 s41, s40, 31
	s_lshl_b64 s[44:45], s[40:41], 18
	s_add_u32 s44, s58, s44
	s_addc_u32 s45, s59, s45
	s_and_b64 s[46:47], s[42:43], exec
	s_cselect_b32 s1, s45, s49
	s_cselect_b32 s5, s44, s48
	s_ashr_i32 s39, s38, 31
	s_lshl_b64 s[46:47], s[38:39], 18
	s_add_u32 s46, s29, s46
	s_addc_u32 s47, s31, s47
	s_and_b64 s[52:53], s[42:43], exec
	s_cselect_b32 s39, s47, s51
	s_cselect_b32 s41, s46, s50
	s_add_u32 s48, s48, 0x20080
	s_addc_u32 s49, s49, 0
	s_add_u32 s75, s50, 0x100
	v_mov_b32_e32 v0, 0
	s_addc_u32 s78, s51, 0
	s_mov_b32 s79, -2
	v_mov_b32_e32 v1, v0
	v_mov_b32_e32 v2, v0
	v_mov_b32_e32 v3, v0
	v_mov_b32_e32 v4, v0
	v_mov_b32_e32 v5, v0
	v_mov_b32_e32 v6, v0
	v_mov_b32_e32 v7, v0
	s_waitcnt vmcnt(0)
	v_pk_mov_b32 v[16:17], 0, 0
	v_pk_mov_b32 v[18:19], 0, 0
	v_pk_mov_b32 v[20:21], 0, 0
	v_pk_mov_b32 v[22:23], 0, 0
	v_pk_mov_b32 v[32:33], 0, 0
	v_pk_mov_b32 v[34:35], 0, 0
	v_pk_mov_b32 v[36:37], 0, 0
	v_pk_mov_b32 v[38:39], 0, 0
	v_pk_mov_b32 v[48:49], 0, 0
	v_pk_mov_b32 v[50:51], 0, 0
	v_pk_mov_b32 v[52:53], 0, 0
	v_pk_mov_b32 v[54:55], 0, 0
	v_pk_mov_b32 v[8:9], 0, 0
	v_pk_mov_b32 v[10:11], 0, 0
	v_pk_mov_b32 v[12:13], 0, 0
	v_pk_mov_b32 v[14:15], 0, 0
	v_pk_mov_b32 v[24:25], 0, 0
	v_pk_mov_b32 v[26:27], 0, 0
	v_pk_mov_b32 v[28:29], 0, 0
	v_pk_mov_b32 v[30:31], 0, 0
	v_pk_mov_b32 v[40:41], 0, 0
	v_pk_mov_b32 v[42:43], 0, 0
	v_pk_mov_b32 v[44:45], 0, 0
	v_pk_mov_b32 v[46:47], 0, 0
	v_pk_mov_b32 v[56:57], 0, 0
	v_pk_mov_b32 v[58:59], 0, 0
	v_pk_mov_b32 v[60:61], 0, 0
	v_pk_mov_b32 v[62:63], 0, 0
	v_pk_mov_b32 v[64:65], 0, 0
	v_pk_mov_b32 v[66:67], 0, 0
	v_pk_mov_b32 v[68:69], 0, 0
	v_pk_mov_b32 v[70:71], 0, 0
	v_pk_mov_b32 v[80:81], 0, 0
	v_pk_mov_b32 v[82:83], 0, 0
	v_pk_mov_b32 v[84:85], 0, 0
	v_pk_mov_b32 v[86:87], 0, 0
	v_pk_mov_b32 v[96:97], 0, 0
	v_pk_mov_b32 v[98:99], 0, 0
	v_pk_mov_b32 v[100:101], 0, 0
	v_pk_mov_b32 v[102:103], 0, 0
	v_pk_mov_b32 v[112:113], 0, 0
	v_pk_mov_b32 v[114:115], 0, 0
	v_pk_mov_b32 v[116:117], 0, 0
	v_pk_mov_b32 v[118:119], 0, 0
	v_pk_mov_b32 v[72:73], 0, 0
	v_pk_mov_b32 v[74:75], 0, 0
	v_pk_mov_b32 v[76:77], 0, 0
	v_pk_mov_b32 v[78:79], 0, 0
	v_pk_mov_b32 v[88:89], 0, 0
	v_pk_mov_b32 v[90:91], 0, 0
	v_pk_mov_b32 v[92:93], 0, 0
	v_pk_mov_b32 v[94:95], 0, 0
	v_pk_mov_b32 v[104:105], 0, 0
	v_pk_mov_b32 v[106:107], 0, 0
	v_pk_mov_b32 v[108:109], 0, 0
	v_pk_mov_b32 v[110:111], 0, 0
	v_pk_mov_b32 v[120:121], 0, 0
	v_pk_mov_b32 v[122:123], 0, 0
	v_pk_mov_b32 v[124:125], 0, 0
	v_pk_mov_b32 v[126:127], 0, 0
.LBB0_242:
	ds_read_b128 v[128:131], v180
	ds_read_b128 v[132:135], v180 offset:1024
	ds_read_b128 v[150:153], v180 offset:2048
	ds_read_b128 v[154:157], v180 offset:3072
	ds_read_b128 v[158:161], v181
	ds_read_b128 v[162:165], v181 offset:1024
	ds_read_b128 v[166:169], v181 offset:2048
	ds_read_b128 v[170:173], v181 offset:3072
	s_add_u32 s50, s48, 0xfffe0080
	s_addc_u32 s51, s49, -1
	s_cmp_eq_u32 s79, 4
	s_cselect_b32 s53, s1, s51
	s_cselect_b32 s52, s5, s50
	s_cselect_b32 s51, s39, s78
	s_cselect_b32 s50, s41, s75
	v_lshl_add_u64 v[212:213], s[48:49], 0, v[144:145]
	s_add_i32 m0, s35, 0xc000
	ds_read_b128 v[174:177], v182
	ds_read_b128 v[184:187], v182 offset:1024
	ds_read_b128 v[188:191], v182 offset:2048
	ds_read_b128 v[192:195], v182 offset:3072
	ds_read_b128 v[196:199], v182 offset:4096
	ds_read_b128 v[200:203], v182 offset:5120
	ds_read_b128 v[204:207], v182 offset:6144
	ds_read_b128 v[208:211], v182 offset:7168
	global_load_lds_dwordx4 v[212:213], off
	v_lshl_add_u64 v[212:213], s[48:49], 0, v[146:147]
	s_add_i32 m0, s35, 0xe000
	s_nop 0
	global_load_lds_dwordx4 v[212:213], off
	s_waitcnt vmcnt(8)
	s_waitcnt lgkmcnt(0)
	s_barrier
	s_waitcnt lgkmcnt(0)
	v_mfma_i32_16x16x64_i8 v[124:127], v[128:131], v[174:177], v[124:127]
	v_mfma_i32_16x16x64_i8 v[120:123], v[150:153], v[174:177], v[120:123]
	v_mfma_i32_16x16x64_i8 v[108:111], v[128:131], v[188:191], v[108:111]
	v_mfma_i32_16x16x64_i8 v[104:107], v[150:153], v[188:191], v[104:107]
	v_mfma_i32_16x16x64_i8 v[92:95], v[128:131], v[196:199], v[92:95]
	v_mfma_i32_16x16x64_i8 v[88:91], v[150:153], v[196:199], v[88:91]
	v_mfma_i32_16x16x64_i8 v[76:79], v[128:131], v[204:207], v[76:79]
	v_mfma_i32_16x16x64_i8 v[72:75], v[150:153], v[204:207], v[72:75]
	v_mfma_i32_16x16x64_i8 v[124:127], v[132:135], v[184:187], v[124:127]
	v_mfma_i32_16x16x64_i8 v[120:123], v[154:157], v[184:187], v[120:123]
	v_mfma_i32_16x16x64_i8 v[108:111], v[132:135], v[192:195], v[108:111]
	v_mfma_i32_16x16x64_i8 v[104:107], v[154:157], v[192:195], v[104:107]
	v_mfma_i32_16x16x64_i8 v[92:95], v[132:135], v[200:203], v[92:95]
	v_mfma_i32_16x16x64_i8 v[88:91], v[154:157], v[200:203], v[88:91]
	v_mfma_i32_16x16x64_i8 v[76:79], v[132:135], v[208:211], v[76:79]
	v_mfma_i32_16x16x64_i8 v[72:75], v[154:157], v[208:211], v[72:75]
	v_mfma_i32_16x16x64_i8 v[116:119], v[158:161], v[174:177], v[116:119]
	v_mfma_i32_16x16x64_i8 v[112:115], v[166:169], v[174:177], v[112:115]
	v_mfma_i32_16x16x64_i8 v[100:103], v[158:161], v[188:191], v[100:103]
	v_mfma_i32_16x16x64_i8 v[96:99], v[166:169], v[188:191], v[96:99]
	v_mfma_i32_16x16x64_i8 v[84:87], v[158:161], v[196:199], v[84:87]
	v_mfma_i32_16x16x64_i8 v[80:83], v[166:169], v[196:199], v[80:83]
	v_mfma_i32_16x16x64_i8 v[68:71], v[158:161], v[204:207], v[68:71]
	v_mfma_i32_16x16x64_i8 v[64:67], v[166:169], v[204:207], v[64:67]
	v_mfma_i32_16x16x64_i8 v[116:119], v[162:165], v[184:187], v[116:119]
	v_mfma_i32_16x16x64_i8 v[112:115], v[170:173], v[184:187], v[112:115]
	v_mfma_i32_16x16x64_i8 v[100:103], v[162:165], v[192:195], v[100:103]
	v_mfma_i32_16x16x64_i8 v[96:99], v[170:173], v[192:195], v[96:99]
	v_mfma_i32_16x16x64_i8 v[84:87], v[162:165], v[200:203], v[84:87]
	v_mfma_i32_16x16x64_i8 v[80:83], v[170:173], v[200:203], v[80:83]
	v_mfma_i32_16x16x64_i8 v[68:71], v[162:165], v[208:211], v[68:71]
	v_mfma_i32_16x16x64_i8 v[64:67], v[170:173], v[208:211], v[64:67]
	s_barrier
; #define PG8_LDA(dst, b, h) do { _Pragma("unroll") for (int m = 0; m < 4; ++m) _Pragma("unroll") for (int k = 0; k < 2; ++k) dst[m][k] = *(const PG8_LAS bf16x8*)(lds + PG8_SA(b, h) + aoff + m * 2048 + k * 1024); } while (0)
; #define PG8_LDB(dst, b, h) do { _Pragma("unroll") for (int n = 0; n < 2; ++n) _Pragma("unroll") for (int k = 0; k < 2; ++k) dst[n][k] = *(const PG8_LAS bf16x8*)(lds + PG8_SB(b, h) + boff + n * 2048 + k * 1024); } while (0)
; #define PG8_WAIT_V(n) asm volatile("s_waitcnt vmcnt(" #n ")" ::: "memory")
; #define PG8_WAIT_L(n) asm volatile("s_waitcnt lgkmcnt(" #n ")" ::: "memory")
; #define PG8_BAR __builtin_amdgcn_s_barrier()
; #define PG8_SCHED __builtin_amdgcn_sched_barrier(0)
; template <class Epi, class Sched, bool ALIGN_EPI = false, bool SP2 = false, bool F8 = false, bool I8 = false, bool PF = false>
; __device__ __forceinline__ void gemm_phase(PG8_LAS unsigned char* lds, const Gemm g, const Sched& S, const Epi& E, const int wave_) {
;     ...
;             if constexpr (SP2) {
;             PG8_LDB(B0, 0, 0); PG8_LDB(B1, 0, 1); PG8_SCHED; PG8_LDA(At, 0, 0); PG8_STAGE(PG8_SA(1, 1), a1 + hstep, voffA);
;             PG8_WAIT_V(8); PG8_WAIT_L(0); PG8_BAR; PG8_MMA(0, 0, At, B0); PG8_MMA(0, 1, At, B1); PG8_BAR; PG8_SCHED;
;             PG8_LDA(At, 0, 1); PG8_STAGE(PG8_SB(0, 0), b2, voffB); PG8_STAGE(PG8_SB(0, 1), b2 + hstep, voffB); PG8_STAGE(PG8_SA(0, 0), a2, voffA);
;             PG8_WAIT_V(8); PG8_WAIT_L(0); PG8_BAR; PG8_MMA(1, 0, At, B0); PG8_MMA(1, 1, At, B1); PG8_BAR; PG8_SCHED;
;             PG8_LDB(B0, 1, 0); PG8_LDB(B1, 1, 1); PG8_SCHED; PG8_LDA(At, 1, 0); PG8_STAGE(PG8_SA(0, 1), a2 + hstep, voffA);
;             PG8_WAIT_V(8); PG8_WAIT_L(0); PG8_BAR; PG8_MMA(0, 0, At, B0); PG8_MMA(0, 1, At, B1); PG8_BAR; PG8_SCHED;
;             PG8_LDA(At, 1, 1); PG8_STAGE(PG8_SB(1, 0), b3, voffB); PG8_STAGE(PG8_SB(1, 1), b3 + hstep, voffB); PG8_STAGE(PG8_SA(1, 0), a3, voffA);
;             PG8_WAIT_V(8); PG8_WAIT_L(0); PG8_BAR; PG8_MMA(1, 0, At, B0); PG8_MMA(1, 1, At, B1); PG8_BAR; PG8_SCHED;
	s_add_i32 s86, s66, s27
	v_lshl_add_u64 v[212:213], s[50:51], 0, v[138:139]
	s_mov_b32 m0, s86
	ds_read_b128 v[174:177], v182 offset:16384
	ds_read_b128 v[184:187], v182 offset:17408
	ds_read_b128 v[188:191], v182 offset:18432
	ds_read_b128 v[192:195], v182 offset:19456
	ds_read_b128 v[196:199], v182 offset:20480
	ds_read_b128 v[200:203], v182 offset:21504
	ds_read_b128 v[204:207], v182 offset:22528
	ds_read_b128 v[208:211], v182 offset:23552
	global_load_lds_dwordx4 v[212:213], off
	s_add_i32 m0, s86, 0x2000
	s_add_u32 s86, s50, 0x20000
	v_lshl_add_u64 v[214:215], s[50:51], 0, v[142:143]
	s_addc_u32 s87, s51, 0
	s_add_i32 vcc_lo, s67, s27
	global_load_lds_dwordx4 v[214:215], off
	v_lshl_add_u64 v[216:217], s[86:87], 0, v[138:139]
	s_mov_b32 m0, vcc_lo
	v_lshl_add_u64 v[218:219], s[52:53], 0, v[140:141]
	global_load_lds_dwordx4 v[216:217], off
	v_lshl_add_u64 v[216:217], s[86:87], 0, v[142:143]
	s_add_i32 m0, vcc_lo, 0x2000
	s_nop 0
	global_load_lds_dwordx4 v[216:217], off
	v_lshl_add_u64 v[216:217], s[52:53], 0, v[136:137]
	s_mov_b32 m0, s35
	s_nop 0
	global_load_lds_dwordx4 v[216:217], off
	s_mov_b32 m0, s37
	s_nop 0
	global_load_lds_dwordx4 v[218:219], off
	s_waitcnt vmcnt(8)
	s_waitcnt lgkmcnt(0)
	s_barrier
	s_waitcnt lgkmcnt(0)
	v_mfma_i32_16x16x64_i8 v[60:63], v[128:131], v[174:177], v[60:63]
	v_mfma_i32_16x16x64_i8 v[56:59], v[150:153], v[174:177], v[56:59]
	v_mfma_i32_16x16x64_i8 v[44:47], v[128:131], v[188:191], v[44:47]
	v_mfma_i32_16x16x64_i8 v[40:43], v[150:153], v[188:191], v[40:43]
	v_mfma_i32_16x16x64_i8 v[28:31], v[128:131], v[196:199], v[28:31]
	v_mfma_i32_16x16x64_i8 v[24:27], v[150:153], v[196:199], v[24:27]
	v_mfma_i32_16x16x64_i8 v[12:15], v[128:131], v[204:207], v[12:15]
	v_mfma_i32_16x16x64_i8 v[8:11], v[150:153], v[204:207], v[8:11]
	v_mfma_i32_16x16x64_i8 v[60:63], v[132:135], v[184:187], v[60:63]
	v_mfma_i32_16x16x64_i8 v[56:59], v[154:157], v[184:187], v[56:59]
	v_mfma_i32_16x16x64_i8 v[44:47], v[132:135], v[192:195], v[44:47]
	v_mfma_i32_16x16x64_i8 v[40:43], v[154:157], v[192:195], v[40:43]
	v_mfma_i32_16x16x64_i8 v[28:31], v[132:135], v[200:203], v[28:31]
	v_mfma_i32_16x16x64_i8 v[24:27], v[154:157], v[200:203], v[24:27]
	v_mfma_i32_16x16x64_i8 v[12:15], v[132:135], v[208:211], v[12:15]
	v_mfma_i32_16x16x64_i8 v[8:11], v[154:157], v[208:211], v[8:11]
	v_mfma_i32_16x16x64_i8 v[52:55], v[158:161], v[174:177], v[52:55]
	v_mfma_i32_16x16x64_i8 v[48:51], v[166:169], v[174:177], v[48:51]
	v_mfma_i32_16x16x64_i8 v[36:39], v[158:161], v[188:191], v[36:39]
	v_mfma_i32_16x16x64_i8 v[32:35], v[166:169], v[188:191], v[32:35]
	v_mfma_i32_16x16x64_i8 v[20:23], v[158:161], v[196:199], v[20:23]
	v_mfma_i32_16x16x64_i8 v[16:19], v[166:169], v[196:199], v[16:19]
	v_mfma_i32_16x16x64_i8 v[4:7], v[158:161], v[204:207], v[4:7]
	v_mfma_i32_16x16x64_i8 v[0:3], v[166:169], v[204:207], v[0:3]
	v_mfma_i32_16x16x64_i8 v[52:55], v[162:165], v[184:187], v[52:55]
	v_mfma_i32_16x16x64_i8 v[48:51], v[170:173], v[184:187], v[48:51]
	v_mfma_i32_16x16x64_i8 v[36:39], v[162:165], v[192:195], v[36:39]
	v_mfma_i32_16x16x64_i8 v[32:35], v[170:173], v[192:195], v[32:35]
	v_mfma_i32_16x16x64_i8 v[20:23], v[162:165], v[200:203], v[20:23]
	v_mfma_i32_16x16x64_i8 v[16:19], v[170:173], v[200:203], v[16:19]
	v_mfma_i32_16x16x64_i8 v[4:7], v[162:165], v[208:211], v[4:7]
	v_mfma_i32_16x16x64_i8 v[0:3], v[170:173], v[208:211], v[0:3]
	s_barrier
	s_add_i32 s86, 0, 0x18000
	s_add_i32 s87, 0, 0x1c000
	v_add_u32_e32 v154, s86, v179
	v_add_u32_e32 v170, s87, v179
	ds_read_b128 v[128:131], v154
	ds_read_b128 v[132:135], v154 offset:1024
	ds_read_b128 v[150:153], v154 offset:2048
	ds_read_b128 v[154:157], v154 offset:3072
	ds_read_b128 v[158:161], v170
	ds_read_b128 v[162:165], v170 offset:1024
	ds_read_b128 v[166:169], v170 offset:2048
	ds_read_b128 v[170:173], v170 offset:3072
	s_add_u32 s52, s52, 0x20000
	s_addc_u32 s53, s53, 0
	s_mov_b32 m0, s54
	v_lshl_add_u64 v[220:221], s[52:53], 0, v[136:137]
	ds_read_b128 v[174:177], v182 offset:32768
	ds_read_b128 v[184:187], v182 offset:33792
	ds_read_b128 v[188:191], v182 offset:34816
	ds_read_b128 v[192:195], v182 offset:35840
	ds_read_b128 v[196:199], v182 offset:36864
	ds_read_b128 v[200:203], v182 offset:37888
	ds_read_b128 v[204:207], v182 offset:38912
	ds_read_b128 v[208:211], v182 offset:39936
	global_load_lds_dwordx4 v[220:221], off
	v_lshl_add_u64 v[220:221], s[52:53], 0, v[140:141]
	s_mov_b32 m0, s55
	s_nop 0
	global_load_lds_dwordx4 v[220:221], off
	s_waitcnt vmcnt(8)
	s_waitcnt lgkmcnt(0)
	s_barrier
; #define PG8_LDA(dst, b, h) do { _Pragma("unroll") for (int m = 0; m < 4; ++m) _Pragma("unroll") for (int k = 0; k < 2; ++k) dst[m][k] = *(const PG8_LAS bf16x8*)(lds + PG8_SA(b, h) + aoff + m * 2048 + k * 1024); } while (0)
; #define PG8_LDB(dst, b, h) do { _Pragma("unroll") for (int n = 0; n < 2; ++n) _Pragma("unroll") for (int k = 0; k < 2; ++k) dst[n][k] = *(const PG8_LAS bf16x8*)(lds + PG8_SB(b, h) + boff + n * 2048 + k * 1024); } while (0)
; #define PG8_WAIT_V(n) asm volatile("s_waitcnt vmcnt(" #n ")" ::: "memory")
; #define PG8_WAIT_L(n) asm volatile("s_waitcnt lgkmcnt(" #n ")" ::: "memory")
; #define PG8_BAR __builtin_amdgcn_s_barrier()
; #define PG8_SCHED __builtin_amdgcn_sched_barrier(0)
; template <class Epi, class Sched, bool ALIGN_EPI = false, bool SP2 = false, bool F8 = false, bool I8 = false, bool PF = false>
; __device__ __forceinline__ void gemm_phase(PG8_LAS unsigned char* lds, const Gemm g, const Sched& S, const Epi& E, const int wave_) {
;     ...
;             if constexpr (SP2) {
;             PG8_LDB(B0, 0, 0); PG8_LDB(B1, 0, 1); PG8_SCHED; PG8_LDA(At, 0, 0); PG8_STAGE(PG8_SA(1, 1), a1 + hstep, voffA);
;             PG8_WAIT_V(8); PG8_WAIT_L(0); PG8_BAR; PG8_MMA(0, 0, At, B0); PG8_MMA(0, 1, At, B1); PG8_BAR; PG8_SCHED;
;             PG8_LDA(At, 0, 1); PG8_STAGE(PG8_SB(0, 0), b2, voffB); PG8_STAGE(PG8_SB(0, 1), b2 + hstep, voffB); PG8_STAGE(PG8_SA(0, 0), a2, voffA);
;             PG8_WAIT_V(8); PG8_WAIT_L(0); PG8_BAR; PG8_MMA(1, 0, At, B0); PG8_MMA(1, 1, At, B1); PG8_BAR; PG8_SCHED;
;             PG8_LDB(B0, 1, 0); PG8_LDB(B1, 1, 1); PG8_SCHED; PG8_LDA(At, 1, 0); PG8_STAGE(PG8_SA(0, 1), a2 + hstep, voffA);
;             PG8_WAIT_V(8); PG8_WAIT_L(0); PG8_BAR; PG8_MMA(0, 0, At, B0); PG8_MMA(0, 1, At, B1); PG8_BAR; PG8_SCHED;
;             PG8_LDA(At, 1, 1); PG8_STAGE(PG8_SB(1, 0), b3, voffB); PG8_STAGE(PG8_SB(1, 1), b3 + hstep, voffB); PG8_STAGE(PG8_SA(1, 0), a3, voffA);
;             PG8_WAIT_V(8); PG8_WAIT_L(0); PG8_BAR; PG8_MMA(1, 0, At, B0); PG8_MMA(1, 1, At, B1); PG8_BAR; PG8_SCHED;
	s_waitcnt lgkmcnt(0)
	v_mfma_i32_16x16x64_i8 v[124:127], v[128:131], v[174:177], v[124:127]
	v_mfma_i32_16x16x64_i8 v[120:123], v[150:153], v[174:177], v[120:123]
	v_mfma_i32_16x16x64_i8 v[108:111], v[128:131], v[188:191], v[108:111]
	v_mfma_i32_16x16x64_i8 v[104:107], v[150:153], v[188:191], v[104:107]
	v_mfma_i32_16x16x64_i8 v[92:95], v[128:131], v[196:199], v[92:95]
	v_mfma_i32_16x16x64_i8 v[88:91], v[150:153], v[196:199], v[88:91]
	v_mfma_i32_16x16x64_i8 v[76:79], v[128:131], v[204:207], v[76:79]
	v_mfma_i32_16x16x64_i8 v[72:75], v[150:153], v[204:207], v[72:75]
	v_mfma_i32_16x16x64_i8 v[124:127], v[132:135], v[184:187], v[124:127]
	v_mfma_i32_16x16x64_i8 v[120:123], v[154:157], v[184:187], v[120:123]
	v_mfma_i32_16x16x64_i8 v[108:111], v[132:135], v[192:195], v[108:111]
	v_mfma_i32_16x16x64_i8 v[104:107], v[154:157], v[192:195], v[104:107]
	v_mfma_i32_16x16x64_i8 v[92:95], v[132:135], v[200:203], v[92:95]
	v_mfma_i32_16x16x64_i8 v[88:91], v[154:157], v[200:203], v[88:91]
	v_mfma_i32_16x16x64_i8 v[76:79], v[132:135], v[208:211], v[76:79]
	v_mfma_i32_16x16x64_i8 v[72:75], v[154:157], v[208:211], v[72:75]
	v_mfma_i32_16x16x64_i8 v[116:119], v[158:161], v[174:177], v[116:119]
	v_mfma_i32_16x16x64_i8 v[112:115], v[166:169], v[174:177], v[112:115]
	v_mfma_i32_16x16x64_i8 v[100:103], v[158:161], v[188:191], v[100:103]
	v_mfma_i32_16x16x64_i8 v[96:99], v[166:169], v[188:191], v[96:99]
	v_mfma_i32_16x16x64_i8 v[84:87], v[158:161], v[196:199], v[84:87]
	v_mfma_i32_16x16x64_i8 v[80:83], v[166:169], v[196:199], v[80:83]
	v_mfma_i32_16x16x64_i8 v[68:71], v[158:161], v[204:207], v[68:71]
	v_mfma_i32_16x16x64_i8 v[64:67], v[166:169], v[204:207], v[64:67]
	v_mfma_i32_16x16x64_i8 v[116:119], v[162:165], v[184:187], v[116:119]
	v_mfma_i32_16x16x64_i8 v[112:115], v[170:173], v[184:187], v[112:115]
	v_mfma_i32_16x16x64_i8 v[100:103], v[162:165], v[192:195], v[100:103]
	v_mfma_i32_16x16x64_i8 v[96:99], v[170:173], v[192:195], v[96:99]
	v_mfma_i32_16x16x64_i8 v[84:87], v[162:165], v[200:203], v[84:87]
	v_mfma_i32_16x16x64_i8 v[80:83], v[170:173], v[200:203], v[80:83]
	v_mfma_i32_16x16x64_i8 v[68:71], v[162:165], v[208:211], v[68:71]
	v_mfma_i32_16x16x64_i8 v[64:67], v[170:173], v[208:211], v[64:67]
	s_barrier
	s_add_i32 s52, s86, s27
	v_lshl_add_u64 v[212:213], v[212:213], 0, s[14:15]
	s_mov_b32 m0, s52
	ds_read_b128 v[174:177], v182 offset:49152
	ds_read_b128 v[184:187], v182 offset:50176
	ds_read_b128 v[188:191], v182 offset:51200
	ds_read_b128 v[192:195], v182 offset:52224
	ds_read_b128 v[196:199], v182 offset:53248
	ds_read_b128 v[200:203], v182 offset:54272
	ds_read_b128 v[204:207], v182 offset:55296
	ds_read_b128 v[208:211], v182 offset:56320
	global_load_lds_dwordx4 v[212:213], off
	s_add_i32 m0, s52, 0x2000
	s_add_u32 s50, s50, 0x20080
	v_lshl_add_u64 v[212:213], v[214:215], 0, s[14:15]
	s_addc_u32 s51, s51, 0
	s_add_i32 s52, s87, s27
	global_load_lds_dwordx4 v[212:213], off
	v_lshl_add_u64 v[212:213], s[50:51], 0, v[138:139]
	s_mov_b32 m0, s52
	s_nop 0
	global_load_lds_dwordx4 v[212:213], off
	v_lshl_add_u64 v[212:213], s[50:51], 0, v[142:143]
	s_add_i32 m0, s52, 0x2000
	s_nop 0
	global_load_lds_dwordx4 v[212:213], off
	v_lshl_add_u64 v[212:213], v[216:217], 0, s[14:15]
	s_mov_b32 m0, s63
	s_nop 0
	global_load_lds_dwordx4 v[212:213], off
	v_lshl_add_u64 v[212:213], v[218:219], 0, s[14:15]
	s_mov_b32 m0, s64
	s_nop 0
	global_load_lds_dwordx4 v[212:213], off
	s_waitcnt vmcnt(8)
	s_waitcnt lgkmcnt(0)
	s_barrier
	s_waitcnt lgkmcnt(0)
	v_mfma_i32_16x16x64_i8 v[60:63], v[128:131], v[174:177], v[60:63]
	v_mfma_i32_16x16x64_i8 v[56:59], v[150:153], v[174:177], v[56:59]
	v_mfma_i32_16x16x64_i8 v[44:47], v[128:131], v[188:191], v[44:47]
	v_mfma_i32_16x16x64_i8 v[40:43], v[150:153], v[188:191], v[40:43]
	v_mfma_i32_16x16x64_i8 v[28:31], v[128:131], v[196:199], v[28:31]
	v_mfma_i32_16x16x64_i8 v[24:27], v[150:153], v[196:199], v[24:27]
	v_mfma_i32_16x16x64_i8 v[12:15], v[128:131], v[204:207], v[12:15]
	v_mfma_i32_16x16x64_i8 v[8:11], v[150:153], v[204:207], v[8:11]
	v_mfma_i32_16x16x64_i8 v[60:63], v[132:135], v[184:187], v[60:63]
	v_mfma_i32_16x16x64_i8 v[56:59], v[154:157], v[184:187], v[56:59]
	v_mfma_i32_16x16x64_i8 v[44:47], v[132:135], v[192:195], v[44:47]
	v_mfma_i32_16x16x64_i8 v[40:43], v[154:157], v[192:195], v[40:43]
	v_mfma_i32_16x16x64_i8 v[28:31], v[132:135], v[200:203], v[28:31]
	v_mfma_i32_16x16x64_i8 v[24:27], v[154:157], v[200:203], v[24:27]
	v_mfma_i32_16x16x64_i8 v[12:15], v[132:135], v[208:211], v[12:15]
	v_mfma_i32_16x16x64_i8 v[8:11], v[154:157], v[208:211], v[8:11]
	v_mfma_i32_16x16x64_i8 v[52:55], v[158:161], v[174:177], v[52:55]
	v_mfma_i32_16x16x64_i8 v[48:51], v[166:169], v[174:177], v[48:51]
	v_mfma_i32_16x16x64_i8 v[36:39], v[158:161], v[188:191], v[36:39]
	v_mfma_i32_16x16x64_i8 v[32:35], v[166:169], v[188:191], v[32:35]
	v_mfma_i32_16x16x64_i8 v[20:23], v[158:161], v[196:199], v[20:23]
	v_mfma_i32_16x16x64_i8 v[16:19], v[166:169], v[196:199], v[16:19]
	v_mfma_i32_16x16x64_i8 v[4:7], v[158:161], v[204:207], v[4:7]
	v_mfma_i32_16x16x64_i8 v[0:3], v[166:169], v[204:207], v[0:3]
	v_mfma_i32_16x16x64_i8 v[52:55], v[162:165], v[184:187], v[52:55]
	v_mfma_i32_16x16x64_i8 v[48:51], v[170:173], v[184:187], v[48:51]
	v_mfma_i32_16x16x64_i8 v[36:39], v[162:165], v[192:195], v[36:39]
	v_mfma_i32_16x16x64_i8 v[32:35], v[170:173], v[192:195], v[32:35]
	v_mfma_i32_16x16x64_i8 v[20:23], v[162:165], v[200:203], v[20:23]
	v_mfma_i32_16x16x64_i8 v[16:19], v[170:173], v[200:203], v[16:19]
	v_mfma_i32_16x16x64_i8 v[4:7], v[162:165], v[208:211], v[4:7]
	v_mfma_i32_16x16x64_i8 v[0:3], v[170:173], v[208:211], v[0:3]
	s_add_i32 s79, s79, 2
	s_add_u32 s48, s48, 0x100
	s_addc_u32 s49, s49, 0
	s_add_u32 s75, s75, 0x100
	s_addc_u32 s78, s78, 0
	s_cmp_gt_u32 s79, 5
	s_barrier
	s_cbranch_scc0 .LBB0_242
	s_and_b64 vcc, exec, s[16:17]
	s_cbranch_vccz .LBB0_245
	s_barrier

; #define PG8_LDA(dst, b, h) do { _Pragma("unroll") for (int m = 0; m < 4; ++m) _Pragma("unroll") for (int k = 0; k < 2; ++k) dst[m][k] = *(const PG8_LAS bf16x8*)(lds + PG8_SA(b, h) + aoff + m * 2048 + k * 1024); } while (0)
; #define PG8_LDB(dst, b, h) do { _Pragma("unroll") for (int n = 0; n < 2; ++n) _Pragma("unroll") for (int k = 0; k < 2; ++k) dst[n][k] = *(const PG8_LAS bf16x8*)(lds + PG8_SB(b, h) + boff + n * 2048 + k * 1024); } while (0)
; #define PG8_WAIT_V(n) asm volatile("s_waitcnt vmcnt(" #n ")" ::: "memory")
; #define PG8_WAIT_L(n) asm volatile("s_waitcnt lgkmcnt(" #n ")" ::: "memory")
; #define PG8_BAR __builtin_amdgcn_s_barrier()
; #define PG8_SCHED __builtin_amdgcn_sched_barrier(0)
; template <class Epi, class Sched, bool ALIGN_EPI = false, bool SP2 = false, bool F8 = false, bool I8 = false, bool PF = false>
; __device__ __forceinline__ void gemm_phase(PG8_LAS unsigned char* lds, const Gemm g, const Sched& S, const Epi& E, const int wave_) {
;     ...
;             if constexpr (SP2) {
;             PG8_LDB(B0, 0, 0); PG8_LDB(B1, 0, 1); PG8_SCHED; PG8_LDA(At, 0, 0); PG8_STAGE(PG8_SA(1, 1), a1 + hstep, voffA);
;             PG8_WAIT_V(8); PG8_WAIT_L(0); PG8_BAR; PG8_MMA(0, 0, At, B0); PG8_MMA(0, 1, At, B1); PG8_BAR; PG8_SCHED;
;     ...
;         for (int a = 0; a < 2; ++a)
; #pragma unroll
;             for (int b = 0; b < 2; ++b)
; #pragma unroll
;                 for (int m = 0; m < 4; ++m)
; #pragma unroll
;                     for (int n = 0; n < 2; ++n) acc[a][b][m][n] = (f32x4){0.f, 0.f, 0.f, 0.f};
.LBB0_452:
	s_ashr_i32 s13, s12, 31
	s_lshl_b64 s[16:17], s[12:13], 19
	s_add_u32 s16, s26, s16
	s_addc_u32 s17, s27, s17
	s_and_b64 s[18:19], s[14:15], exec
	s_cselect_b32 s13, s17, s23
	s_cselect_b32 s52, s16, s22
	s_ashr_i32 s11, s10, 31
	s_lshl_b64 s[18:19], s[10:11], 19
	s_add_u32 s18, s34, s18
	s_addc_u32 s19, s35, s19
	s_and_b64 s[30:31], s[14:15], exec
	s_cselect_b32 s11, s19, s29
	s_cselect_b32 s53, s18, s28
	s_add_u32 s22, s22, 0x40080
	s_addc_u32 s23, s23, 0
	s_add_u32 s54, s28, 0x100
	v_mov_b32_e32 v0, 0
	s_addc_u32 s55, s29, 0
	s_mov_b32 s62, -2
	v_mov_b32_e32 v1, v0
	v_mov_b32_e32 v2, v0
	v_mov_b32_e32 v3, v0
	v_mov_b32_e32 v4, v0
	v_mov_b32_e32 v5, v0
	v_mov_b32_e32 v6, v0
	v_mov_b32_e32 v7, v0
	v_mov_b32_e32 v12, v0
	v_mov_b32_e32 v13, v0
	v_mov_b32_e32 v14, v0
	v_mov_b32_e32 v15, v0
	s_waitcnt vmcnt(0)
	v_pk_mov_b32 v[20:21], 0, 0
	v_pk_mov_b32 v[22:23], 0, 0
	v_pk_mov_b32 v[28:29], 0, 0
	v_pk_mov_b32 v[30:31], 0, 0
	v_pk_mov_b32 v[36:37], 0, 0
	v_pk_mov_b32 v[38:39], 0, 0
	v_pk_mov_b32 v[44:45], 0, 0
	v_pk_mov_b32 v[46:47], 0, 0
	v_pk_mov_b32 v[52:53], 0, 0
	v_pk_mov_b32 v[54:55], 0, 0
	v_pk_mov_b32 v[8:9], 0, 0
	v_pk_mov_b32 v[10:11], 0, 0
	v_pk_mov_b32 v[16:17], 0, 0
	v_pk_mov_b32 v[18:19], 0, 0
	v_pk_mov_b32 v[24:25], 0, 0
	v_pk_mov_b32 v[26:27], 0, 0
	v_pk_mov_b32 v[32:33], 0, 0
	v_pk_mov_b32 v[34:35], 0, 0
	v_pk_mov_b32 v[40:41], 0, 0
	v_pk_mov_b32 v[42:43], 0, 0
	v_pk_mov_b32 v[48:49], 0, 0
	v_pk_mov_b32 v[50:51], 0, 0
	v_pk_mov_b32 v[56:57], 0, 0
	v_pk_mov_b32 v[58:59], 0, 0
	v_pk_mov_b32 v[60:61], 0, 0
	v_pk_mov_b32 v[62:63], 0, 0
	v_pk_mov_b32 v[64:65], 0, 0
	v_pk_mov_b32 v[66:67], 0, 0
	v_pk_mov_b32 v[68:69], 0, 0
	v_pk_mov_b32 v[70:71], 0, 0
	v_pk_mov_b32 v[76:77], 0, 0
	v_pk_mov_b32 v[78:79], 0, 0
	v_pk_mov_b32 v[84:85], 0, 0
	v_pk_mov_b32 v[86:87], 0, 0
	v_pk_mov_b32 v[92:93], 0, 0
	v_pk_mov_b32 v[94:95], 0, 0
	v_pk_mov_b32 v[100:101], 0, 0
	v_pk_mov_b32 v[102:103], 0, 0
	v_pk_mov_b32 v[104:105], 0, 0
	v_pk_mov_b32 v[106:107], 0, 0
	v_pk_mov_b32 v[108:109], 0, 0
	v_pk_mov_b32 v[110:111], 0, 0
	v_pk_mov_b32 v[72:73], 0, 0
	v_pk_mov_b32 v[74:75], 0, 0
	v_pk_mov_b32 v[80:81], 0, 0
	v_pk_mov_b32 v[82:83], 0, 0
	v_pk_mov_b32 v[88:89], 0, 0
	v_pk_mov_b32 v[90:91], 0, 0
	v_pk_mov_b32 v[96:97], 0, 0
	v_pk_mov_b32 v[98:99], 0, 0
	v_pk_mov_b32 v[112:113], 0, 0
	v_pk_mov_b32 v[114:115], 0, 0
	v_pk_mov_b32 v[116:117], 0, 0
	v_pk_mov_b32 v[118:119], 0, 0
	v_pk_mov_b32 v[120:121], 0, 0
	v_pk_mov_b32 v[122:123], 0, 0
	v_pk_mov_b32 v[124:125], 0, 0
	v_pk_mov_b32 v[126:127], 0, 0
.LBB0_453:
	ds_read_b128 v[128:131], v175
	ds_read_b128 v[132:135], v175 offset:1024
	ds_read_b128 v[136:139], v175 offset:2048
	ds_read_b128 v[140:143], v175 offset:3072
	ds_read_b128 v[144:147], v176
	ds_read_b128 v[148:151], v176 offset:1024
	ds_read_b128 v[166:169], v176 offset:2048
	ds_read_b128 v[170:173], v176 offset:3072
	s_add_u32 s28, s22, 0xfffc0080
	s_addc_u32 s29, s23, -1
	s_cmp_eq_u32 s62, 12
	s_cselect_b32 s31, s13, s29
	s_cselect_b32 s30, s52, s28
	s_cselect_b32 s29, s11, s55
	s_cselect_b32 s28, s53, s54
	v_lshl_add_u64 v[210:211], s[22:23], 0, v[160:161]
	s_add_i32 m0, s21, 0xc000
	ds_read_b128 v[178:181], v177
	ds_read_b128 v[182:185], v177 offset:1024
	ds_read_b128 v[186:189], v177 offset:2048
	ds_read_b128 v[190:193], v177 offset:3072
	ds_read_b128 v[194:197], v177 offset:4096
	ds_read_b128 v[198:201], v177 offset:5120
	ds_read_b128 v[202:205], v177 offset:6144
	ds_read_b128 v[206:209], v177 offset:7168
	global_load_lds_dwordx4 v[210:211], off
	v_lshl_add_u64 v[210:211], s[22:23], 0, v[162:163]
	s_add_i32 m0, s21, 0xe000
	s_nop 0
	global_load_lds_dwordx4 v[210:211], off
	s_waitcnt vmcnt(8)
	s_waitcnt lgkmcnt(0)
	s_barrier
	s_waitcnt lgkmcnt(0)
	v_mfma_f32_16x16x32_bf16 v[124:127], v[128:131], v[178:181], v[124:127]
	v_mfma_f32_16x16x32_bf16 v[120:123], v[136:139], v[178:181], v[120:123]
	v_mfma_f32_16x16x32_bf16 v[116:119], v[128:131], v[186:189], v[116:119]
	v_mfma_f32_16x16x32_bf16 v[112:115], v[136:139], v[186:189], v[112:115]
	v_mfma_f32_16x16x32_bf16 v[96:99], v[128:131], v[194:197], v[96:99]
	v_mfma_f32_16x16x32_bf16 v[88:91], v[136:139], v[194:197], v[88:91]
	v_mfma_f32_16x16x32_bf16 v[80:83], v[128:131], v[202:205], v[80:83]
	v_mfma_f32_16x16x32_bf16 v[72:75], v[136:139], v[202:205], v[72:75]
	v_mfma_f32_16x16x32_bf16 v[124:127], v[132:135], v[182:185], v[124:127]
	v_mfma_f32_16x16x32_bf16 v[120:123], v[140:143], v[182:185], v[120:123]
	v_mfma_f32_16x16x32_bf16 v[116:119], v[132:135], v[190:193], v[116:119]
	v_mfma_f32_16x16x32_bf16 v[112:115], v[140:143], v[190:193], v[112:115]
	v_mfma_f32_16x16x32_bf16 v[96:99], v[132:135], v[198:201], v[96:99]
	v_mfma_f32_16x16x32_bf16 v[88:91], v[140:143], v[198:201], v[88:91]
	v_mfma_f32_16x16x32_bf16 v[80:83], v[132:135], v[206:209], v[80:83]
	v_mfma_f32_16x16x32_bf16 v[72:75], v[140:143], v[206:209], v[72:75]
	v_mfma_f32_16x16x32_bf16 v[108:111], v[144:147], v[178:181], v[108:111]
	v_mfma_f32_16x16x32_bf16 v[104:107], v[166:169], v[178:181], v[104:107]
	v_mfma_f32_16x16x32_bf16 v[100:103], v[144:147], v[186:189], v[100:103]
	v_mfma_f32_16x16x32_bf16 v[92:95], v[166:169], v[186:189], v[92:95]
	v_mfma_f32_16x16x32_bf16 v[84:87], v[144:147], v[194:197], v[84:87]
	v_mfma_f32_16x16x32_bf16 v[76:79], v[166:169], v[194:197], v[76:79]
	v_mfma_f32_16x16x32_bf16 v[68:71], v[144:147], v[202:205], v[68:71]
	v_mfma_f32_16x16x32_bf16 v[64:67], v[166:169], v[202:205], v[64:67]
	v_mfma_f32_16x16x32_bf16 v[108:111], v[148:151], v[182:185], v[108:111]
	v_mfma_f32_16x16x32_bf16 v[104:107], v[170:173], v[182:185], v[104:107]
	v_mfma_f32_16x16x32_bf16 v[100:103], v[148:151], v[190:193], v[100:103]
	v_mfma_f32_16x16x32_bf16 v[92:95], v[170:173], v[190:193], v[92:95]
	v_mfma_f32_16x16x32_bf16 v[84:87], v[148:151], v[198:201], v[84:87]
	v_mfma_f32_16x16x32_bf16 v[76:79], v[170:173], v[198:201], v[76:79]
	v_mfma_f32_16x16x32_bf16 v[68:71], v[148:151], v[206:209], v[68:71]
	v_mfma_f32_16x16x32_bf16 v[64:67], v[170:173], v[206:209], v[64:67]
	s_barrier
; #define PG8_LDA(dst, b, h) do { _Pragma("unroll") for (int m = 0; m < 4; ++m) _Pragma("unroll") for (int k = 0; k < 2; ++k) dst[m][k] = *(const PG8_LAS bf16x8*)(lds + PG8_SA(b, h) + aoff + m * 2048 + k * 1024); } while (0)
; #define PG8_LDB(dst, b, h) do { _Pragma("unroll") for (int n = 0; n < 2; ++n) _Pragma("unroll") for (int k = 0; k < 2; ++k) dst[n][k] = *(const PG8_LAS bf16x8*)(lds + PG8_SB(b, h) + boff + n * 2048 + k * 1024); } while (0)
; #define PG8_WAIT_V(n) asm volatile("s_waitcnt vmcnt(" #n ")" ::: "memory")
; #define PG8_WAIT_L(n) asm volatile("s_waitcnt lgkmcnt(" #n ")" ::: "memory")
; #define PG8_BAR __builtin_amdgcn_s_barrier()
; #define PG8_SCHED __builtin_amdgcn_sched_barrier(0)
; template <class Epi, class Sched, bool ALIGN_EPI = false, bool SP2 = false, bool F8 = false, bool I8 = false, bool PF = false>
; __device__ __forceinline__ void gemm_phase(PG8_LAS unsigned char* lds, const Gemm g, const Sched& S, const Epi& E, const int wave_) {
;     ...
;             if constexpr (SP2) {
;             PG8_LDB(B0, 0, 0); PG8_LDB(B1, 0, 1); PG8_SCHED; PG8_LDA(At, 0, 0); PG8_STAGE(PG8_SA(1, 1), a1 + hstep, voffA);
;             PG8_WAIT_V(8); PG8_WAIT_L(0); PG8_BAR; PG8_MMA(0, 0, At, B0); PG8_MMA(0, 1, At, B1); PG8_BAR; PG8_SCHED;
;             PG8_LDA(At, 0, 1); PG8_STAGE(PG8_SB(0, 0), b2, voffB); PG8_STAGE(PG8_SB(0, 1), b2 + hstep, voffB); PG8_STAGE(PG8_SA(0, 0), a2, voffA);
;             PG8_WAIT_V(8); PG8_WAIT_L(0); PG8_BAR; PG8_MMA(1, 0, At, B0); PG8_MMA(1, 1, At, B1); PG8_BAR; PG8_SCHED;
;             PG8_LDB(B0, 1, 0); PG8_LDB(B1, 1, 1); PG8_SCHED; PG8_LDA(At, 1, 0); PG8_STAGE(PG8_SA(0, 1), a2 + hstep, voffA);
;             PG8_WAIT_V(8); PG8_WAIT_L(0); PG8_BAR; PG8_MMA(0, 0, At, B0); PG8_MMA(0, 1, At, B1); PG8_BAR; PG8_SCHED;
;             PG8_LDA(At, 1, 1); PG8_STAGE(PG8_SB(1, 0), b3, voffB); PG8_STAGE(PG8_SB(1, 1), b3 + hstep, voffB); PG8_STAGE(PG8_SA(1, 0), a3, voffA);
;             PG8_WAIT_V(8); PG8_WAIT_L(0); PG8_BAR; PG8_MMA(1, 0, At, B0); PG8_MMA(1, 1, At, B1); PG8_BAR; PG8_SCHED;
	s_add_i32 s63, s49, s36
	v_lshl_add_u64 v[210:211], s[28:29], 0, v[156:157]
	s_mov_b32 m0, s63
	ds_read_b128 v[178:181], v177 offset:16384
	ds_read_b128 v[182:185], v177 offset:17408
	ds_read_b128 v[186:189], v177 offset:18432
	ds_read_b128 v[190:193], v177 offset:19456
	ds_read_b128 v[194:197], v177 offset:20480
	ds_read_b128 v[198:201], v177 offset:21504
	ds_read_b128 v[202:205], v177 offset:22528
	ds_read_b128 v[206:209], v177 offset:23552
	global_load_lds_dwordx4 v[210:211], off
	s_add_i32 m0, s63, 0x2000
	s_add_u32 s64, s28, 0x40000
	v_lshl_add_u64 v[212:213], s[28:29], 0, v[152:153]
	s_addc_u32 s65, s29, 0
	s_add_i32 s63, s50, s36
	global_load_lds_dwordx4 v[212:213], off
	v_lshl_add_u64 v[214:215], s[64:65], 0, v[156:157]
	s_mov_b32 m0, s63
	v_lshl_add_u64 v[216:217], s[30:31], 0, v[154:155]
	global_load_lds_dwordx4 v[214:215], off
	v_lshl_add_u64 v[214:215], s[64:65], 0, v[152:153]
	s_add_i32 m0, s63, 0x2000
	s_nop 0
	global_load_lds_dwordx4 v[214:215], off
	v_lshl_add_u64 v[214:215], s[30:31], 0, v[158:159]
	s_mov_b32 m0, s21
	s_nop 0
	global_load_lds_dwordx4 v[214:215], off
	s_mov_b32 m0, s37
	s_nop 0
	global_load_lds_dwordx4 v[216:217], off
	s_waitcnt vmcnt(8)
	s_waitcnt lgkmcnt(0)
	s_barrier
	s_waitcnt lgkmcnt(0)
	v_mfma_f32_16x16x32_bf16 v[60:63], v[128:131], v[178:181], v[60:63]
	v_mfma_f32_16x16x32_bf16 v[56:59], v[136:139], v[178:181], v[56:59]
	v_mfma_f32_16x16x32_bf16 v[48:51], v[128:131], v[186:189], v[48:51]
	v_mfma_f32_16x16x32_bf16 v[40:43], v[136:139], v[186:189], v[40:43]
	v_mfma_f32_16x16x32_bf16 v[32:35], v[128:131], v[194:197], v[32:35]
	v_mfma_f32_16x16x32_bf16 v[24:27], v[136:139], v[194:197], v[24:27]
	v_mfma_f32_16x16x32_bf16 v[16:19], v[128:131], v[202:205], v[16:19]
	v_mfma_f32_16x16x32_bf16 v[8:11], v[136:139], v[202:205], v[8:11]
	v_mfma_f32_16x16x32_bf16 v[60:63], v[132:135], v[182:185], v[60:63]
	v_mfma_f32_16x16x32_bf16 v[56:59], v[140:143], v[182:185], v[56:59]
	v_mfma_f32_16x16x32_bf16 v[48:51], v[132:135], v[190:193], v[48:51]
	v_mfma_f32_16x16x32_bf16 v[40:43], v[140:143], v[190:193], v[40:43]
	v_mfma_f32_16x16x32_bf16 v[32:35], v[132:135], v[198:201], v[32:35]
	v_mfma_f32_16x16x32_bf16 v[24:27], v[140:143], v[198:201], v[24:27]
	v_mfma_f32_16x16x32_bf16 v[16:19], v[132:135], v[206:209], v[16:19]
	v_mfma_f32_16x16x32_bf16 v[8:11], v[140:143], v[206:209], v[8:11]
	v_mfma_f32_16x16x32_bf16 v[52:55], v[144:147], v[178:181], v[52:55]
	v_mfma_f32_16x16x32_bf16 v[44:47], v[166:169], v[178:181], v[44:47]
	v_mfma_f32_16x16x32_bf16 v[36:39], v[144:147], v[186:189], v[36:39]
	v_mfma_f32_16x16x32_bf16 v[28:31], v[166:169], v[186:189], v[28:31]
	v_mfma_f32_16x16x32_bf16 v[20:23], v[144:147], v[194:197], v[20:23]
	v_mfma_f32_16x16x32_bf16 v[12:15], v[166:169], v[194:197], v[12:15]
	v_mfma_f32_16x16x32_bf16 v[4:7], v[144:147], v[202:205], v[4:7]
	v_mfma_f32_16x16x32_bf16 v[0:3], v[166:169], v[202:205], v[0:3]
	v_mfma_f32_16x16x32_bf16 v[52:55], v[148:151], v[182:185], v[52:55]
	v_mfma_f32_16x16x32_bf16 v[44:47], v[170:173], v[182:185], v[44:47]
	v_mfma_f32_16x16x32_bf16 v[36:39], v[148:151], v[190:193], v[36:39]
	v_mfma_f32_16x16x32_bf16 v[28:31], v[170:173], v[190:193], v[28:31]
	v_mfma_f32_16x16x32_bf16 v[20:23], v[148:151], v[198:201], v[20:23]
	v_mfma_f32_16x16x32_bf16 v[12:15], v[170:173], v[198:201], v[12:15]
	v_mfma_f32_16x16x32_bf16 v[4:7], v[148:151], v[206:209], v[4:7]
	v_mfma_f32_16x16x32_bf16 v[0:3], v[170:173], v[206:209], v[0:3]
	s_barrier
	s_add_i32 s63, 0, 0x18000
	s_add_i32 s64, 0, 0x1c000
	v_add_u32_e32 v140, s63, v174
	v_add_u32_e32 v170, s64, v174
	ds_read_b128 v[128:131], v140
	ds_read_b128 v[132:135], v140 offset:1024
	ds_read_b128 v[136:139], v140 offset:2048
	ds_read_b128 v[140:143], v140 offset:3072
	ds_read_b128 v[144:147], v170
	ds_read_b128 v[148:151], v170 offset:1024
	ds_read_b128 v[166:169], v170 offset:2048
	ds_read_b128 v[170:173], v170 offset:3072
	s_add_u32 s30, s30, 0x40000
	s_addc_u32 s31, s31, 0
	s_mov_b32 m0, s38
	v_lshl_add_u64 v[218:219], s[30:31], 0, v[158:159]
	ds_read_b128 v[178:181], v177 offset:32768
	ds_read_b128 v[182:185], v177 offset:33792
	ds_read_b128 v[186:189], v177 offset:34816
	ds_read_b128 v[190:193], v177 offset:35840
	ds_read_b128 v[194:197], v177 offset:36864
	ds_read_b128 v[198:201], v177 offset:37888
	ds_read_b128 v[202:205], v177 offset:38912
	ds_read_b128 v[206:209], v177 offset:39936
	global_load_lds_dwordx4 v[218:219], off
	v_lshl_add_u64 v[218:219], s[30:31], 0, v[154:155]
	s_mov_b32 m0, s39
	s_nop 0
	global_load_lds_dwordx4 v[218:219], off
	s_waitcnt vmcnt(8)
	s_waitcnt lgkmcnt(0)
	s_barrier
; #define PG8_LDA(dst, b, h) do { _Pragma("unroll") for (int m = 0; m < 4; ++m) _Pragma("unroll") for (int k = 0; k < 2; ++k) dst[m][k] = *(const PG8_LAS bf16x8*)(lds + PG8_SA(b, h) + aoff + m * 2048 + k * 1024); } while (0)
; #define PG8_LDB(dst, b, h) do { _Pragma("unroll") for (int n = 0; n < 2; ++n) _Pragma("unroll") for (int k = 0; k < 2; ++k) dst[n][k] = *(const PG8_LAS bf16x8*)(lds + PG8_SB(b, h) + boff + n * 2048 + k * 1024); } while (0)
; #define PG8_WAIT_V(n) asm volatile("s_waitcnt vmcnt(" #n ")" ::: "memory")
; #define PG8_WAIT_L(n) asm volatile("s_waitcnt lgkmcnt(" #n ")" ::: "memory")
; #define PG8_BAR __builtin_amdgcn_s_barrier()
; #define PG8_SCHED __builtin_amdgcn_sched_barrier(0)
; template <class Epi, class Sched, bool ALIGN_EPI = false, bool SP2 = false, bool F8 = false, bool I8 = false, bool PF = false>
; __device__ __forceinline__ void gemm_phase(PG8_LAS unsigned char* lds, const Gemm g, const Sched& S, const Epi& E, const int wave_) {
;     ...
;             if constexpr (SP2) {
;             PG8_LDB(B0, 0, 0); PG8_LDB(B1, 0, 1); PG8_SCHED; PG8_LDA(At, 0, 0); PG8_STAGE(PG8_SA(1, 1), a1 + hstep, voffA);
;             PG8_WAIT_V(8); PG8_WAIT_L(0); PG8_BAR; PG8_MMA(0, 0, At, B0); PG8_MMA(0, 1, At, B1); PG8_BAR; PG8_SCHED;
;             PG8_LDA(At, 0, 1); PG8_STAGE(PG8_SB(0, 0), b2, voffB); PG8_STAGE(PG8_SB(0, 1), b2 + hstep, voffB); PG8_STAGE(PG8_SA(0, 0), a2, voffA);
;             PG8_WAIT_V(8); PG8_WAIT_L(0); PG8_BAR; PG8_MMA(1, 0, At, B0); PG8_MMA(1, 1, At, B1); PG8_BAR; PG8_SCHED;
;             PG8_LDB(B0, 1, 0); PG8_LDB(B1, 1, 1); PG8_SCHED; PG8_LDA(At, 1, 0); PG8_STAGE(PG8_SA(0, 1), a2 + hstep, voffA);
;             PG8_WAIT_V(8); PG8_WAIT_L(0); PG8_BAR; PG8_MMA(0, 0, At, B0); PG8_MMA(0, 1, At, B1); PG8_BAR; PG8_SCHED;
;             PG8_LDA(At, 1, 1); PG8_STAGE(PG8_SB(1, 0), b3, voffB); PG8_STAGE(PG8_SB(1, 1), b3 + hstep, voffB); PG8_STAGE(PG8_SA(1, 0), a3, voffA);
;             PG8_WAIT_V(8); PG8_WAIT_L(0); PG8_BAR; PG8_MMA(1, 0, At, B0); PG8_MMA(1, 1, At, B1); PG8_BAR; PG8_SCHED;
	s_waitcnt lgkmcnt(0)
	v_mfma_f32_16x16x32_bf16 v[124:127], v[128:131], v[178:181], v[124:127]
	v_mfma_f32_16x16x32_bf16 v[120:123], v[136:139], v[178:181], v[120:123]
	v_mfma_f32_16x16x32_bf16 v[116:119], v[128:131], v[186:189], v[116:119]
	v_mfma_f32_16x16x32_bf16 v[112:115], v[136:139], v[186:189], v[112:115]
	v_mfma_f32_16x16x32_bf16 v[96:99], v[128:131], v[194:197], v[96:99]
	v_mfma_f32_16x16x32_bf16 v[88:91], v[136:139], v[194:197], v[88:91]
	v_mfma_f32_16x16x32_bf16 v[80:83], v[128:131], v[202:205], v[80:83]
	v_mfma_f32_16x16x32_bf16 v[72:75], v[136:139], v[202:205], v[72:75]
	v_mfma_f32_16x16x32_bf16 v[124:127], v[132:135], v[182:185], v[124:127]
	v_mfma_f32_16x16x32_bf16 v[120:123], v[140:143], v[182:185], v[120:123]
	v_mfma_f32_16x16x32_bf16 v[116:119], v[132:135], v[190:193], v[116:119]
	v_mfma_f32_16x16x32_bf16 v[112:115], v[140:143], v[190:193], v[112:115]
	v_mfma_f32_16x16x32_bf16 v[96:99], v[132:135], v[198:201], v[96:99]
	v_mfma_f32_16x16x32_bf16 v[88:91], v[140:143], v[198:201], v[88:91]
	v_mfma_f32_16x16x32_bf16 v[80:83], v[132:135], v[206:209], v[80:83]
	v_mfma_f32_16x16x32_bf16 v[72:75], v[140:143], v[206:209], v[72:75]
	v_mfma_f32_16x16x32_bf16 v[108:111], v[144:147], v[178:181], v[108:111]
	v_mfma_f32_16x16x32_bf16 v[104:107], v[166:169], v[178:181], v[104:107]
	v_mfma_f32_16x16x32_bf16 v[100:103], v[144:147], v[186:189], v[100:103]
	v_mfma_f32_16x16x32_bf16 v[92:95], v[166:169], v[186:189], v[92:95]
	v_mfma_f32_16x16x32_bf16 v[84:87], v[144:147], v[194:197], v[84:87]
	v_mfma_f32_16x16x32_bf16 v[76:79], v[166:169], v[194:197], v[76:79]
	v_mfma_f32_16x16x32_bf16 v[68:71], v[144:147], v[202:205], v[68:71]
	v_mfma_f32_16x16x32_bf16 v[64:67], v[166:169], v[202:205], v[64:67]
	v_mfma_f32_16x16x32_bf16 v[108:111], v[148:151], v[182:185], v[108:111]
	v_mfma_f32_16x16x32_bf16 v[104:107], v[170:173], v[182:185], v[104:107]
	v_mfma_f32_16x16x32_bf16 v[100:103], v[148:151], v[190:193], v[100:103]
	v_mfma_f32_16x16x32_bf16 v[92:95], v[170:173], v[190:193], v[92:95]
	v_mfma_f32_16x16x32_bf16 v[84:87], v[148:151], v[198:201], v[84:87]
	v_mfma_f32_16x16x32_bf16 v[76:79], v[170:173], v[198:201], v[76:79]
	v_mfma_f32_16x16x32_bf16 v[68:71], v[148:151], v[206:209], v[68:71]
	v_mfma_f32_16x16x32_bf16 v[64:67], v[170:173], v[206:209], v[64:67]
	s_barrier
	s_add_i32 s30, s63, s36
	v_lshl_add_u64 v[210:211], v[210:211], 0, s[6:7]
	s_mov_b32 m0, s30
	ds_read_b128 v[178:181], v177 offset:49152
	ds_read_b128 v[182:185], v177 offset:50176
	ds_read_b128 v[186:189], v177 offset:51200
	ds_read_b128 v[190:193], v177 offset:52224
	ds_read_b128 v[194:197], v177 offset:53248
	ds_read_b128 v[198:201], v177 offset:54272
	ds_read_b128 v[202:205], v177 offset:55296
	ds_read_b128 v[206:209], v177 offset:56320
	global_load_lds_dwordx4 v[210:211], off
	s_add_i32 m0, s30, 0x2000
	s_add_u32 s28, s28, 0x40080
	v_lshl_add_u64 v[210:211], v[212:213], 0, s[6:7]
	s_addc_u32 s29, s29, 0
	s_add_i32 s30, s64, s36
	global_load_lds_dwordx4 v[210:211], off
	v_lshl_add_u64 v[210:211], s[28:29], 0, v[156:157]
	s_mov_b32 m0, s30
	s_nop 0
	global_load_lds_dwordx4 v[210:211], off
	v_lshl_add_u64 v[210:211], s[28:29], 0, v[152:153]
	s_add_i32 m0, s30, 0x2000
	s_nop 0
	global_load_lds_dwordx4 v[210:211], off
	v_lshl_add_u64 v[210:211], v[214:215], 0, s[6:7]
	s_mov_b32 m0, s46
	s_nop 0
	global_load_lds_dwordx4 v[210:211], off
	v_lshl_add_u64 v[210:211], v[216:217], 0, s[6:7]
	s_mov_b32 m0, s47
	s_nop 0
	global_load_lds_dwordx4 v[210:211], off
	s_waitcnt vmcnt(8)
	s_waitcnt lgkmcnt(0)
	s_barrier
	s_waitcnt lgkmcnt(0)
	v_mfma_f32_16x16x32_bf16 v[60:63], v[128:131], v[178:181], v[60:63]
	v_mfma_f32_16x16x32_bf16 v[56:59], v[136:139], v[178:181], v[56:59]
	v_mfma_f32_16x16x32_bf16 v[48:51], v[128:131], v[186:189], v[48:51]
	v_mfma_f32_16x16x32_bf16 v[40:43], v[136:139], v[186:189], v[40:43]
	v_mfma_f32_16x16x32_bf16 v[32:35], v[128:131], v[194:197], v[32:35]
	v_mfma_f32_16x16x32_bf16 v[24:27], v[136:139], v[194:197], v[24:27]
	v_mfma_f32_16x16x32_bf16 v[16:19], v[128:131], v[202:205], v[16:19]
	v_mfma_f32_16x16x32_bf16 v[8:11], v[136:139], v[202:205], v[8:11]
	v_mfma_f32_16x16x32_bf16 v[60:63], v[132:135], v[182:185], v[60:63]
	v_mfma_f32_16x16x32_bf16 v[56:59], v[140:143], v[182:185], v[56:59]
	v_mfma_f32_16x16x32_bf16 v[48:51], v[132:135], v[190:193], v[48:51]
	v_mfma_f32_16x16x32_bf16 v[40:43], v[140:143], v[190:193], v[40:43]
	v_mfma_f32_16x16x32_bf16 v[32:35], v[132:135], v[198:201], v[32:35]
	v_mfma_f32_16x16x32_bf16 v[24:27], v[140:143], v[198:201], v[24:27]
	v_mfma_f32_16x16x32_bf16 v[16:19], v[132:135], v[206:209], v[16:19]
	v_mfma_f32_16x16x32_bf16 v[8:11], v[140:143], v[206:209], v[8:11]
	v_mfma_f32_16x16x32_bf16 v[52:55], v[144:147], v[178:181], v[52:55]
	v_mfma_f32_16x16x32_bf16 v[44:47], v[166:169], v[178:181], v[44:47]
	v_mfma_f32_16x16x32_bf16 v[36:39], v[144:147], v[186:189], v[36:39]
	v_mfma_f32_16x16x32_bf16 v[28:31], v[166:169], v[186:189], v[28:31]
	v_mfma_f32_16x16x32_bf16 v[20:23], v[144:147], v[194:197], v[20:23]
	v_mfma_f32_16x16x32_bf16 v[12:15], v[166:169], v[194:197], v[12:15]
	v_mfma_f32_16x16x32_bf16 v[4:7], v[144:147], v[202:205], v[4:7]
	v_mfma_f32_16x16x32_bf16 v[0:3], v[166:169], v[202:205], v[0:3]
	v_mfma_f32_16x16x32_bf16 v[52:55], v[148:151], v[182:185], v[52:55]
	v_mfma_f32_16x16x32_bf16 v[44:47], v[170:173], v[182:185], v[44:47]
	v_mfma_f32_16x16x32_bf16 v[36:39], v[148:151], v[190:193], v[36:39]
	v_mfma_f32_16x16x32_bf16 v[28:31], v[170:173], v[190:193], v[28:31]
	v_mfma_f32_16x16x32_bf16 v[20:23], v[148:151], v[198:201], v[20:23]
	v_mfma_f32_16x16x32_bf16 v[12:15], v[170:173], v[198:201], v[12:15]
	v_mfma_f32_16x16x32_bf16 v[4:7], v[148:151], v[206:209], v[4:7]
	v_mfma_f32_16x16x32_bf16 v[0:3], v[170:173], v[206:209], v[0:3]
	s_add_i32 s62, s62, 2
	s_add_u32 s22, s22, 0x100
	s_addc_u32 s23, s23, 0
	s_add_u32 s54, s54, 0x100
	s_addc_u32 s55, s55, 0
	s_cmp_gt_u32 s62, 13
	s_barrier
	s_cbranch_scc0 .LBB0_453
	s_and_b64 vcc, exec, s[8:9]
	s_cbranch_vccz .LBB0_456
	s_barrier

; #define PG8_LDA(dst, b, h) do { _Pragma("unroll") for (int m = 0; m < 4; ++m) _Pragma("unroll") for (int k = 0; k < 2; ++k) dst[m][k] = *(const PG8_LAS bf16x8*)(lds + PG8_SA(b, h) + aoff + m * 2048 + k * 1024); } while (0)
; #define PG8_LDB(dst, b, h) do { _Pragma("unroll") for (int n = 0; n < 2; ++n) _Pragma("unroll") for (int k = 0; k < 2; ++k) dst[n][k] = *(const PG8_LAS bf16x8*)(lds + PG8_SB(b, h) + boff + n * 2048 + k * 1024); } while (0)
; #define PG8_WAIT_V(n) asm volatile("s_waitcnt vmcnt(" #n ")" ::: "memory")
; #define PG8_WAIT_L(n) asm volatile("s_waitcnt lgkmcnt(" #n ")" ::: "memory")
; #define PG8_BAR __builtin_amdgcn_s_barrier()
; #define PG8_SCHED __builtin_amdgcn_sched_barrier(0)
; template <class Epi, class Sched, bool ALIGN_EPI = false, bool SP2 = false, bool F8 = false, bool I8 = false, bool PF = false>
; __device__ __forceinline__ void gemm_phase(PG8_LAS unsigned char* lds, const Gemm g, const Sched& S, const Epi& E, const int wave_) {
;     ...
;             if constexpr (SP2) {
;             PG8_LDB(B0, 0, 0); PG8_LDB(B1, 0, 1); PG8_SCHED; PG8_LDA(At, 0, 0); PG8_STAGE(PG8_SA(1, 1), a1 + hstep, voffA);
;             PG8_WAIT_V(8); PG8_WAIT_L(0); PG8_BAR; PG8_MMA(0, 0, At, B0); PG8_MMA(0, 1, At, B1); PG8_BAR; PG8_SCHED;
;     ...
;         for (int a = 0; a < 2; ++a)
; #pragma unroll
;             for (int b = 0; b < 2; ++b)
; #pragma unroll
;                 for (int m = 0; m < 4; ++m)
; #pragma unroll
;                     for (int n = 0; n < 2; ++n) acc[a][b][m][n] = (f32x4){0.f, 0.f, 0.f, 0.f};
.LBB0_590:
	s_ashr_i32 s19, s18, 31
	s_lshl_b64 s[22:23], s[18:19], 18
	s_add_u32 s22, s58, s22
	s_addc_u32 s23, s59, s23
	s_and_b64 s[26:27], s[20:21], exec
	s_cselect_b32 s19, s23, s31
	s_cselect_b32 s56, s22, s30
	s_ashr_i32 s17, s16, 31
	s_lshl_b64 s[26:27], s[16:17], 18
	s_add_u32 s26, s15, s26
	s_addc_u32 s27, s38, s27
	s_and_b64 s[36:37], s[20:21], exec
	s_cselect_b32 s17, s27, s35
	s_cselect_b32 s57, s26, s34
	s_add_u32 s30, s30, 0x20080
	s_addc_u32 s31, s31, 0
	s_add_u32 s62, s34, 0x100
	v_mov_b32_e32 v0, 0
	s_addc_u32 s63, s35, 0
	s_mov_b32 s64, -2
	v_mov_b32_e32 v1, v0
	v_mov_b32_e32 v2, v0
	v_mov_b32_e32 v3, v0
	v_mov_b32_e32 v4, v0
	v_mov_b32_e32 v5, v0
	v_mov_b32_e32 v6, v0
	v_mov_b32_e32 v7, v0
	s_waitcnt vmcnt(0)
	v_pk_mov_b32 v[16:17], 0, 0
	v_pk_mov_b32 v[18:19], 0, 0
	v_pk_mov_b32 v[20:21], 0, 0
	v_pk_mov_b32 v[22:23], 0, 0
	v_pk_mov_b32 v[32:33], 0, 0
	v_pk_mov_b32 v[34:35], 0, 0
	v_pk_mov_b32 v[36:37], 0, 0
	v_pk_mov_b32 v[38:39], 0, 0
	v_pk_mov_b32 v[48:49], 0, 0
	v_pk_mov_b32 v[50:51], 0, 0
	v_pk_mov_b32 v[52:53], 0, 0
	v_pk_mov_b32 v[54:55], 0, 0
	v_pk_mov_b32 v[8:9], 0, 0
	v_pk_mov_b32 v[10:11], 0, 0
	v_pk_mov_b32 v[12:13], 0, 0
	v_pk_mov_b32 v[14:15], 0, 0
	v_pk_mov_b32 v[24:25], 0, 0
	v_pk_mov_b32 v[26:27], 0, 0
	v_pk_mov_b32 v[28:29], 0, 0
	v_pk_mov_b32 v[30:31], 0, 0
	v_pk_mov_b32 v[40:41], 0, 0
	v_pk_mov_b32 v[42:43], 0, 0
	v_pk_mov_b32 v[44:45], 0, 0
	v_pk_mov_b32 v[46:47], 0, 0
	v_pk_mov_b32 v[56:57], 0, 0
	v_pk_mov_b32 v[58:59], 0, 0
	v_pk_mov_b32 v[60:61], 0, 0
	v_pk_mov_b32 v[62:63], 0, 0
	v_pk_mov_b32 v[64:65], 0, 0
	v_pk_mov_b32 v[66:67], 0, 0
	v_pk_mov_b32 v[68:69], 0, 0
	v_pk_mov_b32 v[70:71], 0, 0
	v_pk_mov_b32 v[80:81], 0, 0
	v_pk_mov_b32 v[82:83], 0, 0
	v_pk_mov_b32 v[84:85], 0, 0
	v_pk_mov_b32 v[86:87], 0, 0
	v_pk_mov_b32 v[96:97], 0, 0
	v_pk_mov_b32 v[98:99], 0, 0
	v_pk_mov_b32 v[100:101], 0, 0
	v_pk_mov_b32 v[102:103], 0, 0
	v_pk_mov_b32 v[112:113], 0, 0
	v_pk_mov_b32 v[114:115], 0, 0
	v_pk_mov_b32 v[116:117], 0, 0
	v_pk_mov_b32 v[118:119], 0, 0
	v_pk_mov_b32 v[72:73], 0, 0
	v_pk_mov_b32 v[74:75], 0, 0
	v_pk_mov_b32 v[76:77], 0, 0
	v_pk_mov_b32 v[78:79], 0, 0
	v_pk_mov_b32 v[88:89], 0, 0
	v_pk_mov_b32 v[90:91], 0, 0
	v_pk_mov_b32 v[92:93], 0, 0
	v_pk_mov_b32 v[94:95], 0, 0
	v_pk_mov_b32 v[104:105], 0, 0
	v_pk_mov_b32 v[106:107], 0, 0
	v_pk_mov_b32 v[108:109], 0, 0
	v_pk_mov_b32 v[110:111], 0, 0
	v_pk_mov_b32 v[120:121], 0, 0
	v_pk_mov_b32 v[122:123], 0, 0
	v_pk_mov_b32 v[124:125], 0, 0
	v_pk_mov_b32 v[126:127], 0, 0
.LBB0_591:
	ds_read_b128 v[142:145], v153
	ds_read_b128 v[146:149], v153 offset:1024
	ds_read_b128 v[158:161], v153 offset:2048
	ds_read_b128 v[162:165], v153 offset:3072
	ds_read_b128 v[166:169], v154
	ds_read_b128 v[170:173], v154 offset:1024
	ds_read_b128 v[174:177], v154 offset:2048
	ds_read_b128 v[178:181], v154 offset:3072
	s_add_u32 s34, s30, 0xfffe0080
	s_addc_u32 s35, s31, -1
	s_cmp_eq_u32 s64, 4
	s_cselect_b32 s37, s19, s35
	s_cselect_b32 s36, s56, s34
	s_cselect_b32 s35, s17, s63
	s_cselect_b32 s34, s57, s62
	v_lshl_add_u64 v[150:151], s[30:31], 0, v[136:137]
	s_add_i32 m0, s29, 0xc000
	ds_read_b128 v[182:185], v155
	ds_read_b128 v[186:189], v155 offset:1024
	ds_read_b128 v[190:193], v155 offset:2048
	ds_read_b128 v[194:197], v155 offset:3072
	ds_read_b128 v[198:201], v155 offset:4096
	ds_read_b128 v[202:205], v155 offset:5120
	ds_read_b128 v[206:209], v155 offset:6144
	ds_read_b128 v[210:213], v155 offset:7168
	global_load_lds_dwordx4 v[150:151], off
	v_lshl_add_u64 v[150:151], s[30:31], 0, v[138:139]
	s_add_i32 m0, s29, 0xe000
	s_nop 0
	global_load_lds_dwordx4 v[150:151], off
	s_waitcnt vmcnt(8)
	s_waitcnt lgkmcnt(0)
	s_barrier
	s_waitcnt lgkmcnt(0)
	v_mfma_i32_16x16x64_i8 v[124:127], v[142:145], v[182:185], v[124:127]
	v_mfma_i32_16x16x64_i8 v[120:123], v[158:161], v[182:185], v[120:123]
	v_mfma_i32_16x16x64_i8 v[108:111], v[142:145], v[190:193], v[108:111]
	v_mfma_i32_16x16x64_i8 v[104:107], v[158:161], v[190:193], v[104:107]
	v_mfma_i32_16x16x64_i8 v[92:95], v[142:145], v[198:201], v[92:95]
	v_mfma_i32_16x16x64_i8 v[88:91], v[158:161], v[198:201], v[88:91]
	v_mfma_i32_16x16x64_i8 v[76:79], v[142:145], v[206:209], v[76:79]
	v_mfma_i32_16x16x64_i8 v[72:75], v[158:161], v[206:209], v[72:75]
	v_mfma_i32_16x16x64_i8 v[124:127], v[146:149], v[186:189], v[124:127]
	v_mfma_i32_16x16x64_i8 v[120:123], v[162:165], v[186:189], v[120:123]
	v_mfma_i32_16x16x64_i8 v[108:111], v[146:149], v[194:197], v[108:111]
	v_mfma_i32_16x16x64_i8 v[104:107], v[162:165], v[194:197], v[104:107]
	v_mfma_i32_16x16x64_i8 v[92:95], v[146:149], v[202:205], v[92:95]
	v_mfma_i32_16x16x64_i8 v[88:91], v[162:165], v[202:205], v[88:91]
	v_mfma_i32_16x16x64_i8 v[76:79], v[146:149], v[210:213], v[76:79]
	v_mfma_i32_16x16x64_i8 v[72:75], v[162:165], v[210:213], v[72:75]
	v_mfma_i32_16x16x64_i8 v[116:119], v[166:169], v[182:185], v[116:119]
	v_mfma_i32_16x16x64_i8 v[112:115], v[174:177], v[182:185], v[112:115]
	v_mfma_i32_16x16x64_i8 v[100:103], v[166:169], v[190:193], v[100:103]
	v_mfma_i32_16x16x64_i8 v[96:99], v[174:177], v[190:193], v[96:99]
	v_mfma_i32_16x16x64_i8 v[84:87], v[166:169], v[198:201], v[84:87]
	v_mfma_i32_16x16x64_i8 v[80:83], v[174:177], v[198:201], v[80:83]
	v_mfma_i32_16x16x64_i8 v[68:71], v[166:169], v[206:209], v[68:71]
	v_mfma_i32_16x16x64_i8 v[64:67], v[174:177], v[206:209], v[64:67]
	v_mfma_i32_16x16x64_i8 v[116:119], v[170:173], v[186:189], v[116:119]
	v_mfma_i32_16x16x64_i8 v[112:115], v[178:181], v[186:189], v[112:115]
	v_mfma_i32_16x16x64_i8 v[100:103], v[170:173], v[194:197], v[100:103]
	v_mfma_i32_16x16x64_i8 v[96:99], v[178:181], v[194:197], v[96:99]
	v_mfma_i32_16x16x64_i8 v[84:87], v[170:173], v[202:205], v[84:87]
	v_mfma_i32_16x16x64_i8 v[80:83], v[178:181], v[202:205], v[80:83]
	v_mfma_i32_16x16x64_i8 v[68:71], v[170:173], v[210:213], v[68:71]
	v_mfma_i32_16x16x64_i8 v[64:67], v[178:181], v[210:213], v[64:67]
	s_barrier
; #define PG8_LDA(dst, b, h) do { _Pragma("unroll") for (int m = 0; m < 4; ++m) _Pragma("unroll") for (int k = 0; k < 2; ++k) dst[m][k] = *(const PG8_LAS bf16x8*)(lds + PG8_SA(b, h) + aoff + m * 2048 + k * 1024); } while (0)
; #define PG8_LDB(dst, b, h) do { _Pragma("unroll") for (int n = 0; n < 2; ++n) _Pragma("unroll") for (int k = 0; k < 2; ++k) dst[n][k] = *(const PG8_LAS bf16x8*)(lds + PG8_SB(b, h) + boff + n * 2048 + k * 1024); } while (0)
; #define PG8_WAIT_V(n) asm volatile("s_waitcnt vmcnt(" #n ")" ::: "memory")
; #define PG8_WAIT_L(n) asm volatile("s_waitcnt lgkmcnt(" #n ")" ::: "memory")
; #define PG8_BAR __builtin_amdgcn_s_barrier()
; #define PG8_SCHED __builtin_amdgcn_sched_barrier(0)
; template <class Epi, class Sched, bool ALIGN_EPI = false, bool SP2 = false, bool F8 = false, bool I8 = false, bool PF = false>
; __device__ __forceinline__ void gemm_phase(PG8_LAS unsigned char* lds, const Gemm g, const Sched& S, const Epi& E, const int wave_) {
;     ...
;             if constexpr (SP2) {
;             PG8_LDB(B0, 0, 0); PG8_LDB(B1, 0, 1); PG8_SCHED; PG8_LDA(At, 0, 0); PG8_STAGE(PG8_SA(1, 1), a1 + hstep, voffA);
;             PG8_WAIT_V(8); PG8_WAIT_L(0); PG8_BAR; PG8_MMA(0, 0, At, B0); PG8_MMA(0, 1, At, B1); PG8_BAR; PG8_SCHED;
;             PG8_LDA(At, 0, 1); PG8_STAGE(PG8_SB(0, 0), b2, voffB); PG8_STAGE(PG8_SB(0, 1), b2 + hstep, voffB); PG8_STAGE(PG8_SA(0, 0), a2, voffA);
;             PG8_WAIT_V(8); PG8_WAIT_L(0); PG8_BAR; PG8_MMA(1, 0, At, B0); PG8_MMA(1, 1, At, B1); PG8_BAR; PG8_SCHED;
;             PG8_LDB(B0, 1, 0); PG8_LDB(B1, 1, 1); PG8_SCHED; PG8_LDA(At, 1, 0); PG8_STAGE(PG8_SA(0, 1), a2 + hstep, voffA);
;             PG8_WAIT_V(8); PG8_WAIT_L(0); PG8_BAR; PG8_MMA(0, 0, At, B0); PG8_MMA(0, 1, At, B1); PG8_BAR; PG8_SCHED;
;             PG8_LDA(At, 1, 1); PG8_STAGE(PG8_SB(1, 0), b3, voffB); PG8_STAGE(PG8_SB(1, 1), b3 + hstep, voffB); PG8_STAGE(PG8_SA(1, 0), a3, voffA);
;             PG8_WAIT_V(8); PG8_WAIT_L(0); PG8_BAR; PG8_MMA(1, 0, At, B0); PG8_MMA(1, 1, At, B1); PG8_BAR; PG8_SCHED;
	s_add_i32 s65, s51, s39
	v_lshl_add_u64 v[150:151], s[34:35], 0, v[132:133]
	s_mov_b32 m0, s65
	ds_read_b128 v[182:185], v155 offset:16384
	ds_read_b128 v[186:189], v155 offset:17408
	ds_read_b128 v[190:193], v155 offset:18432
	ds_read_b128 v[194:197], v155 offset:19456
	ds_read_b128 v[198:201], v155 offset:20480
	ds_read_b128 v[202:205], v155 offset:21504
	ds_read_b128 v[206:209], v155 offset:22528
	ds_read_b128 v[210:213], v155 offset:23552
	global_load_lds_dwordx4 v[150:151], off
	s_add_i32 m0, s65, 0x2000
	s_add_u32 s66, s34, 0x20000
	v_lshl_add_u64 v[214:215], s[34:35], 0, v[128:129]
	s_addc_u32 s67, s35, 0
	s_add_i32 s65, s52, s39
	global_load_lds_dwordx4 v[214:215], off
	v_lshl_add_u64 v[216:217], s[66:67], 0, v[132:133]
	s_mov_b32 m0, s65
	v_lshl_add_u64 v[218:219], s[36:37], 0, v[130:131]
	global_load_lds_dwordx4 v[216:217], off
	v_lshl_add_u64 v[216:217], s[66:67], 0, v[128:129]
	s_add_i32 m0, s65, 0x2000
	s_nop 0
	global_load_lds_dwordx4 v[216:217], off
	v_lshl_add_u64 v[216:217], s[36:37], 0, v[134:135]
	s_mov_b32 m0, s29
	s_nop 0
	global_load_lds_dwordx4 v[216:217], off
	s_mov_b32 m0, s41
	s_nop 0
	global_load_lds_dwordx4 v[218:219], off
	s_waitcnt vmcnt(8)
	s_waitcnt lgkmcnt(0)
	s_barrier
	s_waitcnt lgkmcnt(0)
	v_mfma_i32_16x16x64_i8 v[60:63], v[142:145], v[182:185], v[60:63]
	v_mfma_i32_16x16x64_i8 v[56:59], v[158:161], v[182:185], v[56:59]
	v_mfma_i32_16x16x64_i8 v[44:47], v[142:145], v[190:193], v[44:47]
	v_mfma_i32_16x16x64_i8 v[40:43], v[158:161], v[190:193], v[40:43]
	v_mfma_i32_16x16x64_i8 v[28:31], v[142:145], v[198:201], v[28:31]
	v_mfma_i32_16x16x64_i8 v[24:27], v[158:161], v[198:201], v[24:27]
	v_mfma_i32_16x16x64_i8 v[12:15], v[142:145], v[206:209], v[12:15]
	v_mfma_i32_16x16x64_i8 v[8:11], v[158:161], v[206:209], v[8:11]
	v_mfma_i32_16x16x64_i8 v[60:63], v[146:149], v[186:189], v[60:63]
	v_mfma_i32_16x16x64_i8 v[56:59], v[162:165], v[186:189], v[56:59]
	v_mfma_i32_16x16x64_i8 v[44:47], v[146:149], v[194:197], v[44:47]
	v_mfma_i32_16x16x64_i8 v[40:43], v[162:165], v[194:197], v[40:43]
	v_mfma_i32_16x16x64_i8 v[28:31], v[146:149], v[202:205], v[28:31]
	v_mfma_i32_16x16x64_i8 v[24:27], v[162:165], v[202:205], v[24:27]
	v_mfma_i32_16x16x64_i8 v[12:15], v[146:149], v[210:213], v[12:15]
	v_mfma_i32_16x16x64_i8 v[8:11], v[162:165], v[210:213], v[8:11]
	v_mfma_i32_16x16x64_i8 v[52:55], v[166:169], v[182:185], v[52:55]
	v_mfma_i32_16x16x64_i8 v[48:51], v[174:177], v[182:185], v[48:51]
	v_mfma_i32_16x16x64_i8 v[36:39], v[166:169], v[190:193], v[36:39]
	v_mfma_i32_16x16x64_i8 v[32:35], v[174:177], v[190:193], v[32:35]
	v_mfma_i32_16x16x64_i8 v[20:23], v[166:169], v[198:201], v[20:23]
	v_mfma_i32_16x16x64_i8 v[16:19], v[174:177], v[198:201], v[16:19]
	v_mfma_i32_16x16x64_i8 v[4:7], v[166:169], v[206:209], v[4:7]
	v_mfma_i32_16x16x64_i8 v[0:3], v[174:177], v[206:209], v[0:3]
	v_mfma_i32_16x16x64_i8 v[52:55], v[170:173], v[186:189], v[52:55]
	v_mfma_i32_16x16x64_i8 v[48:51], v[178:181], v[186:189], v[48:51]
	v_mfma_i32_16x16x64_i8 v[36:39], v[170:173], v[194:197], v[36:39]
	v_mfma_i32_16x16x64_i8 v[32:35], v[178:181], v[194:197], v[32:35]
	v_mfma_i32_16x16x64_i8 v[20:23], v[170:173], v[202:205], v[20:23]
	v_mfma_i32_16x16x64_i8 v[16:19], v[178:181], v[202:205], v[16:19]
	v_mfma_i32_16x16x64_i8 v[4:7], v[170:173], v[210:213], v[4:7]
	v_mfma_i32_16x16x64_i8 v[0:3], v[178:181], v[210:213], v[0:3]
	s_barrier
	s_add_i32 s65, 0, 0x18000
	v_add_u32_e32 v157, s65, v152
	s_add_i32 s66, 0, 0x1c000
	ds_read_b128 v[142:145], v157
	ds_read_b128 v[146:149], v157 offset:1024
	ds_read_b128 v[158:161], v157 offset:2048
	ds_read_b128 v[162:165], v157 offset:3072
	v_add_u32_e32 v157, s66, v152
	ds_read_b128 v[166:169], v157
	ds_read_b128 v[170:173], v157 offset:1024
	ds_read_b128 v[174:177], v157 offset:2048
	ds_read_b128 v[178:181], v157 offset:3072
	s_add_u32 s36, s36, 0x20000
	s_addc_u32 s37, s37, 0
	s_mov_b32 m0, s42
	v_lshl_add_u64 v[220:221], s[36:37], 0, v[134:135]
	ds_read_b128 v[182:185], v155 offset:32768
	ds_read_b128 v[186:189], v155 offset:33792
	ds_read_b128 v[190:193], v155 offset:34816
	ds_read_b128 v[194:197], v155 offset:35840
	ds_read_b128 v[198:201], v155 offset:36864
	ds_read_b128 v[202:205], v155 offset:37888
	ds_read_b128 v[206:209], v155 offset:38912
	ds_read_b128 v[210:213], v155 offset:39936
	global_load_lds_dwordx4 v[220:221], off
	v_lshl_add_u64 v[220:221], s[36:37], 0, v[130:131]
	s_mov_b32 m0, s43
	s_nop 0
	global_load_lds_dwordx4 v[220:221], off
	s_waitcnt vmcnt(8)
	s_waitcnt lgkmcnt(0)
	s_barrier
; #define PG8_LDA(dst, b, h) do { _Pragma("unroll") for (int m = 0; m < 4; ++m) _Pragma("unroll") for (int k = 0; k < 2; ++k) dst[m][k] = *(const PG8_LAS bf16x8*)(lds + PG8_SA(b, h) + aoff + m * 2048 + k * 1024); } while (0)
; #define PG8_LDB(dst, b, h) do { _Pragma("unroll") for (int n = 0; n < 2; ++n) _Pragma("unroll") for (int k = 0; k < 2; ++k) dst[n][k] = *(const PG8_LAS bf16x8*)(lds + PG8_SB(b, h) + boff + n * 2048 + k * 1024); } while (0)
; #define PG8_WAIT_V(n) asm volatile("s_waitcnt vmcnt(" #n ")" ::: "memory")
; #define PG8_WAIT_L(n) asm volatile("s_waitcnt lgkmcnt(" #n ")" ::: "memory")
; #define PG8_BAR __builtin_amdgcn_s_barrier()
; #define PG8_SCHED __builtin_amdgcn_sched_barrier(0)
; template <class Epi, class Sched, bool ALIGN_EPI = false, bool SP2 = false, bool F8 = false, bool I8 = false, bool PF = false>
; __device__ __forceinline__ void gemm_phase(PG8_LAS unsigned char* lds, const Gemm g, const Sched& S, const Epi& E, const int wave_) {
;     ...
;             if constexpr (SP2) {
;             PG8_LDB(B0, 0, 0); PG8_LDB(B1, 0, 1); PG8_SCHED; PG8_LDA(At, 0, 0); PG8_STAGE(PG8_SA(1, 1), a1 + hstep, voffA);
;             PG8_WAIT_V(8); PG8_WAIT_L(0); PG8_BAR; PG8_MMA(0, 0, At, B0); PG8_MMA(0, 1, At, B1); PG8_BAR; PG8_SCHED;
;             PG8_LDA(At, 0, 1); PG8_STAGE(PG8_SB(0, 0), b2, voffB); PG8_STAGE(PG8_SB(0, 1), b2 + hstep, voffB); PG8_STAGE(PG8_SA(0, 0), a2, voffA);
;             PG8_WAIT_V(8); PG8_WAIT_L(0); PG8_BAR; PG8_MMA(1, 0, At, B0); PG8_MMA(1, 1, At, B1); PG8_BAR; PG8_SCHED;
;             PG8_LDB(B0, 1, 0); PG8_LDB(B1, 1, 1); PG8_SCHED; PG8_LDA(At, 1, 0); PG8_STAGE(PG8_SA(0, 1), a2 + hstep, voffA);
;             PG8_WAIT_V(8); PG8_WAIT_L(0); PG8_BAR; PG8_MMA(0, 0, At, B0); PG8_MMA(0, 1, At, B1); PG8_BAR; PG8_SCHED;
;             PG8_LDA(At, 1, 1); PG8_STAGE(PG8_SB(1, 0), b3, voffB); PG8_STAGE(PG8_SB(1, 1), b3 + hstep, voffB); PG8_STAGE(PG8_SA(1, 0), a3, voffA);
;             PG8_WAIT_V(8); PG8_WAIT_L(0); PG8_BAR; PG8_MMA(1, 0, At, B0); PG8_MMA(1, 1, At, B1); PG8_BAR; PG8_SCHED;
	s_waitcnt lgkmcnt(0)
	v_mfma_i32_16x16x64_i8 v[124:127], v[142:145], v[182:185], v[124:127]
	v_mfma_i32_16x16x64_i8 v[120:123], v[158:161], v[182:185], v[120:123]
	v_mfma_i32_16x16x64_i8 v[108:111], v[142:145], v[190:193], v[108:111]
	v_mfma_i32_16x16x64_i8 v[104:107], v[158:161], v[190:193], v[104:107]
	v_mfma_i32_16x16x64_i8 v[92:95], v[142:145], v[198:201], v[92:95]
	v_mfma_i32_16x16x64_i8 v[88:91], v[158:161], v[198:201], v[88:91]
	v_mfma_i32_16x16x64_i8 v[76:79], v[142:145], v[206:209], v[76:79]
	v_mfma_i32_16x16x64_i8 v[72:75], v[158:161], v[206:209], v[72:75]
	v_mfma_i32_16x16x64_i8 v[124:127], v[146:149], v[186:189], v[124:127]
	v_mfma_i32_16x16x64_i8 v[120:123], v[162:165], v[186:189], v[120:123]
	v_mfma_i32_16x16x64_i8 v[108:111], v[146:149], v[194:197], v[108:111]
	v_mfma_i32_16x16x64_i8 v[104:107], v[162:165], v[194:197], v[104:107]
	v_mfma_i32_16x16x64_i8 v[92:95], v[146:149], v[202:205], v[92:95]
	v_mfma_i32_16x16x64_i8 v[88:91], v[162:165], v[202:205], v[88:91]
	v_mfma_i32_16x16x64_i8 v[76:79], v[146:149], v[210:213], v[76:79]
	v_mfma_i32_16x16x64_i8 v[72:75], v[162:165], v[210:213], v[72:75]
	v_mfma_i32_16x16x64_i8 v[116:119], v[166:169], v[182:185], v[116:119]
	v_mfma_i32_16x16x64_i8 v[112:115], v[174:177], v[182:185], v[112:115]
	v_mfma_i32_16x16x64_i8 v[100:103], v[166:169], v[190:193], v[100:103]
	v_mfma_i32_16x16x64_i8 v[96:99], v[174:177], v[190:193], v[96:99]
	v_mfma_i32_16x16x64_i8 v[84:87], v[166:169], v[198:201], v[84:87]
	v_mfma_i32_16x16x64_i8 v[80:83], v[174:177], v[198:201], v[80:83]
	v_mfma_i32_16x16x64_i8 v[68:71], v[166:169], v[206:209], v[68:71]
	v_mfma_i32_16x16x64_i8 v[64:67], v[174:177], v[206:209], v[64:67]
	v_mfma_i32_16x16x64_i8 v[116:119], v[170:173], v[186:189], v[116:119]
	v_mfma_i32_16x16x64_i8 v[112:115], v[178:181], v[186:189], v[112:115]
	v_mfma_i32_16x16x64_i8 v[100:103], v[170:173], v[194:197], v[100:103]
	v_mfma_i32_16x16x64_i8 v[96:99], v[178:181], v[194:197], v[96:99]
	v_mfma_i32_16x16x64_i8 v[84:87], v[170:173], v[202:205], v[84:87]
	v_mfma_i32_16x16x64_i8 v[80:83], v[178:181], v[202:205], v[80:83]
	v_mfma_i32_16x16x64_i8 v[68:71], v[170:173], v[210:213], v[68:71]
	v_mfma_i32_16x16x64_i8 v[64:67], v[178:181], v[210:213], v[64:67]
	s_barrier
	s_add_i32 s36, s65, s39
	v_lshl_add_u64 v[150:151], v[150:151], 0, s[10:11]
	s_mov_b32 m0, s36
	ds_read_b128 v[182:185], v155 offset:49152
	ds_read_b128 v[186:189], v155 offset:50176
	ds_read_b128 v[190:193], v155 offset:51200
	ds_read_b128 v[194:197], v155 offset:52224
	ds_read_b128 v[198:201], v155 offset:53248
	ds_read_b128 v[202:205], v155 offset:54272
	ds_read_b128 v[206:209], v155 offset:55296
	ds_read_b128 v[210:213], v155 offset:56320
	global_load_lds_dwordx4 v[150:151], off
	s_add_i32 m0, s36, 0x2000
	s_add_u32 s34, s34, 0x20080
	v_lshl_add_u64 v[150:151], v[214:215], 0, s[10:11]
	s_addc_u32 s35, s35, 0
	s_add_i32 s36, s66, s39
	global_load_lds_dwordx4 v[150:151], off
	v_lshl_add_u64 v[150:151], s[34:35], 0, v[132:133]
	s_mov_b32 m0, s36
	s_nop 0
	global_load_lds_dwordx4 v[150:151], off
	v_lshl_add_u64 v[150:151], s[34:35], 0, v[128:129]
	s_add_i32 m0, s36, 0x2000
	s_nop 0
	global_load_lds_dwordx4 v[150:151], off
	v_lshl_add_u64 v[150:151], v[216:217], 0, s[10:11]
	s_mov_b32 m0, s48
	s_nop 0
	global_load_lds_dwordx4 v[150:151], off
	v_lshl_add_u64 v[150:151], v[218:219], 0, s[10:11]
	s_mov_b32 m0, s49
	s_nop 0
	global_load_lds_dwordx4 v[150:151], off
	s_waitcnt vmcnt(8)
	s_waitcnt lgkmcnt(0)
	s_barrier
	s_waitcnt lgkmcnt(0)
	v_mfma_i32_16x16x64_i8 v[60:63], v[142:145], v[182:185], v[60:63]
	v_mfma_i32_16x16x64_i8 v[56:59], v[158:161], v[182:185], v[56:59]
	v_mfma_i32_16x16x64_i8 v[44:47], v[142:145], v[190:193], v[44:47]
	v_mfma_i32_16x16x64_i8 v[40:43], v[158:161], v[190:193], v[40:43]
	v_mfma_i32_16x16x64_i8 v[28:31], v[142:145], v[198:201], v[28:31]
	v_mfma_i32_16x16x64_i8 v[24:27], v[158:161], v[198:201], v[24:27]
	v_mfma_i32_16x16x64_i8 v[12:15], v[142:145], v[206:209], v[12:15]
	v_mfma_i32_16x16x64_i8 v[8:11], v[158:161], v[206:209], v[8:11]
	v_mfma_i32_16x16x64_i8 v[60:63], v[146:149], v[186:189], v[60:63]
	v_mfma_i32_16x16x64_i8 v[56:59], v[162:165], v[186:189], v[56:59]
	v_mfma_i32_16x16x64_i8 v[44:47], v[146:149], v[194:197], v[44:47]
	v_mfma_i32_16x16x64_i8 v[40:43], v[162:165], v[194:197], v[40:43]
	v_mfma_i32_16x16x64_i8 v[28:31], v[146:149], v[202:205], v[28:31]
	v_mfma_i32_16x16x64_i8 v[24:27], v[162:165], v[202:205], v[24:27]
	v_mfma_i32_16x16x64_i8 v[12:15], v[146:149], v[210:213], v[12:15]
	v_mfma_i32_16x16x64_i8 v[8:11], v[162:165], v[210:213], v[8:11]
	v_mfma_i32_16x16x64_i8 v[52:55], v[166:169], v[182:185], v[52:55]
	v_mfma_i32_16x16x64_i8 v[48:51], v[174:177], v[182:185], v[48:51]
	v_mfma_i32_16x16x64_i8 v[36:39], v[166:169], v[190:193], v[36:39]
	v_mfma_i32_16x16x64_i8 v[32:35], v[174:177], v[190:193], v[32:35]
	v_mfma_i32_16x16x64_i8 v[20:23], v[166:169], v[198:201], v[20:23]
	v_mfma_i32_16x16x64_i8 v[16:19], v[174:177], v[198:201], v[16:19]
	v_mfma_i32_16x16x64_i8 v[4:7], v[166:169], v[206:209], v[4:7]
	v_mfma_i32_16x16x64_i8 v[0:3], v[174:177], v[206:209], v[0:3]
	v_mfma_i32_16x16x64_i8 v[52:55], v[170:173], v[186:189], v[52:55]
	v_mfma_i32_16x16x64_i8 v[48:51], v[178:181], v[186:189], v[48:51]
	v_mfma_i32_16x16x64_i8 v[36:39], v[170:173], v[194:197], v[36:39]
	v_mfma_i32_16x16x64_i8 v[32:35], v[178:181], v[194:197], v[32:35]
	v_mfma_i32_16x16x64_i8 v[20:23], v[170:173], v[202:205], v[20:23]
	v_mfma_i32_16x16x64_i8 v[16:19], v[178:181], v[202:205], v[16:19]
	v_mfma_i32_16x16x64_i8 v[4:7], v[170:173], v[210:213], v[4:7]
	v_mfma_i32_16x16x64_i8 v[0:3], v[178:181], v[210:213], v[0:3]
	s_add_i32 s64, s64, 2
	s_add_u32 s30, s30, 0x100
	s_addc_u32 s31, s31, 0
	s_add_u32 s62, s62, 0x100
	s_addc_u32 s63, s63, 0
	s_cmp_gt_u32 s64, 5
	s_barrier
	s_cbranch_scc0 .LBB0_591
	s_and_b64 vcc, exec, s[12:13]
	s_cbranch_vccz .LBB0_594
	s_barrier

; #define PG8_LDA(dst, b, h) do { _Pragma("unroll") for (int m = 0; m < 4; ++m) _Pragma("unroll") for (int k = 0; k < 2; ++k) dst[m][k] = *(const PG8_LAS bf16x8*)(lds + PG8_SA(b, h) + aoff + m * 2048 + k * 1024); } while (0)
; #define PG8_LDB(dst, b, h) do { _Pragma("unroll") for (int n = 0; n < 2; ++n) _Pragma("unroll") for (int k = 0; k < 2; ++k) dst[n][k] = *(const PG8_LAS bf16x8*)(lds + PG8_SB(b, h) + boff + n * 2048 + k * 1024); } while (0)
; #define PG8_WAIT_V(n) asm volatile("s_waitcnt vmcnt(" #n ")" ::: "memory")
; #define PG8_WAIT_L(n) asm volatile("s_waitcnt lgkmcnt(" #n ")" ::: "memory")
; #define PG8_BAR __builtin_amdgcn_s_barrier()
; #define PG8_SCHED __builtin_amdgcn_sched_barrier(0)
; template <class Epi, class Sched, bool ALIGN_EPI = false, bool SP2 = false, bool F8 = false, bool I8 = false, bool PF = false>
; __device__ __forceinline__ void gemm_phase(PG8_LAS unsigned char* lds, const Gemm g, const Sched& S, const Epi& E, const int wave_) {
;     ...
;             if constexpr (SP2) {
;             PG8_LDB(B0, 0, 0); PG8_LDB(B1, 0, 1); PG8_SCHED; PG8_LDA(At, 0, 0); PG8_STAGE(PG8_SA(1, 1), a1 + hstep, voffA);
;             PG8_WAIT_V(8); PG8_WAIT_L(0); PG8_BAR; PG8_MMA(0, 0, At, B0); PG8_MMA(0, 1, At, B1); PG8_BAR; PG8_SCHED;
;     ...
;         for (int a = 0; a < 2; ++a)
; #pragma unroll
;             for (int b = 0; b < 2; ++b)
; #pragma unroll
;                 for (int m = 0; m < 4; ++m)
; #pragma unroll
;                     for (int n = 0; n < 2; ++n) acc[a][b][m][n] = (f32x4){0.f, 0.f, 0.f, 0.f};
.LBB0_670:
	s_add_u32 s63, s28, 0x100
	v_mov_b32_e32 v32, 0
	s_addc_u32 s64, s29, 0
	s_mov_b32 s65, -2
	v_mov_b32_e32 v33, v32
	v_mov_b32_e32 v34, v32
	v_mov_b32_e32 v35, v32
	v_mov_b32_e32 v36, v32
	v_mov_b32_e32 v37, v32
	v_mov_b32_e32 v38, v32
	v_mov_b32_e32 v39, v32
	v_mov_b32_e32 v48, v32
	v_mov_b32_e32 v49, v32
	v_mov_b32_e32 v50, v32
	v_mov_b32_e32 v51, v32
	s_waitcnt vmcnt(0)
	v_pk_mov_b32 v[52:53], 0, 0
	v_pk_mov_b32 v[54:55], 0, 0
	v_pk_mov_b32 v[64:65], 0, 0
	v_pk_mov_b32 v[66:67], 0, 0
	v_pk_mov_b32 v[68:69], 0, 0
	v_pk_mov_b32 v[70:71], 0, 0
	v_pk_mov_b32 v[80:81], 0, 0
	v_pk_mov_b32 v[82:83], 0, 0
	v_pk_mov_b32 v[84:85], 0, 0
	v_pk_mov_b32 v[86:87], 0, 0
	v_pk_mov_b32 v[40:41], 0, 0
	v_pk_mov_b32 v[42:43], 0, 0
	v_pk_mov_b32 v[44:45], 0, 0
	v_pk_mov_b32 v[46:47], 0, 0
	v_pk_mov_b32 v[56:57], 0, 0
	v_pk_mov_b32 v[58:59], 0, 0
	v_pk_mov_b32 v[60:61], 0, 0
	v_pk_mov_b32 v[62:63], 0, 0
	v_pk_mov_b32 v[72:73], 0, 0
	v_pk_mov_b32 v[74:75], 0, 0
	v_pk_mov_b32 v[76:77], 0, 0
	v_pk_mov_b32 v[78:79], 0, 0
	v_pk_mov_b32 v[88:89], 0, 0
	v_pk_mov_b32 v[90:91], 0, 0
	v_pk_mov_b32 v[92:93], 0, 0
	v_pk_mov_b32 v[94:95], 0, 0
	v_pk_mov_b32 v[96:97], 0, 0
	v_pk_mov_b32 v[98:99], 0, 0
	v_pk_mov_b32 v[100:101], 0, 0
	v_pk_mov_b32 v[102:103], 0, 0
	v_pk_mov_b32 v[112:113], 0, 0
	v_pk_mov_b32 v[114:115], 0, 0
	v_pk_mov_b32 v[116:117], 0, 0
	v_pk_mov_b32 v[118:119], 0, 0
	v_pk_mov_b32 v[128:129], 0, 0
	v_pk_mov_b32 v[130:131], 0, 0
	v_pk_mov_b32 v[132:133], 0, 0
	v_pk_mov_b32 v[134:135], 0, 0
	v_pk_mov_b32 v[144:145], 0, 0
	v_pk_mov_b32 v[146:147], 0, 0
	v_pk_mov_b32 v[148:149], 0, 0
	v_pk_mov_b32 v[150:151], 0, 0
	v_pk_mov_b32 v[104:105], 0, 0
	v_pk_mov_b32 v[106:107], 0, 0
	v_pk_mov_b32 v[108:109], 0, 0
	v_pk_mov_b32 v[110:111], 0, 0
	v_pk_mov_b32 v[120:121], 0, 0
	v_pk_mov_b32 v[122:123], 0, 0
	v_pk_mov_b32 v[124:125], 0, 0
	v_pk_mov_b32 v[126:127], 0, 0
	v_pk_mov_b32 v[136:137], 0, 0
	v_pk_mov_b32 v[138:139], 0, 0
	v_pk_mov_b32 v[140:141], 0, 0
	v_pk_mov_b32 v[142:143], 0, 0
	v_pk_mov_b32 v[152:153], 0, 0
	v_pk_mov_b32 v[154:155], 0, 0
	v_pk_mov_b32 v[156:157], 0, 0
	v_pk_mov_b32 v[158:159], 0, 0
.LBB0_671:
	ds_read_b128 v[24:27], v209
	ds_read_b128 v[28:31], v209 offset:1024
	ds_read_b128 v[16:19], v209 offset:2048
	ds_read_b128 v[20:23], v209 offset:3072
	ds_read_b128 v[8:11], v210
	ds_read_b128 v[12:15], v210 offset:1024
	ds_read_b128 v[0:3], v210 offset:2048
	ds_read_b128 v[4:7], v210 offset:3072
	s_add_u32 s28, s30, 0x100
	s_addc_u32 s29, s31, 0
	s_cmp_eq_u32 s65, 18
	s_cselect_b32 s37, s23, s29
	s_cselect_b32 s36, s22, s28
	s_cselect_b32 s35, s27, s64
	s_cselect_b32 s34, s26, s63
	v_lshl_add_u64 v[160:161], s[30:31], 0, v[172:173]
	s_add_i32 m0, s40, 0xc000
	ds_read_b128 v[178:181], v211
	ds_read_b128 v[182:185], v211 offset:1024
	ds_read_b128 v[186:189], v211 offset:2048
	ds_read_b128 v[190:193], v211 offset:3072
	ds_read_b128 v[194:197], v211 offset:4096
	ds_read_b128 v[198:201], v211 offset:5120
	ds_read_b128 v[212:215], v211 offset:6144
	ds_read_b128 v[216:219], v211 offset:7168
	global_load_lds_dwordx4 v[160:161], off
	v_lshl_add_u64 v[160:161], s[30:31], 0, v[174:175]
	s_add_i32 m0, s40, 0xe000
	s_nop 0
	global_load_lds_dwordx4 v[160:161], off
	s_waitcnt vmcnt(8)
	s_waitcnt lgkmcnt(0)
	s_barrier
	s_waitcnt lgkmcnt(0)
	v_mfma_f32_16x16x128_f8f6f4 v[156:159], v[24:31], v[178:185], v[156:159]
	v_mfma_f32_16x16x128_f8f6f4 v[152:155], v[16:23], v[178:185], v[152:155]
	v_mfma_f32_16x16x128_f8f6f4 v[140:143], v[24:31], v[186:193], v[140:143]
	v_mfma_f32_16x16x128_f8f6f4 v[136:139], v[16:23], v[186:193], v[136:139]
	v_mfma_f32_16x16x128_f8f6f4 v[124:127], v[24:31], v[194:201], v[124:127]
	v_mfma_f32_16x16x128_f8f6f4 v[120:123], v[16:23], v[194:201], v[120:123]
	v_mfma_f32_16x16x128_f8f6f4 v[108:111], v[24:31], v[212:219], v[108:111]
	v_mfma_f32_16x16x128_f8f6f4 v[104:107], v[16:23], v[212:219], v[104:107]
	v_mfma_f32_16x16x128_f8f6f4 v[148:151], v[8:15], v[178:185], v[148:151]
	v_mfma_f32_16x16x128_f8f6f4 v[144:147], v[0:7], v[178:185], v[144:147]
	v_mfma_f32_16x16x128_f8f6f4 v[132:135], v[8:15], v[186:193], v[132:135]
	v_mfma_f32_16x16x128_f8f6f4 v[128:131], v[0:7], v[186:193], v[128:131]
	v_mfma_f32_16x16x128_f8f6f4 v[116:119], v[8:15], v[194:201], v[116:119]
	v_mfma_f32_16x16x128_f8f6f4 v[112:115], v[0:7], v[194:201], v[112:115]
	v_mfma_f32_16x16x128_f8f6f4 v[100:103], v[8:15], v[212:219], v[100:103]
	v_mfma_f32_16x16x128_f8f6f4 v[96:99], v[0:7], v[212:219], v[96:99]
	s_barrier
	s_add_i32 s30, s53, s39
	v_lshl_add_u64 v[160:161], s[34:35], 0, v[168:169]
	s_mov_b32 m0, s30
	ds_read_b128 v[182:185], v211 offset:16384
	ds_read_b128 v[186:189], v211 offset:17408
	ds_read_b128 v[190:193], v211 offset:18432
	ds_read_b128 v[194:197], v211 offset:19456
	ds_read_b128 v[198:201], v211 offset:20480
	ds_read_b128 v[202:205], v211 offset:21504
	ds_read_b128 v[212:215], v211 offset:22528
	ds_read_b128 v[216:219], v211 offset:23552
	global_load_lds_dwordx4 v[160:161], off
	s_add_i32 m0, s30, 0x2000
	s_add_u32 s30, s34, 0x58000
	v_lshl_add_u64 v[162:163], s[34:35], 0, v[164:165]
	s_addc_u32 s31, s35, 0
	s_add_i32 s66, s54, s39
	global_load_lds_dwordx4 v[162:163], off
	v_lshl_add_u64 v[178:179], s[30:31], 0, v[168:169]
	s_mov_b32 m0, s66
	v_lshl_add_u64 v[180:181], s[36:37], 0, v[166:167]
	global_load_lds_dwordx4 v[178:179], off
	v_lshl_add_u64 v[178:179], s[30:31], 0, v[164:165]
	s_add_i32 m0, s66, 0x2000
	s_nop 0
	global_load_lds_dwordx4 v[178:179], off
	v_lshl_add_u64 v[178:179], s[36:37], 0, v[170:171]
	s_mov_b32 m0, s40
	s_nop 0
	global_load_lds_dwordx4 v[178:179], off
	s_mov_b32 m0, s41
	s_nop 0
	global_load_lds_dwordx4 v[180:181], off
	s_waitcnt vmcnt(8)
	s_waitcnt lgkmcnt(0)
	s_barrier
; #define PG8_LDA(dst, b, h) do { _Pragma("unroll") for (int m = 0; m < 4; ++m) _Pragma("unroll") for (int k = 0; k < 2; ++k) dst[m][k] = *(const PG8_LAS bf16x8*)(lds + PG8_SA(b, h) + aoff + m * 2048 + k * 1024); } while (0)
; #define PG8_LDB(dst, b, h) do { _Pragma("unroll") for (int n = 0; n < 2; ++n) _Pragma("unroll") for (int k = 0; k < 2; ++k) dst[n][k] = *(const PG8_LAS bf16x8*)(lds + PG8_SB(b, h) + boff + n * 2048 + k * 1024); } while (0)
; #define PG8_WAIT_V(n) asm volatile("s_waitcnt vmcnt(" #n ")" ::: "memory")
; #define PG8_WAIT_L(n) asm volatile("s_waitcnt lgkmcnt(" #n ")" ::: "memory")
; #define PG8_BAR __builtin_amdgcn_s_barrier()
; #define PG8_SCHED __builtin_amdgcn_sched_barrier(0)
; template <class Epi, class Sched, bool ALIGN_EPI = false, bool SP2 = false, bool F8 = false, bool I8 = false, bool PF = false>
; __device__ __forceinline__ void gemm_phase(PG8_LAS unsigned char* lds, const Gemm g, const Sched& S, const Epi& E, const int wave_) {
;     ...
;             if constexpr (SP2) {
;             PG8_LDB(B0, 0, 0); PG8_LDB(B1, 0, 1); PG8_SCHED; PG8_LDA(At, 0, 0); PG8_STAGE(PG8_SA(1, 1), a1 + hstep, voffA);
;             PG8_WAIT_V(8); PG8_WAIT_L(0); PG8_BAR; PG8_MMA(0, 0, At, B0); PG8_MMA(0, 1, At, B1); PG8_BAR; PG8_SCHED;
;             PG8_LDA(At, 0, 1); PG8_STAGE(PG8_SB(0, 0), b2, voffB); PG8_STAGE(PG8_SB(0, 1), b2 + hstep, voffB); PG8_STAGE(PG8_SA(0, 0), a2, voffA);
;             PG8_WAIT_V(8); PG8_WAIT_L(0); PG8_BAR; PG8_MMA(1, 0, At, B0); PG8_MMA(1, 1, At, B1); PG8_BAR; PG8_SCHED;
;             PG8_LDB(B0, 1, 0); PG8_LDB(B1, 1, 1); PG8_SCHED; PG8_LDA(At, 1, 0); PG8_STAGE(PG8_SA(0, 1), a2 + hstep, voffA);
;             PG8_WAIT_V(8); PG8_WAIT_L(0); PG8_BAR; PG8_MMA(0, 0, At, B0); PG8_MMA(0, 1, At, B1); PG8_BAR; PG8_SCHED;
;             PG8_LDA(At, 1, 1); PG8_STAGE(PG8_SB(1, 0), b3, voffB); PG8_STAGE(PG8_SB(1, 1), b3 + hstep, voffB); PG8_STAGE(PG8_SA(1, 0), a3, voffA);
;             PG8_WAIT_V(8); PG8_WAIT_L(0); PG8_BAR; PG8_MMA(1, 0, At, B0); PG8_MMA(1, 1, At, B1); PG8_BAR; PG8_SCHED;
	s_waitcnt lgkmcnt(0)
	v_mfma_f32_16x16x128_f8f6f4 v[92:95], v[24:31], v[182:189], v[92:95]
	v_mfma_f32_16x16x128_f8f6f4 v[88:91], v[16:23], v[182:189], v[88:91]
	v_mfma_f32_16x16x128_f8f6f4 v[76:79], v[24:31], v[190:197], v[76:79]
	v_mfma_f32_16x16x128_f8f6f4 v[72:75], v[16:23], v[190:197], v[72:75]
	v_mfma_f32_16x16x128_f8f6f4 v[60:63], v[24:31], v[198:205], v[60:63]
	v_mfma_f32_16x16x128_f8f6f4 v[56:59], v[16:23], v[198:205], v[56:59]
	v_mfma_f32_16x16x128_f8f6f4 v[44:47], v[24:31], v[212:219], v[44:47]
	v_mfma_f32_16x16x128_f8f6f4 v[40:43], v[16:23], v[212:219], v[40:43]
	v_mfma_f32_16x16x128_f8f6f4 v[84:87], v[8:15], v[182:189], v[84:87]
	v_mfma_f32_16x16x128_f8f6f4 v[80:83], v[0:7], v[182:189], v[80:83]
	v_mfma_f32_16x16x128_f8f6f4 v[68:71], v[8:15], v[190:197], v[68:71]
	v_mfma_f32_16x16x128_f8f6f4 v[64:67], v[0:7], v[190:197], v[64:67]
	v_mfma_f32_16x16x128_f8f6f4 v[52:55], v[8:15], v[198:205], v[52:55]
	v_mfma_f32_16x16x128_f8f6f4 v[48:51], v[0:7], v[198:205], v[48:51]
	v_mfma_f32_16x16x128_f8f6f4 v[36:39], v[8:15], v[212:219], v[36:39]
	v_mfma_f32_16x16x128_f8f6f4 v[32:35], v[0:7], v[212:219], v[32:35]
	s_barrier
	s_add_i32 s66, 0, 0x18000
	s_add_i32 s67, 0, 0x1c000
	v_add_u32_e32 v12, s66, v208
	v_add_u32_e32 v28, s67, v208
	ds_read_b128 v[0:3], v12
	ds_read_b128 v[4:7], v12 offset:1024
	ds_read_b128 v[8:11], v12 offset:2048
	ds_read_b128 v[12:15], v12 offset:3072
	ds_read_b128 v[16:19], v28
	ds_read_b128 v[20:23], v28 offset:1024
	ds_read_b128 v[24:27], v28 offset:2048
	ds_read_b128 v[28:31], v28 offset:3072
	s_add_u32 s30, s36, 0x58000
	s_addc_u32 s31, s37, 0
	s_mov_b32 m0, s42
	v_lshl_add_u64 v[206:207], s[30:31], 0, v[170:171]
	ds_read_b128 v[182:185], v211 offset:32768
	ds_read_b128 v[186:189], v211 offset:33792
	ds_read_b128 v[190:193], v211 offset:34816
	ds_read_b128 v[194:197], v211 offset:35840
	ds_read_b128 v[198:201], v211 offset:36864
	ds_read_b128 v[202:205], v211 offset:37888
	ds_read_b128 v[212:215], v211 offset:38912
	ds_read_b128 v[216:219], v211 offset:39936
	global_load_lds_dwordx4 v[206:207], off
	v_lshl_add_u64 v[206:207], s[30:31], 0, v[166:167]
	s_mov_b32 m0, s43
	s_nop 0
	global_load_lds_dwordx4 v[206:207], off
	s_waitcnt vmcnt(8)
	s_waitcnt lgkmcnt(0)
	s_barrier
	s_waitcnt lgkmcnt(0)
	v_mfma_f32_16x16x128_f8f6f4 v[156:159], v[0:7], v[182:189], v[156:159]
	v_mfma_f32_16x16x128_f8f6f4 v[152:155], v[8:15], v[182:189], v[152:155]
	v_mfma_f32_16x16x128_f8f6f4 v[140:143], v[0:7], v[190:197], v[140:143]
	v_mfma_f32_16x16x128_f8f6f4 v[136:139], v[8:15], v[190:197], v[136:139]
	v_mfma_f32_16x16x128_f8f6f4 v[124:127], v[0:7], v[198:205], v[124:127]
	v_mfma_f32_16x16x128_f8f6f4 v[120:123], v[8:15], v[198:205], v[120:123]
	v_mfma_f32_16x16x128_f8f6f4 v[108:111], v[0:7], v[212:219], v[108:111]
	v_mfma_f32_16x16x128_f8f6f4 v[104:107], v[8:15], v[212:219], v[104:107]
	v_mfma_f32_16x16x128_f8f6f4 v[148:151], v[16:23], v[182:189], v[148:151]
	v_mfma_f32_16x16x128_f8f6f4 v[144:147], v[24:31], v[182:189], v[144:147]
	v_mfma_f32_16x16x128_f8f6f4 v[132:135], v[16:23], v[190:197], v[132:135]
	v_mfma_f32_16x16x128_f8f6f4 v[128:131], v[24:31], v[190:197], v[128:131]
	v_mfma_f32_16x16x128_f8f6f4 v[116:119], v[16:23], v[198:205], v[116:119]
	v_mfma_f32_16x16x128_f8f6f4 v[112:115], v[24:31], v[198:205], v[112:115]
	v_mfma_f32_16x16x128_f8f6f4 v[100:103], v[16:23], v[212:219], v[100:103]
	v_mfma_f32_16x16x128_f8f6f4 v[96:99], v[24:31], v[212:219], v[96:99]
	s_barrier
	s_add_i32 s30, s66, s39
	v_lshl_add_u64 v[160:161], v[160:161], 0, s[10:11]
	s_mov_b32 m0, s30
	ds_read_b128 v[182:185], v211 offset:49152
	ds_read_b128 v[186:189], v211 offset:50176
	ds_read_b128 v[190:193], v211 offset:51200
	ds_read_b128 v[194:197], v211 offset:52224
	ds_read_b128 v[198:201], v211 offset:53248
	ds_read_b128 v[202:205], v211 offset:54272
	ds_read_b128 v[212:215], v211 offset:55296
	ds_read_b128 v[216:219], v211 offset:56320
	global_load_lds_dwordx4 v[160:161], off
	s_add_i32 m0, s30, 0x2000
	s_add_u32 s30, s34, 0x58080
	v_lshl_add_u64 v[160:161], v[162:163], 0, s[10:11]
	s_addc_u32 s31, s35, 0
	s_add_i32 s34, s67, s39
	global_load_lds_dwordx4 v[160:161], off
	v_lshl_add_u64 v[160:161], s[30:31], 0, v[168:169]
	s_mov_b32 m0, s34
	s_nop 0
	global_load_lds_dwordx4 v[160:161], off
	v_lshl_add_u64 v[160:161], s[30:31], 0, v[164:165]
	s_add_i32 m0, s34, 0x2000
	s_nop 0
	global_load_lds_dwordx4 v[160:161], off
	v_lshl_add_u64 v[160:161], v[178:179], 0, s[10:11]
	s_mov_b32 m0, s50
	s_nop 0
	global_load_lds_dwordx4 v[160:161], off
	v_lshl_add_u64 v[160:161], v[180:181], 0, s[10:11]
	s_mov_b32 m0, s51
	s_nop 0
	global_load_lds_dwordx4 v[160:161], off
	s_waitcnt vmcnt(8)
	s_waitcnt lgkmcnt(0)
	s_barrier
	s_waitcnt lgkmcnt(0)
	v_mfma_f32_16x16x128_f8f6f4 v[92:95], v[0:7], v[182:189], v[92:95]
	v_mfma_f32_16x16x128_f8f6f4 v[88:91], v[8:15], v[182:189], v[88:91]
	v_mfma_f32_16x16x128_f8f6f4 v[76:79], v[0:7], v[190:197], v[76:79]
	v_mfma_f32_16x16x128_f8f6f4 v[72:75], v[8:15], v[190:197], v[72:75]
	v_mfma_f32_16x16x128_f8f6f4 v[60:63], v[0:7], v[198:205], v[60:63]
	v_mfma_f32_16x16x128_f8f6f4 v[56:59], v[8:15], v[198:205], v[56:59]
	v_mfma_f32_16x16x128_f8f6f4 v[44:47], v[0:7], v[212:219], v[44:47]
	v_mfma_f32_16x16x128_f8f6f4 v[40:43], v[8:15], v[212:219], v[40:43]
	v_mfma_f32_16x16x128_f8f6f4 v[84:87], v[16:23], v[182:189], v[84:87]
	v_mfma_f32_16x16x128_f8f6f4 v[80:83], v[24:31], v[182:189], v[80:83]
	v_mfma_f32_16x16x128_f8f6f4 v[68:71], v[16:23], v[190:197], v[68:71]
	v_mfma_f32_16x16x128_f8f6f4 v[64:67], v[24:31], v[190:197], v[64:67]
	v_mfma_f32_16x16x128_f8f6f4 v[52:55], v[16:23], v[198:205], v[52:55]
	v_mfma_f32_16x16x128_f8f6f4 v[48:51], v[24:31], v[198:205], v[48:51]
	v_mfma_f32_16x16x128_f8f6f4 v[36:39], v[16:23], v[212:219], v[36:39]
	v_mfma_f32_16x16x128_f8f6f4 v[32:35], v[24:31], v[212:219], v[32:35]
	s_add_i32 s65, s65, 2
	s_add_u32 s63, s63, 0x100
	s_addc_u32 s64, s64, 0
	s_cmp_gt_u32 s65, 19
	s_mov_b64 s[30:31], s[28:29]
	s_barrier
	s_cbranch_scc0 .LBB0_671
	s_and_b64 vcc, exec, s[12:13]
	s_cbranch_vccz .LBB0_674
	s_barrier

; #define PG8_LDA(dst, b, h) do { _Pragma("unroll") for (int m = 0; m < 4; ++m) _Pragma("unroll") for (int k = 0; k < 2; ++k) dst[m][k] = *(const PG8_LAS bf16x8*)(lds + PG8_SA(b, h) + aoff + m * 2048 + k * 1024); } while (0)
; #define PG8_LDB(dst, b, h) do { _Pragma("unroll") for (int n = 0; n < 2; ++n) _Pragma("unroll") for (int k = 0; k < 2; ++k) dst[n][k] = *(const PG8_LAS bf16x8*)(lds + PG8_SB(b, h) + boff + n * 2048 + k * 1024); } while (0)
; #define PG8_WAIT_V(n) asm volatile("s_waitcnt vmcnt(" #n ")" ::: "memory")
; #define PG8_WAIT_L(n) asm volatile("s_waitcnt lgkmcnt(" #n ")" ::: "memory")
; #define PG8_BAR __builtin_amdgcn_s_barrier()
; #define PG8_SCHED __builtin_amdgcn_sched_barrier(0)
; template <class Epi, class Sched, bool ALIGN_EPI = false, bool SP2 = false, bool F8 = false, bool I8 = false, bool PF = false>
; __device__ __forceinline__ void gemm_phase(PG8_LAS unsigned char* lds, const Gemm g, const Sched& S, const Epi& E, const int wave_) {
;     ...
;             if constexpr (SP2) {
;             PG8_LDB(B0, 0, 0); PG8_LDB(B1, 0, 1); PG8_SCHED; PG8_LDA(At, 0, 0); PG8_STAGE(PG8_SA(1, 1), a1 + hstep, voffA);
;             PG8_WAIT_V(8); PG8_WAIT_L(0); PG8_BAR; PG8_MMA(0, 0, At, B0); PG8_MMA(0, 1, At, B1); PG8_BAR; PG8_SCHED;
;     ...
;         for (int a = 0; a < 2; ++a)
; #pragma unroll
;             for (int b = 0; b < 2; ++b)
; #pragma unroll
;                 for (int m = 0; m < 4; ++m)
; #pragma unroll
;                     for (int n = 0; n < 2; ++n) acc[a][b][m][n] = (f32x4){0.f, 0.f, 0.f, 0.f};
.LBB0_808:
	s_ashr_i32 s19, s18, 31
	s_lshl_b64 s[22:23], s[18:19], 18
	s_add_u32 s22, s58, s22
	s_addc_u32 s23, s59, s23
	s_and_b64 s[26:27], s[20:21], exec
	s_cselect_b32 s19, s23, s31
	s_cselect_b32 s55, s22, s30
	s_ashr_i32 s17, s16, 31
	s_lshl_b64 s[26:27], s[16:17], 18
	s_add_u32 s26, s15, s26
	s_addc_u32 s27, s38, s27
	s_and_b64 s[36:37], s[20:21], exec
	s_cselect_b32 s17, s27, s35
	s_cselect_b32 s56, s26, s34
	s_add_u32 s30, s30, 0x20080
	s_addc_u32 s31, s31, 0
	s_add_u32 s57, s34, 0x100
	v_mov_b32_e32 v0, 0
	s_addc_u32 s62, s35, 0
	s_mov_b32 s63, -2
	v_mov_b32_e32 v1, v0
	v_mov_b32_e32 v2, v0
	v_mov_b32_e32 v3, v0
	v_mov_b32_e32 v4, v0
	v_mov_b32_e32 v5, v0
	v_mov_b32_e32 v6, v0
	v_mov_b32_e32 v7, v0
	s_waitcnt vmcnt(0)
	v_pk_mov_b32 v[16:17], 0, 0
	v_pk_mov_b32 v[18:19], 0, 0
	v_pk_mov_b32 v[20:21], 0, 0
	v_pk_mov_b32 v[22:23], 0, 0
	v_pk_mov_b32 v[32:33], 0, 0
	v_pk_mov_b32 v[34:35], 0, 0
	v_pk_mov_b32 v[36:37], 0, 0
	v_pk_mov_b32 v[38:39], 0, 0
	v_pk_mov_b32 v[48:49], 0, 0
	v_pk_mov_b32 v[50:51], 0, 0
	v_pk_mov_b32 v[52:53], 0, 0
	v_pk_mov_b32 v[54:55], 0, 0
	v_pk_mov_b32 v[8:9], 0, 0
	v_pk_mov_b32 v[10:11], 0, 0
	v_pk_mov_b32 v[12:13], 0, 0
	v_pk_mov_b32 v[14:15], 0, 0
	v_pk_mov_b32 v[24:25], 0, 0
	v_pk_mov_b32 v[26:27], 0, 0
	v_pk_mov_b32 v[28:29], 0, 0
	v_pk_mov_b32 v[30:31], 0, 0
	v_pk_mov_b32 v[40:41], 0, 0
	v_pk_mov_b32 v[42:43], 0, 0
	v_pk_mov_b32 v[44:45], 0, 0
	v_pk_mov_b32 v[46:47], 0, 0
	v_pk_mov_b32 v[56:57], 0, 0
	v_pk_mov_b32 v[58:59], 0, 0
	v_pk_mov_b32 v[60:61], 0, 0
	v_pk_mov_b32 v[62:63], 0, 0
	v_pk_mov_b32 v[64:65], 0, 0
	v_pk_mov_b32 v[66:67], 0, 0
	v_pk_mov_b32 v[68:69], 0, 0
	v_pk_mov_b32 v[70:71], 0, 0
	v_pk_mov_b32 v[80:81], 0, 0
	v_pk_mov_b32 v[82:83], 0, 0
	v_pk_mov_b32 v[84:85], 0, 0
	v_pk_mov_b32 v[86:87], 0, 0
	v_pk_mov_b32 v[96:97], 0, 0
	v_pk_mov_b32 v[98:99], 0, 0
	v_pk_mov_b32 v[100:101], 0, 0
	v_pk_mov_b32 v[102:103], 0, 0
	v_pk_mov_b32 v[112:113], 0, 0
	v_pk_mov_b32 v[114:115], 0, 0
	v_pk_mov_b32 v[116:117], 0, 0
	v_pk_mov_b32 v[118:119], 0, 0
	v_pk_mov_b32 v[72:73], 0, 0
	v_pk_mov_b32 v[74:75], 0, 0
	v_pk_mov_b32 v[76:77], 0, 0
	v_pk_mov_b32 v[78:79], 0, 0
	v_pk_mov_b32 v[88:89], 0, 0
	v_pk_mov_b32 v[90:91], 0, 0
	v_pk_mov_b32 v[92:93], 0, 0
	v_pk_mov_b32 v[94:95], 0, 0
	v_pk_mov_b32 v[104:105], 0, 0
	v_pk_mov_b32 v[106:107], 0, 0
	v_pk_mov_b32 v[108:109], 0, 0
	v_pk_mov_b32 v[110:111], 0, 0
	v_pk_mov_b32 v[120:121], 0, 0
	v_pk_mov_b32 v[122:123], 0, 0
	v_pk_mov_b32 v[124:125], 0, 0
	v_pk_mov_b32 v[126:127], 0, 0
.LBB0_809:
	ds_read_b128 v[142:145], v151
	ds_read_b128 v[156:159], v151 offset:1024
	ds_read_b128 v[160:163], v151 offset:2048
	ds_read_b128 v[164:167], v151 offset:3072
	ds_read_b128 v[168:171], v153
	ds_read_b128 v[172:175], v153 offset:1024
	ds_read_b128 v[176:179], v153 offset:2048
	ds_read_b128 v[180:183], v153 offset:3072
	s_add_u32 s34, s30, 0xfffe0080
	s_addc_u32 s35, s31, -1
	s_cmp_eq_u32 s63, 4
	s_cselect_b32 s37, s19, s35
	s_cselect_b32 s36, s55, s34
	s_cselect_b32 s35, s17, s62
	s_cselect_b32 s34, s56, s57
	v_lshl_add_u64 v[146:147], s[30:31], 0, v[136:137]
	s_add_i32 m0, s29, 0xc000
	ds_read_b128 v[184:187], v155
	ds_read_b128 v[188:191], v155 offset:1024
	ds_read_b128 v[192:195], v155 offset:2048
	ds_read_b128 v[196:199], v155 offset:3072
	ds_read_b128 v[200:203], v155 offset:4096
	ds_read_b128 v[204:207], v155 offset:5120
	ds_read_b128 v[208:211], v155 offset:6144
	ds_read_b128 v[212:215], v155 offset:7168
	global_load_lds_dwordx4 v[146:147], off
	v_lshl_add_u64 v[146:147], s[30:31], 0, v[138:139]
	s_add_i32 m0, s29, 0xe000
	s_nop 0
	global_load_lds_dwordx4 v[146:147], off
	s_waitcnt vmcnt(8)
	s_waitcnt lgkmcnt(0)
	s_barrier
	s_waitcnt lgkmcnt(0)
	v_mfma_i32_16x16x64_i8 v[124:127], v[142:145], v[184:187], v[124:127]
	v_mfma_i32_16x16x64_i8 v[120:123], v[160:163], v[184:187], v[120:123]
	v_mfma_i32_16x16x64_i8 v[108:111], v[142:145], v[192:195], v[108:111]
	v_mfma_i32_16x16x64_i8 v[104:107], v[160:163], v[192:195], v[104:107]
	v_mfma_i32_16x16x64_i8 v[92:95], v[142:145], v[200:203], v[92:95]
	v_mfma_i32_16x16x64_i8 v[88:91], v[160:163], v[200:203], v[88:91]
	v_mfma_i32_16x16x64_i8 v[76:79], v[142:145], v[208:211], v[76:79]
	v_mfma_i32_16x16x64_i8 v[72:75], v[160:163], v[208:211], v[72:75]
	v_mfma_i32_16x16x64_i8 v[124:127], v[156:159], v[188:191], v[124:127]
	v_mfma_i32_16x16x64_i8 v[120:123], v[164:167], v[188:191], v[120:123]
	v_mfma_i32_16x16x64_i8 v[108:111], v[156:159], v[196:199], v[108:111]
	v_mfma_i32_16x16x64_i8 v[104:107], v[164:167], v[196:199], v[104:107]
	v_mfma_i32_16x16x64_i8 v[92:95], v[156:159], v[204:207], v[92:95]
	v_mfma_i32_16x16x64_i8 v[88:91], v[164:167], v[204:207], v[88:91]
	v_mfma_i32_16x16x64_i8 v[76:79], v[156:159], v[212:215], v[76:79]
	v_mfma_i32_16x16x64_i8 v[72:75], v[164:167], v[212:215], v[72:75]
	v_mfma_i32_16x16x64_i8 v[116:119], v[168:171], v[184:187], v[116:119]
	v_mfma_i32_16x16x64_i8 v[112:115], v[176:179], v[184:187], v[112:115]
	v_mfma_i32_16x16x64_i8 v[100:103], v[168:171], v[192:195], v[100:103]
	v_mfma_i32_16x16x64_i8 v[96:99], v[176:179], v[192:195], v[96:99]
	v_mfma_i32_16x16x64_i8 v[84:87], v[168:171], v[200:203], v[84:87]
	v_mfma_i32_16x16x64_i8 v[80:83], v[176:179], v[200:203], v[80:83]
	v_mfma_i32_16x16x64_i8 v[68:71], v[168:171], v[208:211], v[68:71]
	v_mfma_i32_16x16x64_i8 v[64:67], v[176:179], v[208:211], v[64:67]
	v_mfma_i32_16x16x64_i8 v[116:119], v[172:175], v[188:191], v[116:119]
	v_mfma_i32_16x16x64_i8 v[112:115], v[180:183], v[188:191], v[112:115]
	v_mfma_i32_16x16x64_i8 v[100:103], v[172:175], v[196:199], v[100:103]
	v_mfma_i32_16x16x64_i8 v[96:99], v[180:183], v[196:199], v[96:99]
	v_mfma_i32_16x16x64_i8 v[84:87], v[172:175], v[204:207], v[84:87]
	v_mfma_i32_16x16x64_i8 v[80:83], v[180:183], v[204:207], v[80:83]
	v_mfma_i32_16x16x64_i8 v[68:71], v[172:175], v[212:215], v[68:71]
	v_mfma_i32_16x16x64_i8 v[64:67], v[180:183], v[212:215], v[64:67]
	s_barrier
; #define PG8_LDA(dst, b, h) do { _Pragma("unroll") for (int m = 0; m < 4; ++m) _Pragma("unroll") for (int k = 0; k < 2; ++k) dst[m][k] = *(const PG8_LAS bf16x8*)(lds + PG8_SA(b, h) + aoff + m * 2048 + k * 1024); } while (0)
; #define PG8_LDB(dst, b, h) do { _Pragma("unroll") for (int n = 0; n < 2; ++n) _Pragma("unroll") for (int k = 0; k < 2; ++k) dst[n][k] = *(const PG8_LAS bf16x8*)(lds + PG8_SB(b, h) + boff + n * 2048 + k * 1024); } while (0)
; #define PG8_WAIT_V(n) asm volatile("s_waitcnt vmcnt(" #n ")" ::: "memory")
; #define PG8_WAIT_L(n) asm volatile("s_waitcnt lgkmcnt(" #n ")" ::: "memory")
; #define PG8_BAR __builtin_amdgcn_s_barrier()
; #define PG8_SCHED __builtin_amdgcn_sched_barrier(0)
; template <class Epi, class Sched, bool ALIGN_EPI = false, bool SP2 = false, bool F8 = false, bool I8 = false, bool PF = false>
; __device__ __forceinline__ void gemm_phase(PG8_LAS unsigned char* lds, const Gemm g, const Sched& S, const Epi& E, const int wave_) {
;     ...
;             if constexpr (SP2) {
;             PG8_LDB(B0, 0, 0); PG8_LDB(B1, 0, 1); PG8_SCHED; PG8_LDA(At, 0, 0); PG8_STAGE(PG8_SA(1, 1), a1 + hstep, voffA);
;             PG8_WAIT_V(8); PG8_WAIT_L(0); PG8_BAR; PG8_MMA(0, 0, At, B0); PG8_MMA(0, 1, At, B1); PG8_BAR; PG8_SCHED;
;             PG8_LDA(At, 0, 1); PG8_STAGE(PG8_SB(0, 0), b2, voffB); PG8_STAGE(PG8_SB(0, 1), b2 + hstep, voffB); PG8_STAGE(PG8_SA(0, 0), a2, voffA);
;             PG8_WAIT_V(8); PG8_WAIT_L(0); PG8_BAR; PG8_MMA(1, 0, At, B0); PG8_MMA(1, 1, At, B1); PG8_BAR; PG8_SCHED;
;             PG8_LDB(B0, 1, 0); PG8_LDB(B1, 1, 1); PG8_SCHED; PG8_LDA(At, 1, 0); PG8_STAGE(PG8_SA(0, 1), a2 + hstep, voffA);
;             PG8_WAIT_V(8); PG8_WAIT_L(0); PG8_BAR; PG8_MMA(0, 0, At, B0); PG8_MMA(0, 1, At, B1); PG8_BAR; PG8_SCHED;
;             PG8_LDA(At, 1, 1); PG8_STAGE(PG8_SB(1, 0), b3, voffB); PG8_STAGE(PG8_SB(1, 1), b3 + hstep, voffB); PG8_STAGE(PG8_SA(1, 0), a3, voffA);
;             PG8_WAIT_V(8); PG8_WAIT_L(0); PG8_BAR; PG8_MMA(1, 0, At, B0); PG8_MMA(1, 1, At, B1); PG8_BAR; PG8_SCHED;
	s_add_i32 s64, s51, s39
	v_lshl_add_u64 v[146:147], s[34:35], 0, v[132:133]
	s_mov_b32 m0, s64
	ds_read_b128 v[184:187], v155 offset:16384
	ds_read_b128 v[188:191], v155 offset:17408
	ds_read_b128 v[192:195], v155 offset:18432
	ds_read_b128 v[196:199], v155 offset:19456
	ds_read_b128 v[200:203], v155 offset:20480
	ds_read_b128 v[204:207], v155 offset:21504
	ds_read_b128 v[208:211], v155 offset:22528
	ds_read_b128 v[212:215], v155 offset:23552
	global_load_lds_dwordx4 v[146:147], off
	s_add_i32 m0, s64, 0x2000
	s_add_u32 s64, s34, 0x20000
	v_lshl_add_u64 v[216:217], s[34:35], 0, v[128:129]
	s_addc_u32 s65, s35, 0
	s_add_i32 s66, s52, s39
	global_load_lds_dwordx4 v[216:217], off
	v_lshl_add_u64 v[218:219], s[64:65], 0, v[132:133]
	s_mov_b32 m0, s66
	v_lshl_add_u64 v[220:221], s[36:37], 0, v[130:131]
	global_load_lds_dwordx4 v[218:219], off
	v_lshl_add_u64 v[218:219], s[64:65], 0, v[128:129]
	s_add_i32 m0, s66, 0x2000
	s_nop 0
	global_load_lds_dwordx4 v[218:219], off
	v_lshl_add_u64 v[218:219], s[36:37], 0, v[134:135]
	s_mov_b32 m0, s29
	s_nop 0
	global_load_lds_dwordx4 v[218:219], off
	s_mov_b32 m0, s41
	s_nop 0
	global_load_lds_dwordx4 v[220:221], off
	s_waitcnt vmcnt(8)
	s_waitcnt lgkmcnt(0)
	s_barrier
	s_waitcnt lgkmcnt(0)
	v_mfma_i32_16x16x64_i8 v[60:63], v[142:145], v[184:187], v[60:63]
	v_mfma_i32_16x16x64_i8 v[56:59], v[160:163], v[184:187], v[56:59]
	v_mfma_i32_16x16x64_i8 v[44:47], v[142:145], v[192:195], v[44:47]
	v_mfma_i32_16x16x64_i8 v[40:43], v[160:163], v[192:195], v[40:43]
	v_mfma_i32_16x16x64_i8 v[28:31], v[142:145], v[200:203], v[28:31]
	v_mfma_i32_16x16x64_i8 v[24:27], v[160:163], v[200:203], v[24:27]
	v_mfma_i32_16x16x64_i8 v[12:15], v[142:145], v[208:211], v[12:15]
	v_mfma_i32_16x16x64_i8 v[8:11], v[160:163], v[208:211], v[8:11]
	v_mfma_i32_16x16x64_i8 v[60:63], v[156:159], v[188:191], v[60:63]
	v_mfma_i32_16x16x64_i8 v[56:59], v[164:167], v[188:191], v[56:59]
	v_mfma_i32_16x16x64_i8 v[44:47], v[156:159], v[196:199], v[44:47]
	v_mfma_i32_16x16x64_i8 v[40:43], v[164:167], v[196:199], v[40:43]
	v_mfma_i32_16x16x64_i8 v[28:31], v[156:159], v[204:207], v[28:31]
	v_mfma_i32_16x16x64_i8 v[24:27], v[164:167], v[204:207], v[24:27]
	v_mfma_i32_16x16x64_i8 v[12:15], v[156:159], v[212:215], v[12:15]
	v_mfma_i32_16x16x64_i8 v[8:11], v[164:167], v[212:215], v[8:11]
	v_mfma_i32_16x16x64_i8 v[52:55], v[168:171], v[184:187], v[52:55]
	v_mfma_i32_16x16x64_i8 v[48:51], v[176:179], v[184:187], v[48:51]
	v_mfma_i32_16x16x64_i8 v[36:39], v[168:171], v[192:195], v[36:39]
	v_mfma_i32_16x16x64_i8 v[32:35], v[176:179], v[192:195], v[32:35]
	v_mfma_i32_16x16x64_i8 v[20:23], v[168:171], v[200:203], v[20:23]
	v_mfma_i32_16x16x64_i8 v[16:19], v[176:179], v[200:203], v[16:19]
	v_mfma_i32_16x16x64_i8 v[4:7], v[168:171], v[208:211], v[4:7]
	v_mfma_i32_16x16x64_i8 v[0:3], v[176:179], v[208:211], v[0:3]
	v_mfma_i32_16x16x64_i8 v[52:55], v[172:175], v[188:191], v[52:55]
	v_mfma_i32_16x16x64_i8 v[48:51], v[180:183], v[188:191], v[48:51]
	v_mfma_i32_16x16x64_i8 v[36:39], v[172:175], v[196:199], v[36:39]
	v_mfma_i32_16x16x64_i8 v[32:35], v[180:183], v[196:199], v[32:35]
	v_mfma_i32_16x16x64_i8 v[20:23], v[172:175], v[204:207], v[20:23]
	v_mfma_i32_16x16x64_i8 v[16:19], v[180:183], v[204:207], v[16:19]
	v_mfma_i32_16x16x64_i8 v[4:7], v[172:175], v[212:215], v[4:7]
	v_mfma_i32_16x16x64_i8 v[0:3], v[180:183], v[212:215], v[0:3]
	s_barrier
	s_add_i32 s64, 0, 0x18000
	v_add_u32_e32 v148, s64, v149
	s_add_i32 s65, 0, 0x1c000
	ds_read_b128 v[142:145], v148
	ds_read_b128 v[156:159], v148 offset:1024
	ds_read_b128 v[160:163], v148 offset:2048
	ds_read_b128 v[164:167], v148 offset:3072
	v_add_u32_e32 v148, s65, v149
	ds_read_b128 v[168:171], v148
	ds_read_b128 v[172:175], v148 offset:1024
	ds_read_b128 v[176:179], v148 offset:2048
	ds_read_b128 v[180:183], v148 offset:3072
	s_add_u32 s36, s36, 0x20000
	s_addc_u32 s37, s37, 0
	s_mov_b32 m0, s42
	v_lshl_add_u64 v[222:223], s[36:37], 0, v[134:135]
	ds_read_b128 v[184:187], v155 offset:32768
	ds_read_b128 v[188:191], v155 offset:33792
	ds_read_b128 v[192:195], v155 offset:34816
	ds_read_b128 v[196:199], v155 offset:35840
	ds_read_b128 v[200:203], v155 offset:36864
	ds_read_b128 v[204:207], v155 offset:37888
	ds_read_b128 v[208:211], v155 offset:38912
	ds_read_b128 v[212:215], v155 offset:39936
	global_load_lds_dwordx4 v[222:223], off
	v_lshl_add_u64 v[222:223], s[36:37], 0, v[130:131]
	s_mov_b32 m0, s43
	s_nop 0
	global_load_lds_dwordx4 v[222:223], off
	s_waitcnt vmcnt(8)
	s_waitcnt lgkmcnt(0)
	s_barrier
; #define PG8_LDA(dst, b, h) do { _Pragma("unroll") for (int m = 0; m < 4; ++m) _Pragma("unroll") for (int k = 0; k < 2; ++k) dst[m][k] = *(const PG8_LAS bf16x8*)(lds + PG8_SA(b, h) + aoff + m * 2048 + k * 1024); } while (0)
; #define PG8_LDB(dst, b, h) do { _Pragma("unroll") for (int n = 0; n < 2; ++n) _Pragma("unroll") for (int k = 0; k < 2; ++k) dst[n][k] = *(const PG8_LAS bf16x8*)(lds + PG8_SB(b, h) + boff + n * 2048 + k * 1024); } while (0)
; #define PG8_WAIT_V(n) asm volatile("s_waitcnt vmcnt(" #n ")" ::: "memory")
; #define PG8_WAIT_L(n) asm volatile("s_waitcnt lgkmcnt(" #n ")" ::: "memory")
; #define PG8_BAR __builtin_amdgcn_s_barrier()
; #define PG8_SCHED __builtin_amdgcn_sched_barrier(0)
; template <class Epi, class Sched, bool ALIGN_EPI = false, bool SP2 = false, bool F8 = false, bool I8 = false, bool PF = false>
; __device__ __forceinline__ void gemm_phase(PG8_LAS unsigned char* lds, const Gemm g, const Sched& S, const Epi& E, const int wave_) {
;     ...
;             if constexpr (SP2) {
;             PG8_LDB(B0, 0, 0); PG8_LDB(B1, 0, 1); PG8_SCHED; PG8_LDA(At, 0, 0); PG8_STAGE(PG8_SA(1, 1), a1 + hstep, voffA);
;             PG8_WAIT_V(8); PG8_WAIT_L(0); PG8_BAR; PG8_MMA(0, 0, At, B0); PG8_MMA(0, 1, At, B1); PG8_BAR; PG8_SCHED;
;             PG8_LDA(At, 0, 1); PG8_STAGE(PG8_SB(0, 0), b2, voffB); PG8_STAGE(PG8_SB(0, 1), b2 + hstep, voffB); PG8_STAGE(PG8_SA(0, 0), a2, voffA);
;             PG8_WAIT_V(8); PG8_WAIT_L(0); PG8_BAR; PG8_MMA(1, 0, At, B0); PG8_MMA(1, 1, At, B1); PG8_BAR; PG8_SCHED;
;             PG8_LDB(B0, 1, 0); PG8_LDB(B1, 1, 1); PG8_SCHED; PG8_LDA(At, 1, 0); PG8_STAGE(PG8_SA(0, 1), a2 + hstep, voffA);
;             PG8_WAIT_V(8); PG8_WAIT_L(0); PG8_BAR; PG8_MMA(0, 0, At, B0); PG8_MMA(0, 1, At, B1); PG8_BAR; PG8_SCHED;
;             PG8_LDA(At, 1, 1); PG8_STAGE(PG8_SB(1, 0), b3, voffB); PG8_STAGE(PG8_SB(1, 1), b3 + hstep, voffB); PG8_STAGE(PG8_SA(1, 0), a3, voffA);
;             PG8_WAIT_V(8); PG8_WAIT_L(0); PG8_BAR; PG8_MMA(1, 0, At, B0); PG8_MMA(1, 1, At, B1); PG8_BAR; PG8_SCHED;
	s_waitcnt lgkmcnt(0)
	v_mfma_i32_16x16x64_i8 v[124:127], v[142:145], v[184:187], v[124:127]
	v_mfma_i32_16x16x64_i8 v[120:123], v[160:163], v[184:187], v[120:123]
	v_mfma_i32_16x16x64_i8 v[108:111], v[142:145], v[192:195], v[108:111]
	v_mfma_i32_16x16x64_i8 v[104:107], v[160:163], v[192:195], v[104:107]
	v_mfma_i32_16x16x64_i8 v[92:95], v[142:145], v[200:203], v[92:95]
	v_mfma_i32_16x16x64_i8 v[88:91], v[160:163], v[200:203], v[88:91]
	v_mfma_i32_16x16x64_i8 v[76:79], v[142:145], v[208:211], v[76:79]
	v_mfma_i32_16x16x64_i8 v[72:75], v[160:163], v[208:211], v[72:75]
	v_mfma_i32_16x16x64_i8 v[124:127], v[156:159], v[188:191], v[124:127]
	v_mfma_i32_16x16x64_i8 v[120:123], v[164:167], v[188:191], v[120:123]
	v_mfma_i32_16x16x64_i8 v[108:111], v[156:159], v[196:199], v[108:111]
	v_mfma_i32_16x16x64_i8 v[104:107], v[164:167], v[196:199], v[104:107]
	v_mfma_i32_16x16x64_i8 v[92:95], v[156:159], v[204:207], v[92:95]
	v_mfma_i32_16x16x64_i8 v[88:91], v[164:167], v[204:207], v[88:91]
	v_mfma_i32_16x16x64_i8 v[76:79], v[156:159], v[212:215], v[76:79]
	v_mfma_i32_16x16x64_i8 v[72:75], v[164:167], v[212:215], v[72:75]
	v_mfma_i32_16x16x64_i8 v[116:119], v[168:171], v[184:187], v[116:119]
	v_mfma_i32_16x16x64_i8 v[112:115], v[176:179], v[184:187], v[112:115]
	v_mfma_i32_16x16x64_i8 v[100:103], v[168:171], v[192:195], v[100:103]
	v_mfma_i32_16x16x64_i8 v[96:99], v[176:179], v[192:195], v[96:99]
	v_mfma_i32_16x16x64_i8 v[84:87], v[168:171], v[200:203], v[84:87]
	v_mfma_i32_16x16x64_i8 v[80:83], v[176:179], v[200:203], v[80:83]
	v_mfma_i32_16x16x64_i8 v[68:71], v[168:171], v[208:211], v[68:71]
	v_mfma_i32_16x16x64_i8 v[64:67], v[176:179], v[208:211], v[64:67]
	v_mfma_i32_16x16x64_i8 v[116:119], v[172:175], v[188:191], v[116:119]
	v_mfma_i32_16x16x64_i8 v[112:115], v[180:183], v[188:191], v[112:115]
	v_mfma_i32_16x16x64_i8 v[100:103], v[172:175], v[196:199], v[100:103]
	v_mfma_i32_16x16x64_i8 v[96:99], v[180:183], v[196:199], v[96:99]
	v_mfma_i32_16x16x64_i8 v[84:87], v[172:175], v[204:207], v[84:87]
	v_mfma_i32_16x16x64_i8 v[80:83], v[180:183], v[204:207], v[80:83]
	v_mfma_i32_16x16x64_i8 v[68:71], v[172:175], v[212:215], v[68:71]
	v_mfma_i32_16x16x64_i8 v[64:67], v[180:183], v[212:215], v[64:67]
	s_barrier
	s_add_i32 s36, s64, s39
	v_lshl_add_u64 v[146:147], v[146:147], 0, s[10:11]
	s_mov_b32 m0, s36
	ds_read_b128 v[184:187], v155 offset:49152
	ds_read_b128 v[188:191], v155 offset:50176
	ds_read_b128 v[192:195], v155 offset:51200
	ds_read_b128 v[196:199], v155 offset:52224
	ds_read_b128 v[200:203], v155 offset:53248
	ds_read_b128 v[204:207], v155 offset:54272
	ds_read_b128 v[208:211], v155 offset:55296
	ds_read_b128 v[212:215], v155 offset:56320
	global_load_lds_dwordx4 v[146:147], off
	s_add_i32 m0, s36, 0x2000
	s_add_u32 s34, s34, 0x20080
	v_lshl_add_u64 v[146:147], v[216:217], 0, s[10:11]
	s_addc_u32 s35, s35, 0
	s_add_i32 s36, s65, s39
	global_load_lds_dwordx4 v[146:147], off
	v_lshl_add_u64 v[146:147], s[34:35], 0, v[132:133]
	s_mov_b32 m0, s36
	s_nop 0
	global_load_lds_dwordx4 v[146:147], off
	v_lshl_add_u64 v[146:147], s[34:35], 0, v[128:129]
	s_add_i32 m0, s36, 0x2000
	s_nop 0
	global_load_lds_dwordx4 v[146:147], off
	v_lshl_add_u64 v[146:147], v[218:219], 0, s[10:11]
	s_mov_b32 m0, s48
	s_nop 0
	global_load_lds_dwordx4 v[146:147], off
	v_lshl_add_u64 v[146:147], v[220:221], 0, s[10:11]
	s_mov_b32 m0, s49
	s_nop 0
	global_load_lds_dwordx4 v[146:147], off
	s_waitcnt vmcnt(8)
	s_waitcnt lgkmcnt(0)
	s_barrier
	s_waitcnt lgkmcnt(0)
	v_mfma_i32_16x16x64_i8 v[60:63], v[142:145], v[184:187], v[60:63]
	v_mfma_i32_16x16x64_i8 v[56:59], v[160:163], v[184:187], v[56:59]
	v_mfma_i32_16x16x64_i8 v[44:47], v[142:145], v[192:195], v[44:47]
	v_mfma_i32_16x16x64_i8 v[40:43], v[160:163], v[192:195], v[40:43]
	v_mfma_i32_16x16x64_i8 v[28:31], v[142:145], v[200:203], v[28:31]
	v_mfma_i32_16x16x64_i8 v[24:27], v[160:163], v[200:203], v[24:27]
	v_mfma_i32_16x16x64_i8 v[12:15], v[142:145], v[208:211], v[12:15]
	v_mfma_i32_16x16x64_i8 v[8:11], v[160:163], v[208:211], v[8:11]
	v_mfma_i32_16x16x64_i8 v[60:63], v[156:159], v[188:191], v[60:63]
	v_mfma_i32_16x16x64_i8 v[56:59], v[164:167], v[188:191], v[56:59]
	v_mfma_i32_16x16x64_i8 v[44:47], v[156:159], v[196:199], v[44:47]
	v_mfma_i32_16x16x64_i8 v[40:43], v[164:167], v[196:199], v[40:43]
	v_mfma_i32_16x16x64_i8 v[28:31], v[156:159], v[204:207], v[28:31]
	v_mfma_i32_16x16x64_i8 v[24:27], v[164:167], v[204:207], v[24:27]
	v_mfma_i32_16x16x64_i8 v[12:15], v[156:159], v[212:215], v[12:15]
	v_mfma_i32_16x16x64_i8 v[8:11], v[164:167], v[212:215], v[8:11]
	v_mfma_i32_16x16x64_i8 v[52:55], v[168:171], v[184:187], v[52:55]
	v_mfma_i32_16x16x64_i8 v[48:51], v[176:179], v[184:187], v[48:51]
	v_mfma_i32_16x16x64_i8 v[36:39], v[168:171], v[192:195], v[36:39]
	v_mfma_i32_16x16x64_i8 v[32:35], v[176:179], v[192:195], v[32:35]
	v_mfma_i32_16x16x64_i8 v[20:23], v[168:171], v[200:203], v[20:23]
	v_mfma_i32_16x16x64_i8 v[16:19], v[176:179], v[200:203], v[16:19]
	v_mfma_i32_16x16x64_i8 v[4:7], v[168:171], v[208:211], v[4:7]
	v_mfma_i32_16x16x64_i8 v[0:3], v[176:179], v[208:211], v[0:3]
	v_mfma_i32_16x16x64_i8 v[52:55], v[172:175], v[188:191], v[52:55]
	v_mfma_i32_16x16x64_i8 v[48:51], v[180:183], v[188:191], v[48:51]
	v_mfma_i32_16x16x64_i8 v[36:39], v[172:175], v[196:199], v[36:39]
	v_mfma_i32_16x16x64_i8 v[32:35], v[180:183], v[196:199], v[32:35]
	v_mfma_i32_16x16x64_i8 v[20:23], v[172:175], v[204:207], v[20:23]
	v_mfma_i32_16x16x64_i8 v[16:19], v[180:183], v[204:207], v[16:19]
	v_mfma_i32_16x16x64_i8 v[4:7], v[172:175], v[212:215], v[4:7]
	v_mfma_i32_16x16x64_i8 v[0:3], v[180:183], v[212:215], v[0:3]
	s_add_i32 s63, s63, 2
	s_add_u32 s30, s30, 0x100
	s_addc_u32 s31, s31, 0
	s_add_u32 s57, s57, 0x100
	s_addc_u32 s62, s62, 0
	s_cmp_gt_u32 s63, 5
	s_barrier
	s_cbranch_scc0 .LBB0_809
	s_and_b64 vcc, exec, s[12:13]
	s_cbranch_vccz .LBB0_812
	s_barrier

; #define PG8_LDA(dst, b, h) do { _Pragma("unroll") for (int m = 0; m < 4; ++m) _Pragma("unroll") for (int k = 0; k < 2; ++k) dst[m][k] = *(const PG8_LAS bf16x8*)(lds + PG8_SA(b, h) + aoff + m * 2048 + k * 1024); } while (0)
; #define PG8_LDB(dst, b, h) do { _Pragma("unroll") for (int n = 0; n < 2; ++n) _Pragma("unroll") for (int k = 0; k < 2; ++k) dst[n][k] = *(const PG8_LAS bf16x8*)(lds + PG8_SB(b, h) + boff + n * 2048 + k * 1024); } while (0)
; #define PG8_WAIT_V(n) asm volatile("s_waitcnt vmcnt(" #n ")" ::: "memory")
; #define PG8_WAIT_L(n) asm volatile("s_waitcnt lgkmcnt(" #n ")" ::: "memory")
; #define PG8_BAR __builtin_amdgcn_s_barrier()
; #define PG8_SCHED __builtin_amdgcn_sched_barrier(0)
; template <class Epi, class Sched, bool ALIGN_EPI = false, bool SP2 = false, bool F8 = false, bool I8 = false, bool PF = false>
; __device__ __forceinline__ void gemm_phase(PG8_LAS unsigned char* lds, const Gemm g, const Sched& S, const Epi& E, const int wave_) {
;     ...
;             if constexpr (SP2) {
;             PG8_LDB(B0, 0, 0); PG8_LDB(B1, 0, 1); PG8_SCHED; PG8_LDA(At, 0, 0); PG8_STAGE(PG8_SA(1, 1), a1 + hstep, voffA);
;             PG8_WAIT_V(8); PG8_WAIT_L(0); PG8_BAR; PG8_MMA(0, 0, At, B0); PG8_MMA(0, 1, At, B1); PG8_BAR; PG8_SCHED;
;     ...
;         for (int a = 0; a < 2; ++a)
; #pragma unroll
;             for (int b = 0; b < 2; ++b)
; #pragma unroll
;                 for (int m = 0; m < 4; ++m)
; #pragma unroll
;                     for (int n = 0; n < 2; ++n) acc[a][b][m][n] = (f32x4){0.f, 0.f, 0.f, 0.f};
.LBB0_966:
	s_ashr_i32 s27, s26, 31
	s_lshl_b64 s[30:31], s[26:27], 18
	s_add_u32 s30, s49, s30
	s_addc_u32 s31, s50, s31
	s_and_b64 s[34:35], s[28:29], exec
	s_cselect_b32 s5, s31, s39
	s_cselect_b32 s27, s30, s38
	s_ashr_i32 s23, s22, 31
	s_lshl_b64 s[34:35], s[22:23], 18
	s_add_u32 s34, s46, s34
	s_addc_u32 s35, s47, s35
	s_and_b64 s[42:43], s[28:29], exec
	s_cselect_b32 s23, s35, s41
	s_cselect_b32 s37, s34, s40
	s_add_u32 s38, s38, 0x20080
	s_addc_u32 s39, s39, 0
	s_add_u32 s70, s40, 0x100
	v_mov_b32_e32 v0, 0
	s_addc_u32 s71, s41, 0
	s_mov_b32 s72, -2
	v_mov_b32_e32 v1, v0
	v_mov_b32_e32 v2, v0
	v_mov_b32_e32 v3, v0
	v_mov_b32_e32 v4, v0
	v_mov_b32_e32 v5, v0
	v_mov_b32_e32 v6, v0
	v_mov_b32_e32 v7, v0
	s_waitcnt vmcnt(0)
	v_pk_mov_b32 v[16:17], 0, 0
	v_pk_mov_b32 v[18:19], 0, 0
	v_pk_mov_b32 v[20:21], 0, 0
	v_pk_mov_b32 v[22:23], 0, 0
	v_pk_mov_b32 v[32:33], 0, 0
	v_pk_mov_b32 v[34:35], 0, 0
	v_pk_mov_b32 v[36:37], 0, 0
	v_pk_mov_b32 v[38:39], 0, 0
	v_pk_mov_b32 v[48:49], 0, 0
	v_pk_mov_b32 v[50:51], 0, 0
	v_pk_mov_b32 v[52:53], 0, 0
	v_pk_mov_b32 v[54:55], 0, 0
	v_pk_mov_b32 v[8:9], 0, 0
	v_pk_mov_b32 v[10:11], 0, 0
	v_pk_mov_b32 v[12:13], 0, 0
	v_pk_mov_b32 v[14:15], 0, 0
	v_pk_mov_b32 v[24:25], 0, 0
	v_pk_mov_b32 v[26:27], 0, 0
	v_pk_mov_b32 v[28:29], 0, 0
	v_pk_mov_b32 v[30:31], 0, 0
	v_pk_mov_b32 v[40:41], 0, 0
	v_pk_mov_b32 v[42:43], 0, 0
	v_pk_mov_b32 v[44:45], 0, 0
	v_pk_mov_b32 v[46:47], 0, 0
	v_pk_mov_b32 v[56:57], 0, 0
	v_pk_mov_b32 v[58:59], 0, 0
	v_pk_mov_b32 v[60:61], 0, 0
	v_pk_mov_b32 v[62:63], 0, 0
	v_pk_mov_b32 v[64:65], 0, 0
	v_pk_mov_b32 v[66:67], 0, 0
	v_pk_mov_b32 v[68:69], 0, 0
	v_pk_mov_b32 v[70:71], 0, 0
	v_pk_mov_b32 v[80:81], 0, 0
	v_pk_mov_b32 v[82:83], 0, 0
	v_pk_mov_b32 v[84:85], 0, 0
	v_pk_mov_b32 v[86:87], 0, 0
	v_pk_mov_b32 v[96:97], 0, 0
	v_pk_mov_b32 v[98:99], 0, 0
	v_pk_mov_b32 v[100:101], 0, 0
	v_pk_mov_b32 v[102:103], 0, 0
	v_pk_mov_b32 v[112:113], 0, 0
	v_pk_mov_b32 v[114:115], 0, 0
	v_pk_mov_b32 v[116:117], 0, 0
	v_pk_mov_b32 v[118:119], 0, 0
	v_pk_mov_b32 v[72:73], 0, 0
	v_pk_mov_b32 v[74:75], 0, 0
	v_pk_mov_b32 v[76:77], 0, 0
	v_pk_mov_b32 v[78:79], 0, 0
	v_pk_mov_b32 v[88:89], 0, 0
	v_pk_mov_b32 v[90:91], 0, 0
	v_pk_mov_b32 v[92:93], 0, 0
	v_pk_mov_b32 v[94:95], 0, 0
	v_pk_mov_b32 v[104:105], 0, 0
	v_pk_mov_b32 v[106:107], 0, 0
	v_pk_mov_b32 v[108:109], 0, 0
	v_pk_mov_b32 v[110:111], 0, 0
	v_pk_mov_b32 v[120:121], 0, 0
	v_pk_mov_b32 v[122:123], 0, 0
	v_pk_mov_b32 v[124:125], 0, 0
	v_pk_mov_b32 v[126:127], 0, 0
.LBB0_967:
	ds_read_b128 v[144:147], v151
	ds_read_b128 v[154:157], v151 offset:1024
	ds_read_b128 v[158:161], v151 offset:2048
	ds_read_b128 v[162:165], v151 offset:3072
	ds_read_b128 v[166:169], v152
	ds_read_b128 v[170:173], v152 offset:1024
	ds_read_b128 v[174:177], v152 offset:2048
	ds_read_b128 v[178:181], v152 offset:3072
	s_add_u32 s40, s38, 0xfffe0080
	s_addc_u32 s41, s39, -1
	s_cmp_eq_u32 s72, 4
	s_cselect_b32 s43, s5, s41
	s_cselect_b32 s42, s27, s40
	s_cselect_b32 s41, s23, s71
	s_cselect_b32 s40, s37, s70
	v_lshl_add_u64 v[148:149], s[38:39], 0, v[138:139]
	s_add_i32 m0, s51, 0xc000
	ds_read_b128 v[182:185], v153
	ds_read_b128 v[186:189], v153 offset:1024
	ds_read_b128 v[190:193], v153 offset:2048
	ds_read_b128 v[194:197], v153 offset:3072
	ds_read_b128 v[198:201], v153 offset:4096
	ds_read_b128 v[202:205], v153 offset:5120
	ds_read_b128 v[206:209], v153 offset:6144
	ds_read_b128 v[210:213], v153 offset:7168
	global_load_lds_dwordx4 v[148:149], off
	v_lshl_add_u64 v[148:149], s[38:39], 0, v[140:141]
	s_add_i32 m0, s51, 0xe000
	s_nop 0
	global_load_lds_dwordx4 v[148:149], off
	s_waitcnt vmcnt(8)
	s_waitcnt lgkmcnt(0)
	s_barrier
	s_waitcnt lgkmcnt(0)
	v_mfma_f32_16x16x32_bf16 v[124:127], v[144:147], v[182:185], v[124:127]
	v_mfma_f32_16x16x32_bf16 v[120:123], v[158:161], v[182:185], v[120:123]
	v_mfma_f32_16x16x32_bf16 v[108:111], v[144:147], v[190:193], v[108:111]
	v_mfma_f32_16x16x32_bf16 v[104:107], v[158:161], v[190:193], v[104:107]
	v_mfma_f32_16x16x32_bf16 v[92:95], v[144:147], v[198:201], v[92:95]
	v_mfma_f32_16x16x32_bf16 v[88:91], v[158:161], v[198:201], v[88:91]
	v_mfma_f32_16x16x32_bf16 v[76:79], v[144:147], v[206:209], v[76:79]
	v_mfma_f32_16x16x32_bf16 v[72:75], v[158:161], v[206:209], v[72:75]
	v_mfma_f32_16x16x32_bf16 v[124:127], v[154:157], v[186:189], v[124:127]
	v_mfma_f32_16x16x32_bf16 v[120:123], v[162:165], v[186:189], v[120:123]
	v_mfma_f32_16x16x32_bf16 v[108:111], v[154:157], v[194:197], v[108:111]
	v_mfma_f32_16x16x32_bf16 v[104:107], v[162:165], v[194:197], v[104:107]
	v_mfma_f32_16x16x32_bf16 v[92:95], v[154:157], v[202:205], v[92:95]
	v_mfma_f32_16x16x32_bf16 v[88:91], v[162:165], v[202:205], v[88:91]
	v_mfma_f32_16x16x32_bf16 v[76:79], v[154:157], v[210:213], v[76:79]
	v_mfma_f32_16x16x32_bf16 v[72:75], v[162:165], v[210:213], v[72:75]
	v_mfma_f32_16x16x32_bf16 v[116:119], v[166:169], v[182:185], v[116:119]
	v_mfma_f32_16x16x32_bf16 v[112:115], v[174:177], v[182:185], v[112:115]
	v_mfma_f32_16x16x32_bf16 v[100:103], v[166:169], v[190:193], v[100:103]
	v_mfma_f32_16x16x32_bf16 v[96:99], v[174:177], v[190:193], v[96:99]
	v_mfma_f32_16x16x32_bf16 v[84:87], v[166:169], v[198:201], v[84:87]
	v_mfma_f32_16x16x32_bf16 v[80:83], v[174:177], v[198:201], v[80:83]
	v_mfma_f32_16x16x32_bf16 v[68:71], v[166:169], v[206:209], v[68:71]
	v_mfma_f32_16x16x32_bf16 v[64:67], v[174:177], v[206:209], v[64:67]
	v_mfma_f32_16x16x32_bf16 v[116:119], v[170:173], v[186:189], v[116:119]
	v_mfma_f32_16x16x32_bf16 v[112:115], v[178:181], v[186:189], v[112:115]
	v_mfma_f32_16x16x32_bf16 v[100:103], v[170:173], v[194:197], v[100:103]
	v_mfma_f32_16x16x32_bf16 v[96:99], v[178:181], v[194:197], v[96:99]
	v_mfma_f32_16x16x32_bf16 v[84:87], v[170:173], v[202:205], v[84:87]
	v_mfma_f32_16x16x32_bf16 v[80:83], v[178:181], v[202:205], v[80:83]
	v_mfma_f32_16x16x32_bf16 v[68:71], v[170:173], v[210:213], v[68:71]
	v_mfma_f32_16x16x32_bf16 v[64:67], v[178:181], v[210:213], v[64:67]
	s_barrier
; #define PG8_LDA(dst, b, h) do { _Pragma("unroll") for (int m = 0; m < 4; ++m) _Pragma("unroll") for (int k = 0; k < 2; ++k) dst[m][k] = *(const PG8_LAS bf16x8*)(lds + PG8_SA(b, h) + aoff + m * 2048 + k * 1024); } while (0)
; #define PG8_LDB(dst, b, h) do { _Pragma("unroll") for (int n = 0; n < 2; ++n) _Pragma("unroll") for (int k = 0; k < 2; ++k) dst[n][k] = *(const PG8_LAS bf16x8*)(lds + PG8_SB(b, h) + boff + n * 2048 + k * 1024); } while (0)
; #define PG8_WAIT_V(n) asm volatile("s_waitcnt vmcnt(" #n ")" ::: "memory")
; #define PG8_WAIT_L(n) asm volatile("s_waitcnt lgkmcnt(" #n ")" ::: "memory")
; #define PG8_BAR __builtin_amdgcn_s_barrier()
; #define PG8_SCHED __builtin_amdgcn_sched_barrier(0)
; template <class Epi, class Sched, bool ALIGN_EPI = false, bool SP2 = false, bool F8 = false, bool I8 = false, bool PF = false>
; __device__ __forceinline__ void gemm_phase(PG8_LAS unsigned char* lds, const Gemm g, const Sched& S, const Epi& E, const int wave_) {
;     ...
;             PG8_LDA(At, 0, 1); PG8_STAGE(PG8_SB(0, 0), b2, voffB); PG8_STAGE(PG8_SB(0, 1), b2 + hstep, voffB); PG8_STAGE(PG8_SA(0, 0), a2, voffA);
;             PG8_WAIT_V(8); PG8_WAIT_L(0); PG8_BAR; PG8_MMA(1, 0, At, B0); PG8_MMA(1, 1, At, B1); PG8_BAR; PG8_SCHED;
;             PG8_LDB(B0, 1, 0); PG8_LDB(B1, 1, 1); PG8_SCHED; PG8_LDA(At, 1, 0); PG8_STAGE(PG8_SA(0, 1), a2 + hstep, voffA);
;             PG8_WAIT_V(8); PG8_WAIT_L(0); PG8_BAR; PG8_MMA(0, 0, At, B0); PG8_MMA(0, 1, At, B1); PG8_BAR; PG8_SCHED;
	s_add_i32 s73, s67, s48
	v_lshl_add_u64 v[148:149], s[40:41], 0, v[130:131]
	s_mov_b32 m0, s73
	ds_read_b128 v[182:185], v153 offset:16384
	ds_read_b128 v[186:189], v153 offset:17408
	ds_read_b128 v[190:193], v153 offset:18432
	ds_read_b128 v[194:197], v153 offset:19456
	ds_read_b128 v[198:201], v153 offset:20480
	ds_read_b128 v[202:205], v153 offset:21504
	ds_read_b128 v[206:209], v153 offset:22528
	ds_read_b128 v[210:213], v153 offset:23552
	global_load_lds_dwordx4 v[148:149], off
	s_add_i32 m0, s73, 0x2000
	s_add_u32 s74, s40, 0x20000
	v_lshl_add_u64 v[214:215], s[40:41], 0, v[134:135]
	s_addc_u32 s75, s41, 0
	s_add_i32 s73, s68, s48
	global_load_lds_dwordx4 v[214:215], off
	v_lshl_add_u64 v[216:217], s[74:75], 0, v[130:131]
	s_mov_b32 m0, s73
	v_lshl_add_u64 v[218:219], s[42:43], 0, v[132:133]
	global_load_lds_dwordx4 v[216:217], off
	v_lshl_add_u64 v[216:217], s[74:75], 0, v[134:135]
	s_add_i32 m0, s73, 0x2000
	s_nop 0
	global_load_lds_dwordx4 v[216:217], off
	v_lshl_add_u64 v[216:217], s[42:43], 0, v[128:129]
	s_mov_b32 m0, s51
	s_nop 0
	global_load_lds_dwordx4 v[216:217], off
	s_mov_b32 m0, s52
	s_nop 0
	global_load_lds_dwordx4 v[218:219], off
	s_waitcnt vmcnt(8)
	s_waitcnt lgkmcnt(0)
	s_barrier
	s_waitcnt lgkmcnt(0)
	v_mfma_f32_16x16x32_bf16 v[60:63], v[144:147], v[182:185], v[60:63]
	v_mfma_f32_16x16x32_bf16 v[56:59], v[158:161], v[182:185], v[56:59]
	v_mfma_f32_16x16x32_bf16 v[44:47], v[144:147], v[190:193], v[44:47]
	v_mfma_f32_16x16x32_bf16 v[40:43], v[158:161], v[190:193], v[40:43]
	v_mfma_f32_16x16x32_bf16 v[28:31], v[144:147], v[198:201], v[28:31]
	v_mfma_f32_16x16x32_bf16 v[24:27], v[158:161], v[198:201], v[24:27]
	v_mfma_f32_16x16x32_bf16 v[12:15], v[144:147], v[206:209], v[12:15]
	v_mfma_f32_16x16x32_bf16 v[8:11], v[158:161], v[206:209], v[8:11]
	v_mfma_f32_16x16x32_bf16 v[60:63], v[154:157], v[186:189], v[60:63]
	v_mfma_f32_16x16x32_bf16 v[56:59], v[162:165], v[186:189], v[56:59]
	v_mfma_f32_16x16x32_bf16 v[44:47], v[154:157], v[194:197], v[44:47]
	v_mfma_f32_16x16x32_bf16 v[40:43], v[162:165], v[194:197], v[40:43]
	v_mfma_f32_16x16x32_bf16 v[28:31], v[154:157], v[202:205], v[28:31]
	v_mfma_f32_16x16x32_bf16 v[24:27], v[162:165], v[202:205], v[24:27]
	v_mfma_f32_16x16x32_bf16 v[12:15], v[154:157], v[210:213], v[12:15]
	v_mfma_f32_16x16x32_bf16 v[8:11], v[162:165], v[210:213], v[8:11]
	v_mfma_f32_16x16x32_bf16 v[52:55], v[166:169], v[182:185], v[52:55]
	v_mfma_f32_16x16x32_bf16 v[48:51], v[174:177], v[182:185], v[48:51]
	v_mfma_f32_16x16x32_bf16 v[36:39], v[166:169], v[190:193], v[36:39]
	v_mfma_f32_16x16x32_bf16 v[32:35], v[174:177], v[190:193], v[32:35]
	v_mfma_f32_16x16x32_bf16 v[20:23], v[166:169], v[198:201], v[20:23]
	v_mfma_f32_16x16x32_bf16 v[16:19], v[174:177], v[198:201], v[16:19]
	v_mfma_f32_16x16x32_bf16 v[4:7], v[166:169], v[206:209], v[4:7]
	v_mfma_f32_16x16x32_bf16 v[0:3], v[174:177], v[206:209], v[0:3]
	v_mfma_f32_16x16x32_bf16 v[52:55], v[170:173], v[186:189], v[52:55]
	v_mfma_f32_16x16x32_bf16 v[48:51], v[178:181], v[186:189], v[48:51]
	v_mfma_f32_16x16x32_bf16 v[36:39], v[170:173], v[194:197], v[36:39]
	v_mfma_f32_16x16x32_bf16 v[32:35], v[178:181], v[194:197], v[32:35]
	v_mfma_f32_16x16x32_bf16 v[20:23], v[170:173], v[202:205], v[20:23]
	v_mfma_f32_16x16x32_bf16 v[16:19], v[178:181], v[202:205], v[16:19]
	v_mfma_f32_16x16x32_bf16 v[4:7], v[170:173], v[210:213], v[4:7]
	v_mfma_f32_16x16x32_bf16 v[0:3], v[178:181], v[210:213], v[0:3]
	s_barrier
	s_add_i32 s73, 0, 0x18000
	v_add_u32_e32 v136, s73, v150
	s_add_i32 s74, 0, 0x1c000
	ds_read_b128 v[144:147], v136
	ds_read_b128 v[154:157], v136 offset:1024
	ds_read_b128 v[158:161], v136 offset:2048
	ds_read_b128 v[162:165], v136 offset:3072
	v_add_u32_e32 v136, s74, v150
	ds_read_b128 v[166:169], v136
	ds_read_b128 v[170:173], v136 offset:1024
	ds_read_b128 v[174:177], v136 offset:2048
	ds_read_b128 v[178:181], v136 offset:3072
	s_add_u32 s42, s42, 0x20000
	s_addc_u32 s43, s43, 0
	s_mov_b32 m0, s53
	v_lshl_add_u64 v[220:221], s[42:43], 0, v[128:129]
	ds_read_b128 v[182:185], v153 offset:32768
	ds_read_b128 v[186:189], v153 offset:33792
	ds_read_b128 v[190:193], v153 offset:34816
	ds_read_b128 v[194:197], v153 offset:35840
	ds_read_b128 v[198:201], v153 offset:36864
	ds_read_b128 v[202:205], v153 offset:37888
	ds_read_b128 v[206:209], v153 offset:38912
	ds_read_b128 v[210:213], v153 offset:39936
	global_load_lds_dwordx4 v[220:221], off
	v_lshl_add_u64 v[220:221], s[42:43], 0, v[132:133]
	s_mov_b32 m0, s54
	s_nop 0
	global_load_lds_dwordx4 v[220:221], off
	s_waitcnt vmcnt(8)
	s_waitcnt lgkmcnt(0)
	s_barrier
; #define PG8_LDA(dst, b, h) do { _Pragma("unroll") for (int m = 0; m < 4; ++m) _Pragma("unroll") for (int k = 0; k < 2; ++k) dst[m][k] = *(const PG8_LAS bf16x8*)(lds + PG8_SA(b, h) + aoff + m * 2048 + k * 1024); } while (0)
; #define PG8_WAIT_V(n) asm volatile("s_waitcnt vmcnt(" #n ")" ::: "memory")
; #define PG8_WAIT_L(n) asm volatile("s_waitcnt lgkmcnt(" #n ")" ::: "memory")
; #define PG8_BAR __builtin_amdgcn_s_barrier()
; #define PG8_SCHED __builtin_amdgcn_sched_barrier(0)
; template <class Epi, class Sched, bool ALIGN_EPI = false, bool SP2 = false, bool F8 = false, bool I8 = false, bool PF = false>
; __device__ __forceinline__ void gemm_phase(PG8_LAS unsigned char* lds, const Gemm g, const Sched& S, const Epi& E, const int wave_) {
;     ...
;             PG8_WAIT_V(8); PG8_WAIT_L(0); PG8_BAR; PG8_MMA(0, 0, At, B0); PG8_MMA(0, 1, At, B1); PG8_BAR; PG8_SCHED;
;             PG8_LDA(At, 1, 1); PG8_STAGE(PG8_SB(1, 0), b3, voffB); PG8_STAGE(PG8_SB(1, 1), b3 + hstep, voffB); PG8_STAGE(PG8_SA(1, 0), a3, voffA);
;             PG8_WAIT_V(8); PG8_WAIT_L(0); PG8_BAR; PG8_MMA(1, 0, At, B0); PG8_MMA(1, 1, At, B1); PG8_BAR; PG8_SCHED;
	s_waitcnt lgkmcnt(0)
	v_mfma_f32_16x16x32_bf16 v[124:127], v[144:147], v[182:185], v[124:127]
	v_mfma_f32_16x16x32_bf16 v[120:123], v[158:161], v[182:185], v[120:123]
	v_mfma_f32_16x16x32_bf16 v[108:111], v[144:147], v[190:193], v[108:111]
	v_mfma_f32_16x16x32_bf16 v[104:107], v[158:161], v[190:193], v[104:107]
	v_mfma_f32_16x16x32_bf16 v[92:95], v[144:147], v[198:201], v[92:95]
	v_mfma_f32_16x16x32_bf16 v[88:91], v[158:161], v[198:201], v[88:91]
	v_mfma_f32_16x16x32_bf16 v[76:79], v[144:147], v[206:209], v[76:79]
	v_mfma_f32_16x16x32_bf16 v[72:75], v[158:161], v[206:209], v[72:75]
	v_mfma_f32_16x16x32_bf16 v[124:127], v[154:157], v[186:189], v[124:127]
	v_mfma_f32_16x16x32_bf16 v[120:123], v[162:165], v[186:189], v[120:123]
	v_mfma_f32_16x16x32_bf16 v[108:111], v[154:157], v[194:197], v[108:111]
	v_mfma_f32_16x16x32_bf16 v[104:107], v[162:165], v[194:197], v[104:107]
	v_mfma_f32_16x16x32_bf16 v[92:95], v[154:157], v[202:205], v[92:95]
	v_mfma_f32_16x16x32_bf16 v[88:91], v[162:165], v[202:205], v[88:91]
	v_mfma_f32_16x16x32_bf16 v[76:79], v[154:157], v[210:213], v[76:79]
	v_mfma_f32_16x16x32_bf16 v[72:75], v[162:165], v[210:213], v[72:75]
	v_mfma_f32_16x16x32_bf16 v[116:119], v[166:169], v[182:185], v[116:119]
	v_mfma_f32_16x16x32_bf16 v[112:115], v[174:177], v[182:185], v[112:115]
	v_mfma_f32_16x16x32_bf16 v[100:103], v[166:169], v[190:193], v[100:103]
	v_mfma_f32_16x16x32_bf16 v[96:99], v[174:177], v[190:193], v[96:99]
	v_mfma_f32_16x16x32_bf16 v[84:87], v[166:169], v[198:201], v[84:87]
	v_mfma_f32_16x16x32_bf16 v[80:83], v[174:177], v[198:201], v[80:83]
	v_mfma_f32_16x16x32_bf16 v[68:71], v[166:169], v[206:209], v[68:71]
	v_mfma_f32_16x16x32_bf16 v[64:67], v[174:177], v[206:209], v[64:67]
	v_mfma_f32_16x16x32_bf16 v[116:119], v[170:173], v[186:189], v[116:119]
	v_mfma_f32_16x16x32_bf16 v[112:115], v[178:181], v[186:189], v[112:115]
	v_mfma_f32_16x16x32_bf16 v[100:103], v[170:173], v[194:197], v[100:103]
	v_mfma_f32_16x16x32_bf16 v[96:99], v[178:181], v[194:197], v[96:99]
	v_mfma_f32_16x16x32_bf16 v[84:87], v[170:173], v[202:205], v[84:87]
	v_mfma_f32_16x16x32_bf16 v[80:83], v[178:181], v[202:205], v[80:83]
	v_mfma_f32_16x16x32_bf16 v[68:71], v[170:173], v[210:213], v[68:71]
	v_mfma_f32_16x16x32_bf16 v[64:67], v[178:181], v[210:213], v[64:67]
	s_barrier
	s_add_i32 s42, s73, s48
	v_lshl_add_u64 v[148:149], v[148:149], 0, s[16:17]
	s_mov_b32 m0, s42
	ds_read_b128 v[182:185], v153 offset:49152
	ds_read_b128 v[186:189], v153 offset:50176
	ds_read_b128 v[190:193], v153 offset:51200
	ds_read_b128 v[194:197], v153 offset:52224
	ds_read_b128 v[198:201], v153 offset:53248
	ds_read_b128 v[202:205], v153 offset:54272
	ds_read_b128 v[206:209], v153 offset:55296
	ds_read_b128 v[210:213], v153 offset:56320
	global_load_lds_dwordx4 v[148:149], off
	s_add_i32 m0, s42, 0x2000
	s_add_u32 s40, s40, 0x20080
	v_lshl_add_u64 v[148:149], v[214:215], 0, s[16:17]
	s_addc_u32 s41, s41, 0
	s_add_i32 s42, s74, s48
	global_load_lds_dwordx4 v[148:149], off
	v_lshl_add_u64 v[148:149], s[40:41], 0, v[130:131]
	s_mov_b32 m0, s42
	s_nop 0
	global_load_lds_dwordx4 v[148:149], off
	v_lshl_add_u64 v[148:149], s[40:41], 0, v[134:135]
	s_add_i32 m0, s42, 0x2000
	s_nop 0
	global_load_lds_dwordx4 v[148:149], off
	v_lshl_add_u64 v[148:149], v[216:217], 0, s[16:17]
	s_mov_b32 m0, s62
	s_nop 0
	global_load_lds_dwordx4 v[148:149], off
	v_lshl_add_u64 v[148:149], v[218:219], 0, s[16:17]
	s_mov_b32 m0, s63
	s_nop 0
	global_load_lds_dwordx4 v[148:149], off
	s_waitcnt vmcnt(8)
	s_waitcnt lgkmcnt(0)
	s_barrier
	s_waitcnt lgkmcnt(0)
	v_mfma_f32_16x16x32_bf16 v[60:63], v[144:147], v[182:185], v[60:63]
	v_mfma_f32_16x16x32_bf16 v[56:59], v[158:161], v[182:185], v[56:59]
	v_mfma_f32_16x16x32_bf16 v[44:47], v[144:147], v[190:193], v[44:47]
	v_mfma_f32_16x16x32_bf16 v[40:43], v[158:161], v[190:193], v[40:43]
	v_mfma_f32_16x16x32_bf16 v[28:31], v[144:147], v[198:201], v[28:31]
	v_mfma_f32_16x16x32_bf16 v[24:27], v[158:161], v[198:201], v[24:27]
	v_mfma_f32_16x16x32_bf16 v[12:15], v[144:147], v[206:209], v[12:15]
	v_mfma_f32_16x16x32_bf16 v[8:11], v[158:161], v[206:209], v[8:11]
	v_mfma_f32_16x16x32_bf16 v[60:63], v[154:157], v[186:189], v[60:63]
	v_mfma_f32_16x16x32_bf16 v[56:59], v[162:165], v[186:189], v[56:59]
	v_mfma_f32_16x16x32_bf16 v[44:47], v[154:157], v[194:197], v[44:47]
	v_mfma_f32_16x16x32_bf16 v[40:43], v[162:165], v[194:197], v[40:43]
	v_mfma_f32_16x16x32_bf16 v[28:31], v[154:157], v[202:205], v[28:31]
	v_mfma_f32_16x16x32_bf16 v[24:27], v[162:165], v[202:205], v[24:27]
	v_mfma_f32_16x16x32_bf16 v[12:15], v[154:157], v[210:213], v[12:15]
	v_mfma_f32_16x16x32_bf16 v[8:11], v[162:165], v[210:213], v[8:11]
	v_mfma_f32_16x16x32_bf16 v[52:55], v[166:169], v[182:185], v[52:55]
	v_mfma_f32_16x16x32_bf16 v[48:51], v[174:177], v[182:185], v[48:51]
	v_mfma_f32_16x16x32_bf16 v[36:39], v[166:169], v[190:193], v[36:39]
	v_mfma_f32_16x16x32_bf16 v[32:35], v[174:177], v[190:193], v[32:35]
	v_mfma_f32_16x16x32_bf16 v[20:23], v[166:169], v[198:201], v[20:23]
	v_mfma_f32_16x16x32_bf16 v[16:19], v[174:177], v[198:201], v[16:19]
	v_mfma_f32_16x16x32_bf16 v[4:7], v[166:169], v[206:209], v[4:7]
	v_mfma_f32_16x16x32_bf16 v[0:3], v[174:177], v[206:209], v[0:3]
	v_mfma_f32_16x16x32_bf16 v[52:55], v[170:173], v[186:189], v[52:55]
	v_mfma_f32_16x16x32_bf16 v[48:51], v[178:181], v[186:189], v[48:51]
	v_mfma_f32_16x16x32_bf16 v[36:39], v[170:173], v[194:197], v[36:39]
	v_mfma_f32_16x16x32_bf16 v[32:35], v[178:181], v[194:197], v[32:35]
	v_mfma_f32_16x16x32_bf16 v[20:23], v[170:173], v[202:205], v[20:23]
	v_mfma_f32_16x16x32_bf16 v[16:19], v[178:181], v[202:205], v[16:19]
	v_mfma_f32_16x16x32_bf16 v[4:7], v[170:173], v[210:213], v[4:7]
	v_mfma_f32_16x16x32_bf16 v[0:3], v[178:181], v[210:213], v[0:3]
	s_add_i32 s72, s72, 2
	s_add_u32 s38, s38, 0x100
	s_addc_u32 s39, s39, 0
	s_add_u32 s70, s70, 0x100
	s_addc_u32 s71, s71, 0
	s_cmp_gt_u32 s72, 5
	s_barrier
	s_cbranch_scc0 .LBB0_967
	s_and_b64 vcc, exec, s[18:19]
	s_cbranch_vccz .LBB0_970
	s_barrier

; template <class Epi, class Sched, bool ALIGN_EPI = false, bool SP2 = false, bool F8 = false, bool I8 = false, bool PF = false>
; __device__ __forceinline__ void gemm_phase(PG8_LAS unsigned char* lds, const Gemm g, const Sched& S, const Epi& E, const int wave_) {
;     ...
;         const char* nA = has_next ? (const char*)g.A + (size_t)nxt.pm * tstep : cA; const char* nB = has_next ? (const char*)g.Bt + (size_t)nxt.pb * tstep : cB;
;         for (int t = 0; t < nt; t += 2) {
;             const bool last = (t == nt - 2);
;             const char* a1 = cA + (size_t)(t + 1) * kstep;
;             const char* a2 = last ? nA : cA + (size_t)(t + 2) * kstep; const char* b2 = last ? nB : cB + (size_t)(t + 2) * kstep;
;             const char* a3 = a2 + kstep; const char* b3 = b2 + kstep;
;             if (last && has_next) S.a_ready(nxt);
;             if constexpr (PF) {
;             PG8_STAGE(wr ? PG8_SA(0, 0) : PG8_SA(1, 1), wr ? a2 : a1 + hstep, voffA); PG8_STAGE(wr ? PG8_SB(0, 0) : PG8_SB(1, 1), wr ? b2 : cB + (size_t)(t + 1) * kstep + hstep, voffB);
;             PG8_WAIT_V(8); PG8_BAR;
;             PG8_X1(0); __builtin_amdgcn_s_waitcnt(0xC07F); PG8_BAR; PG8_SCHED;
;             PG8_STAGE(wr ? PG8_SA(0, 1) : PG8_SA(0, 0), wr ? a2 + hstep : a2, voffA); PG8_STAGE(wr ? PG8_SB(0, 1) : PG8_SB(0, 0), wr ? b2 + hstep : b2, voffB);
;             PG8_WAIT_V(8); PG8_BAR;
;             PG8_X2(0); __builtin_amdgcn_s_waitcnt(0xC07F); PG8_BAR; PG8_SCHED;
;             PG8_STAGE(wr ? PG8_SA(1, 0) : PG8_SA(0, 1), wr ? a3 : a2 + hstep, voffA); PG8_STAGE(wr ? PG8_SB(1, 0) : PG8_SB(0, 1), wr ? b3 : b2 + hstep, voffB);
;             PG8_WAIT_V(8); PG8_BAR;
;             PG8_X1(1); __builtin_amdgcn_s_waitcnt(0xC07F); PG8_BAR; PG8_SCHED;
;             PG8_STAGE(wr ? PG8_SA(1, 1) : PG8_SA(1, 0), wr ? a3 + hstep : a3, voffA); PG8_STAGE(wr ? PG8_SB(1, 1) : PG8_SB(1, 0), wr ? b3 + hstep : b3, voffB);
;             PG8_WAIT_V(8); PG8_BAR;
;             PG8_X2(1); __builtin_amdgcn_s_waitcnt(0xC07F); PG8_BAR; PG8_SCHED;
;             } else
;             if constexpr (SP2) {
;     ...
; #pragma unroll
;         for (int a = 0; a < 2; ++a)
; #pragma unroll
;             for (int b = 0; b < 2; ++b)
; #pragma unroll
;                 for (int m = 0; m < 4; ++m)
; #pragma unroll
;                     for (int n = 0; n < 2; ++n) acc[a][b][m][n] = (f32x4){0.f, 0.f, 0.f, 0.f};
.LBB0_1303:
	s_ashr_i32 s21, s20, 31
	s_lshl_b64 s[24:25], s[20:21], 19
	s_add_u32 s24, s48, s24
	s_addc_u32 s25, s49, s25
	s_and_b64 s[26:27], s[22:23], exec
	s_cselect_b32 s21, s25, s31
	s_cselect_b32 s62, s24, s30
	s_ashr_i32 s19, s18, 31
	s_lshl_b64 s[26:27], s[18:19], 19
	s_add_u32 s26, s38, s26
	s_addc_u32 s27, s39, s27
	s_and_b64 s[36:37], s[22:23], exec
	s_cselect_b32 s19, s27, s35
	s_cselect_b32 s63, s26, s34
	s_add_u32 s30, s30, 0x40080
	s_addc_u32 s31, s31, 0
	s_add_u32 s64, s34, 0x100
	v_mov_b32_e32 v0, 0
	s_addc_u32 s65, s35, 0
	s_mov_b32 s66, -2
	v_mov_b32_e32 v1, v0
	v_pk_mov_b32 v[2:3], 0, 0
	v_pk_mov_b32 v[4:5], 0, 0
	v_pk_mov_b32 v[6:7], 0, 0
	v_pk_mov_b32 v[16:17], 0, 0
	v_pk_mov_b32 v[18:19], 0, 0
	v_pk_mov_b32 v[20:21], 0, 0
	v_pk_mov_b32 v[22:23], 0, 0
	v_pk_mov_b32 v[32:33], 0, 0
	v_pk_mov_b32 v[34:35], 0, 0
	v_pk_mov_b32 v[36:37], 0, 0
	v_pk_mov_b32 v[38:39], 0, 0
	v_pk_mov_b32 v[48:49], 0, 0
	v_pk_mov_b32 v[50:51], 0, 0
	v_pk_mov_b32 v[52:53], 0, 0
	v_pk_mov_b32 v[54:55], 0, 0
	v_pk_mov_b32 v[8:9], 0, 0
	v_pk_mov_b32 v[10:11], 0, 0
	v_pk_mov_b32 v[12:13], 0, 0
	v_pk_mov_b32 v[14:15], 0, 0
	v_pk_mov_b32 v[24:25], 0, 0
	v_pk_mov_b32 v[26:27], 0, 0
	v_pk_mov_b32 v[28:29], 0, 0
	v_pk_mov_b32 v[30:31], 0, 0
	v_pk_mov_b32 v[40:41], 0, 0
	v_pk_mov_b32 v[42:43], 0, 0
	v_pk_mov_b32 v[44:45], 0, 0
	v_pk_mov_b32 v[46:47], 0, 0
	v_pk_mov_b32 v[56:57], 0, 0
	v_pk_mov_b32 v[58:59], 0, 0
	v_pk_mov_b32 v[60:61], 0, 0
	v_pk_mov_b32 v[62:63], 0, 0
	v_pk_mov_b32 v[64:65], 0, 0
	v_pk_mov_b32 v[66:67], 0, 0
	v_pk_mov_b32 v[68:69], 0, 0
	v_pk_mov_b32 v[70:71], 0, 0
	v_pk_mov_b32 v[80:81], 0, 0
	v_pk_mov_b32 v[82:83], 0, 0
	v_pk_mov_b32 v[84:85], 0, 0
	v_pk_mov_b32 v[86:87], 0, 0
	v_pk_mov_b32 v[96:97], 0, 0
	v_pk_mov_b32 v[98:99], 0, 0
	v_pk_mov_b32 v[100:101], 0, 0
	v_pk_mov_b32 v[102:103], 0, 0
	v_pk_mov_b32 v[112:113], 0, 0
	v_pk_mov_b32 v[114:115], 0, 0
	v_pk_mov_b32 v[116:117], 0, 0
	v_pk_mov_b32 v[118:119], 0, 0
	v_pk_mov_b32 v[72:73], 0, 0
	v_pk_mov_b32 v[74:75], 0, 0
	v_pk_mov_b32 v[76:77], 0, 0
	v_pk_mov_b32 v[78:79], 0, 0
	v_pk_mov_b32 v[88:89], 0, 0
	v_pk_mov_b32 v[90:91], 0, 0
	v_pk_mov_b32 v[92:93], 0, 0
	v_pk_mov_b32 v[94:95], 0, 0
	v_pk_mov_b32 v[104:105], 0, 0
	v_pk_mov_b32 v[106:107], 0, 0
	v_pk_mov_b32 v[108:109], 0, 0
	v_pk_mov_b32 v[110:111], 0, 0
	v_pk_mov_b32 v[120:121], 0, 0
	v_pk_mov_b32 v[122:123], 0, 0
	v_pk_mov_b32 v[124:125], 0, 0
	v_pk_mov_b32 v[126:127], 0, 0
.LBB0_1304:
	ds_read_b128 v[128:131], v209
	ds_read_b128 v[132:135], v209 offset:1024
	ds_read_b128 v[136:139], v209 offset:2048
	ds_read_b128 v[140:143], v209 offset:3072
	ds_read_b128 v[144:147], v210
	ds_read_b128 v[148:151], v210 offset:1024
	ds_read_b128 v[152:155], v210 offset:2048
	ds_read_b128 v[156:159], v210 offset:3072
	s_add_u32 s34, s30, 0xfffc0080
	s_addc_u32 s35, s31, -1
	s_cmp_eq_u32 s66, 12
	s_cselect_b32 s37, s21, s35
	s_cselect_b32 s36, s62, s34
	s_cselect_b32 s35, s19, s65
	s_cselect_b32 s34, s63, s64
	v_lshl_add_u64 v[206:207], s[30:31], 0, v[188:189]
	s_add_i32 m0, s29, 0xc000
	ds_read_b128 v[160:163], v211
	ds_read_b128 v[164:167], v211 offset:1024
	ds_read_b128 v[168:171], v211 offset:2048
	ds_read_b128 v[172:175], v211 offset:3072
	ds_read_b128 v[176:179], v211 offset:4096
	ds_read_b128 v[194:197], v211 offset:5120
	ds_read_b128 v[198:201], v211 offset:6144
	ds_read_b128 v[202:205], v211 offset:7168
	global_load_lds_dwordx4 v[206:207], off
	v_lshl_add_u64 v[206:207], s[30:31], 0, v[190:191]
	s_add_i32 m0, s29, 0xe000
	s_nop 0
	global_load_lds_dwordx4 v[206:207], off
	s_waitcnt vmcnt(8)
	s_waitcnt lgkmcnt(0)
	s_barrier
	s_waitcnt lgkmcnt(0)
	v_mfma_f32_16x16x32_bf16 v[124:127], v[128:131], v[160:163], v[124:127]
	v_mfma_f32_16x16x32_bf16 v[120:123], v[136:139], v[160:163], v[120:123]
	v_mfma_f32_16x16x32_bf16 v[108:111], v[128:131], v[168:171], v[108:111]
	v_mfma_f32_16x16x32_bf16 v[104:107], v[136:139], v[168:171], v[104:107]
	v_mfma_f32_16x16x32_bf16 v[92:95], v[128:131], v[176:179], v[92:95]
	v_mfma_f32_16x16x32_bf16 v[88:91], v[136:139], v[176:179], v[88:91]
	v_mfma_f32_16x16x32_bf16 v[76:79], v[128:131], v[198:201], v[76:79]
	v_mfma_f32_16x16x32_bf16 v[72:75], v[136:139], v[198:201], v[72:75]
	v_mfma_f32_16x16x32_bf16 v[124:127], v[132:135], v[164:167], v[124:127]
	v_mfma_f32_16x16x32_bf16 v[120:123], v[140:143], v[164:167], v[120:123]
	v_mfma_f32_16x16x32_bf16 v[108:111], v[132:135], v[172:175], v[108:111]
	v_mfma_f32_16x16x32_bf16 v[104:107], v[140:143], v[172:175], v[104:107]
	v_mfma_f32_16x16x32_bf16 v[92:95], v[132:135], v[194:197], v[92:95]
	v_mfma_f32_16x16x32_bf16 v[88:91], v[140:143], v[194:197], v[88:91]
	v_mfma_f32_16x16x32_bf16 v[76:79], v[132:135], v[202:205], v[76:79]
	v_mfma_f32_16x16x32_bf16 v[72:75], v[140:143], v[202:205], v[72:75]
	v_mfma_f32_16x16x32_bf16 v[116:119], v[144:147], v[160:163], v[116:119]
	v_mfma_f32_16x16x32_bf16 v[112:115], v[152:155], v[160:163], v[112:115]
	v_mfma_f32_16x16x32_bf16 v[100:103], v[144:147], v[168:171], v[100:103]
	v_mfma_f32_16x16x32_bf16 v[96:99], v[152:155], v[168:171], v[96:99]
	v_mfma_f32_16x16x32_bf16 v[84:87], v[144:147], v[176:179], v[84:87]
	v_mfma_f32_16x16x32_bf16 v[80:83], v[152:155], v[176:179], v[80:83]
	v_mfma_f32_16x16x32_bf16 v[68:71], v[144:147], v[198:201], v[68:71]
	v_mfma_f32_16x16x32_bf16 v[64:67], v[152:155], v[198:201], v[64:67]
	v_mfma_f32_16x16x32_bf16 v[116:119], v[148:151], v[164:167], v[116:119]
	v_mfma_f32_16x16x32_bf16 v[112:115], v[156:159], v[164:167], v[112:115]
	v_mfma_f32_16x16x32_bf16 v[100:103], v[148:151], v[172:175], v[100:103]
	v_mfma_f32_16x16x32_bf16 v[96:99], v[156:159], v[172:175], v[96:99]
	v_mfma_f32_16x16x32_bf16 v[84:87], v[148:151], v[194:197], v[84:87]
	v_mfma_f32_16x16x32_bf16 v[80:83], v[156:159], v[194:197], v[80:83]
	v_mfma_f32_16x16x32_bf16 v[68:71], v[148:151], v[202:205], v[68:71]
	v_mfma_f32_16x16x32_bf16 v[64:67], v[156:159], v[202:205], v[64:67]
	s_barrier
; #define PG8_LDA(dst, b, h) do { _Pragma("unroll") for (int m = 0; m < 4; ++m) _Pragma("unroll") for (int k = 0; k < 2; ++k) dst[m][k] = *(const PG8_LAS bf16x8*)(lds + PG8_SA(b, h) + aoff + m * 2048 + k * 1024); } while (0)
; #define PG8_LDB(dst, b, h) do { _Pragma("unroll") for (int n = 0; n < 2; ++n) _Pragma("unroll") for (int k = 0; k < 2; ++k) dst[n][k] = *(const PG8_LAS bf16x8*)(lds + PG8_SB(b, h) + boff + n * 2048 + k * 1024); } while (0)
; #define PG8_WAIT_V(n) asm volatile("s_waitcnt vmcnt(" #n ")" ::: "memory")
; #define PG8_WAIT_L(n) asm volatile("s_waitcnt lgkmcnt(" #n ")" ::: "memory")
; #define PG8_BAR __builtin_amdgcn_s_barrier()
; #define PG8_SCHED __builtin_amdgcn_sched_barrier(0)
; template <class Epi, class Sched, bool ALIGN_EPI = false, bool SP2 = false, bool F8 = false, bool I8 = false, bool PF = false>
; __device__ __forceinline__ void gemm_phase(PG8_LAS unsigned char* lds, const Gemm g, const Sched& S, const Epi& E, const int wave_) {
;     ...
;             PG8_LDA(At, 0, 1); PG8_STAGE(PG8_SB(0, 0), b2, voffB); PG8_STAGE(PG8_SB(0, 1), b2 + hstep, voffB); PG8_STAGE(PG8_SA(0, 0), a2, voffA);
;             PG8_WAIT_V(8); PG8_WAIT_L(0); PG8_BAR; PG8_MMA(1, 0, At, B0); PG8_MMA(1, 1, At, B1); PG8_BAR; PG8_SCHED;
;             PG8_LDB(B0, 1, 0); PG8_LDB(B1, 1, 1); PG8_SCHED; PG8_LDA(At, 1, 0); PG8_STAGE(PG8_SA(0, 1), a2 + hstep, voffA);
;             PG8_WAIT_V(8); PG8_WAIT_L(0); PG8_BAR; PG8_MMA(0, 0, At, B0); PG8_MMA(0, 1, At, B1); PG8_BAR; PG8_SCHED;
	s_add_i32 s67, s55, s40
	v_lshl_add_u64 v[206:207], s[34:35], 0, v[184:185]
	s_mov_b32 m0, s67
	ds_read_b128 v[160:163], v211 offset:16384
	ds_read_b128 v[164:167], v211 offset:17408
	ds_read_b128 v[168:171], v211 offset:18432
	ds_read_b128 v[172:175], v211 offset:19456
	ds_read_b128 v[176:179], v211 offset:20480
	ds_read_b128 v[194:197], v211 offset:21504
	ds_read_b128 v[198:201], v211 offset:22528
	ds_read_b128 v[202:205], v211 offset:23552
	global_load_lds_dwordx4 v[206:207], off
	s_add_i32 m0, s67, 0x2000
	s_add_u32 s68, s34, 0x40000
	v_lshl_add_u64 v[212:213], s[34:35], 0, v[180:181]
	s_addc_u32 s69, s35, 0
	s_add_i32 s67, s56, s40
	global_load_lds_dwordx4 v[212:213], off
	v_lshl_add_u64 v[214:215], s[68:69], 0, v[184:185]
	s_mov_b32 m0, s67
	v_lshl_add_u64 v[216:217], s[36:37], 0, v[182:183]
	global_load_lds_dwordx4 v[214:215], off
	v_lshl_add_u64 v[214:215], s[68:69], 0, v[180:181]
	s_add_i32 m0, s67, 0x2000
	s_nop 0
	global_load_lds_dwordx4 v[214:215], off
	v_lshl_add_u64 v[214:215], s[36:37], 0, v[186:187]
	s_mov_b32 m0, s29
	s_nop 0
	global_load_lds_dwordx4 v[214:215], off
	s_mov_b32 m0, s41
	s_nop 0
	global_load_lds_dwordx4 v[216:217], off
	s_waitcnt vmcnt(8)
	s_waitcnt lgkmcnt(0)
	s_barrier
	s_waitcnt lgkmcnt(0)
	v_mfma_f32_16x16x32_bf16 v[60:63], v[128:131], v[160:163], v[60:63]
	v_mfma_f32_16x16x32_bf16 v[56:59], v[136:139], v[160:163], v[56:59]
	v_mfma_f32_16x16x32_bf16 v[44:47], v[128:131], v[168:171], v[44:47]
	v_mfma_f32_16x16x32_bf16 v[40:43], v[136:139], v[168:171], v[40:43]
	v_mfma_f32_16x16x32_bf16 v[28:31], v[128:131], v[176:179], v[28:31]
	v_mfma_f32_16x16x32_bf16 v[24:27], v[136:139], v[176:179], v[24:27]
	v_mfma_f32_16x16x32_bf16 v[12:15], v[128:131], v[198:201], v[12:15]
	v_mfma_f32_16x16x32_bf16 v[8:11], v[136:139], v[198:201], v[8:11]
	v_mfma_f32_16x16x32_bf16 v[60:63], v[132:135], v[164:167], v[60:63]
	v_mfma_f32_16x16x32_bf16 v[56:59], v[140:143], v[164:167], v[56:59]
	v_mfma_f32_16x16x32_bf16 v[44:47], v[132:135], v[172:175], v[44:47]
	v_mfma_f32_16x16x32_bf16 v[40:43], v[140:143], v[172:175], v[40:43]
	v_mfma_f32_16x16x32_bf16 v[28:31], v[132:135], v[194:197], v[28:31]
	v_mfma_f32_16x16x32_bf16 v[24:27], v[140:143], v[194:197], v[24:27]
	v_mfma_f32_16x16x32_bf16 v[12:15], v[132:135], v[202:205], v[12:15]
	v_mfma_f32_16x16x32_bf16 v[8:11], v[140:143], v[202:205], v[8:11]
	v_mfma_f32_16x16x32_bf16 v[52:55], v[144:147], v[160:163], v[52:55]
	v_mfma_f32_16x16x32_bf16 v[48:51], v[152:155], v[160:163], v[48:51]
	v_mfma_f32_16x16x32_bf16 v[36:39], v[144:147], v[168:171], v[36:39]
	v_mfma_f32_16x16x32_bf16 v[32:35], v[152:155], v[168:171], v[32:35]
	v_mfma_f32_16x16x32_bf16 v[20:23], v[144:147], v[176:179], v[20:23]
	v_mfma_f32_16x16x32_bf16 v[16:19], v[152:155], v[176:179], v[16:19]
	v_mfma_f32_16x16x32_bf16 v[4:7], v[144:147], v[198:201], v[4:7]
	v_mfma_f32_16x16x32_bf16 v[0:3], v[152:155], v[198:201], v[0:3]
	v_mfma_f32_16x16x32_bf16 v[52:55], v[148:151], v[164:167], v[52:55]
	v_mfma_f32_16x16x32_bf16 v[48:51], v[156:159], v[164:167], v[48:51]
	v_mfma_f32_16x16x32_bf16 v[36:39], v[148:151], v[172:175], v[36:39]
	v_mfma_f32_16x16x32_bf16 v[32:35], v[156:159], v[172:175], v[32:35]
	v_mfma_f32_16x16x32_bf16 v[20:23], v[148:151], v[194:197], v[20:23]
	v_mfma_f32_16x16x32_bf16 v[16:19], v[156:159], v[194:197], v[16:19]
	v_mfma_f32_16x16x32_bf16 v[4:7], v[148:151], v[202:205], v[4:7]
	v_mfma_f32_16x16x32_bf16 v[0:3], v[156:159], v[202:205], v[0:3]
	s_barrier
	s_add_i32 s67, 0, 0x18000
	s_add_i32 s68, 0, 0x1c000
	v_add_u32_e32 v140, s67, v208
	v_add_u32_e32 v156, s68, v208
	ds_read_b128 v[128:131], v140
	ds_read_b128 v[132:135], v140 offset:1024
	ds_read_b128 v[136:139], v140 offset:2048
	ds_read_b128 v[140:143], v140 offset:3072
	ds_read_b128 v[144:147], v156
	ds_read_b128 v[148:151], v156 offset:1024
	ds_read_b128 v[152:155], v156 offset:2048
	ds_read_b128 v[156:159], v156 offset:3072
	s_add_u32 s36, s36, 0x40000
	s_addc_u32 s37, s37, 0
	s_mov_b32 m0, s42
	v_lshl_add_u64 v[218:219], s[36:37], 0, v[186:187]
	ds_read_b128 v[160:163], v211 offset:32768
	ds_read_b128 v[164:167], v211 offset:33792
	ds_read_b128 v[168:171], v211 offset:34816
	ds_read_b128 v[172:175], v211 offset:35840
	ds_read_b128 v[176:179], v211 offset:36864
	ds_read_b128 v[194:197], v211 offset:37888
	ds_read_b128 v[198:201], v211 offset:38912
	ds_read_b128 v[202:205], v211 offset:39936
	global_load_lds_dwordx4 v[218:219], off
	v_lshl_add_u64 v[218:219], s[36:37], 0, v[182:183]
	s_mov_b32 m0, s43
	s_nop 0
	global_load_lds_dwordx4 v[218:219], off
	s_waitcnt vmcnt(8)
	s_waitcnt lgkmcnt(0)
	s_barrier
; #define PG8_LDA(dst, b, h) do { _Pragma("unroll") for (int m = 0; m < 4; ++m) _Pragma("unroll") for (int k = 0; k < 2; ++k) dst[m][k] = *(const PG8_LAS bf16x8*)(lds + PG8_SA(b, h) + aoff + m * 2048 + k * 1024); } while (0)
; #define PG8_WAIT_V(n) asm volatile("s_waitcnt vmcnt(" #n ")" ::: "memory")
; #define PG8_WAIT_L(n) asm volatile("s_waitcnt lgkmcnt(" #n ")" ::: "memory")
; #define PG8_BAR __builtin_amdgcn_s_barrier()
; #define PG8_SCHED __builtin_amdgcn_sched_barrier(0)
; template <class Epi, class Sched, bool ALIGN_EPI = false, bool SP2 = false, bool F8 = false, bool I8 = false, bool PF = false>
; __device__ __forceinline__ void gemm_phase(PG8_LAS unsigned char* lds, const Gemm g, const Sched& S, const Epi& E, const int wave_) {
;     ...
;             PG8_WAIT_V(8); PG8_WAIT_L(0); PG8_BAR; PG8_MMA(0, 0, At, B0); PG8_MMA(0, 1, At, B1); PG8_BAR; PG8_SCHED;
;             PG8_LDA(At, 1, 1); PG8_STAGE(PG8_SB(1, 0), b3, voffB); PG8_STAGE(PG8_SB(1, 1), b3 + hstep, voffB); PG8_STAGE(PG8_SA(1, 0), a3, voffA);
;             PG8_WAIT_V(8); PG8_WAIT_L(0); PG8_BAR; PG8_MMA(1, 0, At, B0); PG8_MMA(1, 1, At, B1); PG8_BAR; PG8_SCHED;
	s_waitcnt lgkmcnt(0)
	v_mfma_f32_16x16x32_bf16 v[124:127], v[128:131], v[160:163], v[124:127]
	v_mfma_f32_16x16x32_bf16 v[120:123], v[136:139], v[160:163], v[120:123]
	v_mfma_f32_16x16x32_bf16 v[108:111], v[128:131], v[168:171], v[108:111]
	v_mfma_f32_16x16x32_bf16 v[104:107], v[136:139], v[168:171], v[104:107]
	v_mfma_f32_16x16x32_bf16 v[92:95], v[128:131], v[176:179], v[92:95]
	v_mfma_f32_16x16x32_bf16 v[88:91], v[136:139], v[176:179], v[88:91]
	v_mfma_f32_16x16x32_bf16 v[76:79], v[128:131], v[198:201], v[76:79]
	v_mfma_f32_16x16x32_bf16 v[72:75], v[136:139], v[198:201], v[72:75]
	v_mfma_f32_16x16x32_bf16 v[124:127], v[132:135], v[164:167], v[124:127]
	v_mfma_f32_16x16x32_bf16 v[120:123], v[140:143], v[164:167], v[120:123]
	v_mfma_f32_16x16x32_bf16 v[108:111], v[132:135], v[172:175], v[108:111]
	v_mfma_f32_16x16x32_bf16 v[104:107], v[140:143], v[172:175], v[104:107]
	v_mfma_f32_16x16x32_bf16 v[92:95], v[132:135], v[194:197], v[92:95]
	v_mfma_f32_16x16x32_bf16 v[88:91], v[140:143], v[194:197], v[88:91]
	v_mfma_f32_16x16x32_bf16 v[76:79], v[132:135], v[202:205], v[76:79]
	v_mfma_f32_16x16x32_bf16 v[72:75], v[140:143], v[202:205], v[72:75]
	v_mfma_f32_16x16x32_bf16 v[116:119], v[144:147], v[160:163], v[116:119]
	v_mfma_f32_16x16x32_bf16 v[112:115], v[152:155], v[160:163], v[112:115]
	v_mfma_f32_16x16x32_bf16 v[100:103], v[144:147], v[168:171], v[100:103]
	v_mfma_f32_16x16x32_bf16 v[96:99], v[152:155], v[168:171], v[96:99]
	v_mfma_f32_16x16x32_bf16 v[84:87], v[144:147], v[176:179], v[84:87]
	v_mfma_f32_16x16x32_bf16 v[80:83], v[152:155], v[176:179], v[80:83]
	v_mfma_f32_16x16x32_bf16 v[68:71], v[144:147], v[198:201], v[68:71]
	v_mfma_f32_16x16x32_bf16 v[64:67], v[152:155], v[198:201], v[64:67]
	v_mfma_f32_16x16x32_bf16 v[116:119], v[148:151], v[164:167], v[116:119]
	v_mfma_f32_16x16x32_bf16 v[112:115], v[156:159], v[164:167], v[112:115]
	v_mfma_f32_16x16x32_bf16 v[100:103], v[148:151], v[172:175], v[100:103]
	v_mfma_f32_16x16x32_bf16 v[96:99], v[156:159], v[172:175], v[96:99]
	v_mfma_f32_16x16x32_bf16 v[84:87], v[148:151], v[194:197], v[84:87]
	v_mfma_f32_16x16x32_bf16 v[80:83], v[156:159], v[194:197], v[80:83]
	v_mfma_f32_16x16x32_bf16 v[68:71], v[148:151], v[202:205], v[68:71]
	v_mfma_f32_16x16x32_bf16 v[64:67], v[156:159], v[202:205], v[64:67]
	s_barrier
	s_add_i32 s36, s67, s40
	v_lshl_add_u64 v[206:207], v[206:207], 0, s[8:9]
	s_mov_b32 m0, s36
	ds_read_b128 v[160:163], v211 offset:49152
	ds_read_b128 v[164:167], v211 offset:50176
	ds_read_b128 v[168:171], v211 offset:51200
	ds_read_b128 v[172:175], v211 offset:52224
	ds_read_b128 v[176:179], v211 offset:53248
	ds_read_b128 v[194:197], v211 offset:54272
	ds_read_b128 v[198:201], v211 offset:55296
	ds_read_b128 v[202:205], v211 offset:56320
	global_load_lds_dwordx4 v[206:207], off
	s_add_i32 m0, s36, 0x2000
	s_add_u32 s34, s34, 0x40080
	v_lshl_add_u64 v[206:207], v[212:213], 0, s[8:9]
	s_addc_u32 s35, s35, 0
	s_add_i32 s36, s68, s40
	global_load_lds_dwordx4 v[206:207], off
	v_lshl_add_u64 v[206:207], s[34:35], 0, v[184:185]
	s_mov_b32 m0, s36
	s_nop 0
	global_load_lds_dwordx4 v[206:207], off
	v_lshl_add_u64 v[206:207], s[34:35], 0, v[180:181]
	s_add_i32 m0, s36, 0x2000
	s_nop 0
	global_load_lds_dwordx4 v[206:207], off
	v_lshl_add_u64 v[206:207], v[214:215], 0, s[8:9]
	s_mov_b32 m0, s52
	s_nop 0
	global_load_lds_dwordx4 v[206:207], off
	v_lshl_add_u64 v[206:207], v[216:217], 0, s[8:9]
	s_mov_b32 m0, s53
	s_nop 0
	global_load_lds_dwordx4 v[206:207], off
	s_waitcnt vmcnt(8)
	s_waitcnt lgkmcnt(0)
	s_barrier
	s_waitcnt lgkmcnt(0)
	v_mfma_f32_16x16x32_bf16 v[60:63], v[128:131], v[160:163], v[60:63]
	v_mfma_f32_16x16x32_bf16 v[56:59], v[136:139], v[160:163], v[56:59]
	v_mfma_f32_16x16x32_bf16 v[44:47], v[128:131], v[168:171], v[44:47]
	v_mfma_f32_16x16x32_bf16 v[40:43], v[136:139], v[168:171], v[40:43]
	v_mfma_f32_16x16x32_bf16 v[28:31], v[128:131], v[176:179], v[28:31]
	v_mfma_f32_16x16x32_bf16 v[24:27], v[136:139], v[176:179], v[24:27]
	v_mfma_f32_16x16x32_bf16 v[12:15], v[128:131], v[198:201], v[12:15]
	v_mfma_f32_16x16x32_bf16 v[8:11], v[136:139], v[198:201], v[8:11]
	v_mfma_f32_16x16x32_bf16 v[60:63], v[132:135], v[164:167], v[60:63]
	v_mfma_f32_16x16x32_bf16 v[56:59], v[140:143], v[164:167], v[56:59]
	v_mfma_f32_16x16x32_bf16 v[44:47], v[132:135], v[172:175], v[44:47]
	v_mfma_f32_16x16x32_bf16 v[40:43], v[140:143], v[172:175], v[40:43]
	v_mfma_f32_16x16x32_bf16 v[28:31], v[132:135], v[194:197], v[28:31]
	v_mfma_f32_16x16x32_bf16 v[24:27], v[140:143], v[194:197], v[24:27]
	v_mfma_f32_16x16x32_bf16 v[12:15], v[132:135], v[202:205], v[12:15]
	v_mfma_f32_16x16x32_bf16 v[8:11], v[140:143], v[202:205], v[8:11]
	v_mfma_f32_16x16x32_bf16 v[52:55], v[144:147], v[160:163], v[52:55]
	v_mfma_f32_16x16x32_bf16 v[48:51], v[152:155], v[160:163], v[48:51]
	v_mfma_f32_16x16x32_bf16 v[36:39], v[144:147], v[168:171], v[36:39]
	v_mfma_f32_16x16x32_bf16 v[32:35], v[152:155], v[168:171], v[32:35]
	v_mfma_f32_16x16x32_bf16 v[20:23], v[144:147], v[176:179], v[20:23]
	v_mfma_f32_16x16x32_bf16 v[16:19], v[152:155], v[176:179], v[16:19]
	v_mfma_f32_16x16x32_bf16 v[4:7], v[144:147], v[198:201], v[4:7]
	v_mfma_f32_16x16x32_bf16 v[0:3], v[152:155], v[198:201], v[0:3]
	v_mfma_f32_16x16x32_bf16 v[52:55], v[148:151], v[164:167], v[52:55]
	v_mfma_f32_16x16x32_bf16 v[48:51], v[156:159], v[164:167], v[48:51]
	v_mfma_f32_16x16x32_bf16 v[36:39], v[148:151], v[172:175], v[36:39]
	v_mfma_f32_16x16x32_bf16 v[32:35], v[156:159], v[172:175], v[32:35]
	v_mfma_f32_16x16x32_bf16 v[20:23], v[148:151], v[194:197], v[20:23]
	v_mfma_f32_16x16x32_bf16 v[16:19], v[156:159], v[194:197], v[16:19]
	v_mfma_f32_16x16x32_bf16 v[4:7], v[148:151], v[202:205], v[4:7]
	v_mfma_f32_16x16x32_bf16 v[0:3], v[156:159], v[202:205], v[0:3]
	s_add_i32 s66, s66, 2
	s_add_u32 s30, s30, 0x100
	s_addc_u32 s31, s31, 0
	s_add_u32 s64, s64, 0x100
	s_addc_u32 s65, s65, 0
	s_cmp_gt_u32 s66, 13
	s_barrier
	s_cbranch_scc0 .LBB0_1304
	s_and_b64 vcc, exec, s[10:11]
	s_cbranch_vccz .LBB0_1307
	s_barrier

; template <class Epi, class Sched, bool ALIGN_EPI = false, bool SP2 = false, bool F8 = false, bool I8 = false, bool PF = false>
; __device__ __forceinline__ void gemm_phase(PG8_LAS unsigned char* lds, const Gemm g, const Sched& S, const Epi& E, const int wave_) {
;     ...
;         const char* nA = has_next ? (const char*)g.A + (size_t)nxt.pm * tstep : cA; const char* nB = has_next ? (const char*)g.Bt + (size_t)nxt.pb * tstep : cB;
;         for (int t = 0; t < nt; t += 2) {
;             const bool last = (t == nt - 2);
;             const char* a1 = cA + (size_t)(t + 1) * kstep;
;             const char* a2 = last ? nA : cA + (size_t)(t + 2) * kstep; const char* b2 = last ? nB : cB + (size_t)(t + 2) * kstep;
;             const char* a3 = a2 + kstep; const char* b3 = b2 + kstep;
;             if (last && has_next) S.a_ready(nxt);
;             if constexpr (PF) {
;             PG8_STAGE(wr ? PG8_SA(0, 0) : PG8_SA(1, 1), wr ? a2 : a1 + hstep, voffA); PG8_STAGE(wr ? PG8_SB(0, 0) : PG8_SB(1, 1), wr ? b2 : cB + (size_t)(t + 1) * kstep + hstep, voffB);
;             PG8_WAIT_V(8); PG8_BAR;
;             PG8_X1(0); __builtin_amdgcn_s_waitcnt(0xC07F); PG8_BAR; PG8_SCHED;
;             PG8_STAGE(wr ? PG8_SA(0, 1) : PG8_SA(0, 0), wr ? a2 + hstep : a2, voffA); PG8_STAGE(wr ? PG8_SB(0, 1) : PG8_SB(0, 0), wr ? b2 + hstep : b2, voffB);
;             PG8_WAIT_V(8); PG8_BAR;
;             PG8_X2(0); __builtin_amdgcn_s_waitcnt(0xC07F); PG8_BAR; PG8_SCHED;
;             PG8_STAGE(wr ? PG8_SA(1, 0) : PG8_SA(0, 1), wr ? a3 : a2 + hstep, voffA); PG8_STAGE(wr ? PG8_SB(1, 0) : PG8_SB(0, 1), wr ? b3 : b2 + hstep, voffB);
;             PG8_WAIT_V(8); PG8_BAR;
;             PG8_X1(1); __builtin_amdgcn_s_waitcnt(0xC07F); PG8_BAR; PG8_SCHED;
;             PG8_STAGE(wr ? PG8_SA(1, 1) : PG8_SA(1, 0), wr ? a3 + hstep : a3, voffA); PG8_STAGE(wr ? PG8_SB(1, 1) : PG8_SB(1, 0), wr ? b3 + hstep : b3, voffB);
;             PG8_WAIT_V(8); PG8_BAR;
;             PG8_X2(1); __builtin_amdgcn_s_waitcnt(0xC07F); PG8_BAR; PG8_SCHED;
;             } else
;             if constexpr (SP2) {
;     ...
; #pragma unroll
;         for (int a = 0; a < 2; ++a)
; #pragma unroll
;             for (int b = 0; b < 2; ++b)
; #pragma unroll
;                 for (int m = 0; m < 4; ++m)
; #pragma unroll
;                     for (int n = 0; n < 2; ++n) acc[a][b][m][n] = (f32x4){0.f, 0.f, 0.f, 0.f};
.LBB0_1539:
	s_ashr_i32 s19, s18, 31
	s_lshl_b64 s[22:23], s[18:19], 18
	s_add_u32 s22, s58, s22
	s_addc_u32 s23, s59, s23
	s_and_b64 s[26:27], s[24:25], exec
	s_cselect_b32 s19, s23, s31
	s_cselect_b32 s21, s22, s30
	s_ashr_i32 s17, s16, 31
	s_lshl_b64 s[26:27], s[16:17], 18
	s_add_u32 s26, s40, s26
	s_addc_u32 s27, s41, s27
	s_and_b64 s[36:37], s[24:25], exec
	s_cselect_b32 s17, s27, s35
	s_cselect_b32 s71, s26, s34
	s_add_u32 s30, s30, 0x20080
	s_addc_u32 s31, s31, 0
	s_add_u32 s72, s34, 0x100
	v_mov_b32_e32 v32, 0
	s_addc_u32 s73, s35, 0
	s_mov_b32 s74, -2
	v_mov_b32_e32 v33, v32
	v_pk_mov_b32 v[34:35], 0, 0
	v_pk_mov_b32 v[40:41], 0, 0
	v_pk_mov_b32 v[42:43], 0, 0
	v_pk_mov_b32 v[48:49], 0, 0
	v_pk_mov_b32 v[50:51], 0, 0
	v_pk_mov_b32 v[56:57], 0, 0
	v_pk_mov_b32 v[58:59], 0, 0
	v_pk_mov_b32 v[64:65], 0, 0
	v_pk_mov_b32 v[66:67], 0, 0
	v_pk_mov_b32 v[72:73], 0, 0
	v_pk_mov_b32 v[74:75], 0, 0
	v_pk_mov_b32 v[80:81], 0, 0
	v_pk_mov_b32 v[82:83], 0, 0
	v_pk_mov_b32 v[88:89], 0, 0
	v_pk_mov_b32 v[90:91], 0, 0
	v_pk_mov_b32 v[36:37], 0, 0
	v_pk_mov_b32 v[38:39], 0, 0
	v_pk_mov_b32 v[44:45], 0, 0
	v_pk_mov_b32 v[46:47], 0, 0
	v_pk_mov_b32 v[52:53], 0, 0
	v_pk_mov_b32 v[54:55], 0, 0
	v_pk_mov_b32 v[60:61], 0, 0
	v_pk_mov_b32 v[62:63], 0, 0
	v_pk_mov_b32 v[68:69], 0, 0
	v_pk_mov_b32 v[70:71], 0, 0
	v_pk_mov_b32 v[76:77], 0, 0
	v_pk_mov_b32 v[78:79], 0, 0
	v_pk_mov_b32 v[84:85], 0, 0
	v_pk_mov_b32 v[86:87], 0, 0
	v_pk_mov_b32 v[92:93], 0, 0
	v_pk_mov_b32 v[94:95], 0, 0
	v_pk_mov_b32 v[96:97], 0, 0
	v_pk_mov_b32 v[98:99], 0, 0
	v_pk_mov_b32 v[104:105], 0, 0
	v_pk_mov_b32 v[106:107], 0, 0
	v_pk_mov_b32 v[112:113], 0, 0
	v_pk_mov_b32 v[114:115], 0, 0
	v_pk_mov_b32 v[120:121], 0, 0
	v_pk_mov_b32 v[122:123], 0, 0
	v_pk_mov_b32 v[128:129], 0, 0
	v_pk_mov_b32 v[130:131], 0, 0
	v_pk_mov_b32 v[136:137], 0, 0
	v_pk_mov_b32 v[138:139], 0, 0
	v_pk_mov_b32 v[144:145], 0, 0
	v_pk_mov_b32 v[146:147], 0, 0
	v_pk_mov_b32 v[152:153], 0, 0
	v_pk_mov_b32 v[154:155], 0, 0
	v_pk_mov_b32 v[100:101], 0, 0
	v_pk_mov_b32 v[102:103], 0, 0
	v_pk_mov_b32 v[108:109], 0, 0
	v_pk_mov_b32 v[110:111], 0, 0
	v_pk_mov_b32 v[116:117], 0, 0
	v_pk_mov_b32 v[118:119], 0, 0
	v_pk_mov_b32 v[124:125], 0, 0
	v_pk_mov_b32 v[126:127], 0, 0
	v_pk_mov_b32 v[132:133], 0, 0
	v_pk_mov_b32 v[134:135], 0, 0
	v_pk_mov_b32 v[140:141], 0, 0
	v_pk_mov_b32 v[142:143], 0, 0
	v_pk_mov_b32 v[148:149], 0, 0
	v_pk_mov_b32 v[150:151], 0, 0
	v_pk_mov_b32 v[156:157], 0, 0
	v_pk_mov_b32 v[158:159], 0, 0
.LBB0_1540:
	ds_read_b128 v[24:27], v181
	ds_read_b128 v[28:31], v181 offset:1024
	ds_read_b128 v[16:19], v181 offset:2048
	ds_read_b128 v[20:23], v181 offset:3072
	ds_read_b128 v[8:11], v182
	ds_read_b128 v[12:15], v182 offset:1024
	ds_read_b128 v[0:3], v182 offset:2048
	ds_read_b128 v[4:7], v182 offset:3072
	s_add_u32 s34, s30, 0xfffe0080
	s_addc_u32 s35, s31, -1
	s_cmp_eq_u32 s74, 4
	s_cselect_b32 s37, s19, s35
	s_cselect_b32 s36, s21, s34
	s_cselect_b32 s35, s17, s73
	s_cselect_b32 s34, s71, s72
	v_lshl_add_u64 v[210:211], s[30:31], 0, v[168:169]
	s_add_i32 m0, s29, 0xc000
	ds_read_b128 v[172:175], v183
	ds_read_b128 v[176:179], v183 offset:1024
	ds_read_b128 v[186:189], v183 offset:2048
	ds_read_b128 v[190:193], v183 offset:3072
	ds_read_b128 v[194:197], v183 offset:4096
	ds_read_b128 v[198:201], v183 offset:5120
	ds_read_b128 v[202:205], v183 offset:6144
	ds_read_b128 v[206:209], v183 offset:7168
	global_load_lds_dwordx4 v[210:211], off
	v_lshl_add_u64 v[210:211], s[30:31], 0, v[170:171]
	s_add_i32 m0, s29, 0xe000
	s_nop 0
	global_load_lds_dwordx4 v[210:211], off
	s_waitcnt vmcnt(8)
	s_waitcnt lgkmcnt(0)
	s_barrier
	s_waitcnt lgkmcnt(0)
	v_mfma_f32_16x16x128_f8f6f4 v[156:159], v[24:31], v[172:179], v[156:159]
	v_lshl_add_u64 v[222:223], s[34:35], 0, v[160:161]
	v_mfma_f32_16x16x128_f8f6f4 v[148:151], v[16:23], v[172:179], v[148:151]
	v_lshl_add_u64 v[224:225], s[34:35], 0, v[166:167]
	v_mfma_f32_16x16x128_f8f6f4 v[140:143], v[24:31], v[186:193], v[140:143]
	s_add_u32 s76, s34, 0x20000
	s_addc_u32 s77, s35, 0
	v_mfma_f32_16x16x128_f8f6f4 v[132:135], v[16:23], v[186:193], v[132:135]
	v_lshl_add_u64 v[226:227], s[76:77], 0, v[160:161]
	v_mfma_f32_16x16x128_f8f6f4 v[124:127], v[24:31], v[194:201], v[124:127]
	v_lshl_add_u64 v[228:229], s[76:77], 0, v[166:167]
	v_mfma_f32_16x16x128_f8f6f4 v[116:119], v[16:23], v[194:201], v[116:119]
	v_lshl_add_u64 v[230:231], s[36:37], 0, v[162:163]
	v_mfma_f32_16x16x128_f8f6f4 v[108:111], v[24:31], v[202:209], v[108:111]
	v_lshl_add_u64 v[232:233], s[36:37], 0, v[164:165]
	v_mfma_f32_16x16x128_f8f6f4 v[100:103], v[16:23], v[202:209], v[100:103]
	v_mfma_f32_16x16x128_f8f6f4 v[152:155], v[8:15], v[172:179], v[152:155]
	v_mfma_f32_16x16x128_f8f6f4 v[144:147], v[0:7], v[172:179], v[144:147]
	v_mfma_f32_16x16x128_f8f6f4 v[136:139], v[8:15], v[186:193], v[136:139]
	v_mfma_f32_16x16x128_f8f6f4 v[128:131], v[0:7], v[186:193], v[128:131]
	v_mfma_f32_16x16x128_f8f6f4 v[120:123], v[8:15], v[194:201], v[120:123]
	v_mfma_f32_16x16x128_f8f6f4 v[112:115], v[0:7], v[194:201], v[112:115]
	v_mfma_f32_16x16x128_f8f6f4 v[104:107], v[8:15], v[202:209], v[104:107]
	v_mfma_f32_16x16x128_f8f6f4 v[96:99], v[0:7], v[202:209], v[96:99]
	s_barrier
	s_add_i32 s75, s55, s39
	s_mov_b32 m0, s75
	ds_read_b128 v[186:189], v183 offset:16384
	ds_read_b128 v[190:193], v183 offset:17408
	ds_read_b128 v[194:197], v183 offset:18432
	ds_read_b128 v[198:201], v183 offset:19456
	ds_read_b128 v[202:205], v183 offset:20480
	ds_read_b128 v[206:209], v183 offset:21504
	ds_read_b128 v[210:213], v183 offset:22528
	ds_read_b128 v[214:217], v183 offset:23552
	global_load_lds_dwordx4 v[222:223], off
	s_add_i32 m0, s75, 0x2000
	s_add_i32 s75, s64, s39
	global_load_lds_dwordx4 v[224:225], off
	s_mov_b32 m0, s75
	s_nop 0
	global_load_lds_dwordx4 v[226:227], off
	s_add_i32 m0, s75, 0x2000
	s_nop 0
	global_load_lds_dwordx4 v[228:229], off
	s_mov_b32 m0, s29
	s_nop 0
	global_load_lds_dwordx4 v[230:231], off
	s_mov_b32 m0, s42
	s_nop 0
	global_load_lds_dwordx4 v[232:233], off
	s_waitcnt vmcnt(8)
	s_waitcnt lgkmcnt(0)
	s_barrier
; #define PG8_LDA(dst, b, h) do { _Pragma("unroll") for (int m = 0; m < 4; ++m) _Pragma("unroll") for (int k = 0; k < 2; ++k) dst[m][k] = *(const PG8_LAS bf16x8*)(lds + PG8_SA(b, h) + aoff + m * 2048 + k * 1024); } while (0)
; #define PG8_LDB(dst, b, h) do { _Pragma("unroll") for (int n = 0; n < 2; ++n) _Pragma("unroll") for (int k = 0; k < 2; ++k) dst[n][k] = *(const PG8_LAS bf16x8*)(lds + PG8_SB(b, h) + boff + n * 2048 + k * 1024); } while (0)
; #define PG8_WAIT_V(n) asm volatile("s_waitcnt vmcnt(" #n ")" ::: "memory")
; #define PG8_WAIT_L(n) asm volatile("s_waitcnt lgkmcnt(" #n ")" ::: "memory")
; #define PG8_BAR __builtin_amdgcn_s_barrier()
; #define PG8_SCHED __builtin_amdgcn_sched_barrier(0)
; template <class Epi, class Sched, bool ALIGN_EPI = false, bool SP2 = false, bool F8 = false, bool I8 = false, bool PF = false>
; __device__ __forceinline__ void gemm_phase(PG8_LAS unsigned char* lds, const Gemm g, const Sched& S, const Epi& E, const int wave_) {
;     ...
;             PG8_WAIT_V(8); PG8_WAIT_L(0); PG8_BAR; PG8_MMA(1, 0, At, B0); PG8_MMA(1, 1, At, B1); PG8_BAR; PG8_SCHED;
;             PG8_LDB(B0, 1, 0); PG8_LDB(B1, 1, 1); PG8_SCHED; PG8_LDA(At, 1, 0); PG8_STAGE(PG8_SA(0, 1), a2 + hstep, voffA);
;             PG8_WAIT_V(8); PG8_WAIT_L(0); PG8_BAR; PG8_MMA(0, 0, At, B0); PG8_MMA(0, 1, At, B1); PG8_BAR; PG8_SCHED;
;             PG8_LDA(At, 1, 1); PG8_STAGE(PG8_SB(1, 0), b3, voffB); PG8_STAGE(PG8_SB(1, 1), b3 + hstep, voffB); PG8_STAGE(PG8_SA(1, 0), a3, voffA);
;             PG8_WAIT_V(8); PG8_WAIT_L(0); PG8_BAR; PG8_MMA(1, 0, At, B0); PG8_MMA(1, 1, At, B1); PG8_BAR; PG8_SCHED;
	s_waitcnt lgkmcnt(0)
	v_mfma_f32_16x16x128_f8f6f4 v[92:95], v[24:31], v[186:193], v[92:95]
	v_mfma_f32_16x16x128_f8f6f4 v[84:87], v[16:23], v[186:193], v[84:87]
	v_mfma_f32_16x16x128_f8f6f4 v[76:79], v[24:31], v[194:201], v[76:79]
	v_mfma_f32_16x16x128_f8f6f4 v[68:71], v[16:23], v[194:201], v[68:71]
	v_mfma_f32_16x16x128_f8f6f4 v[60:63], v[24:31], v[202:209], v[60:63]
	v_mfma_f32_16x16x128_f8f6f4 v[52:55], v[16:23], v[202:209], v[52:55]
	v_mfma_f32_16x16x128_f8f6f4 v[44:47], v[24:31], v[210:217], v[44:47]
	v_mfma_f32_16x16x128_f8f6f4 v[36:39], v[16:23], v[210:217], v[36:39]
	v_mfma_f32_16x16x128_f8f6f4 v[88:91], v[8:15], v[186:193], v[88:91]
	v_mfma_f32_16x16x128_f8f6f4 v[80:83], v[0:7], v[186:193], v[80:83]
	v_mfma_f32_16x16x128_f8f6f4 v[72:75], v[8:15], v[194:201], v[72:75]
	v_mfma_f32_16x16x128_f8f6f4 v[64:67], v[0:7], v[194:201], v[64:67]
	v_mfma_f32_16x16x128_f8f6f4 v[56:59], v[8:15], v[202:209], v[56:59]
	v_mfma_f32_16x16x128_f8f6f4 v[48:51], v[0:7], v[202:209], v[48:51]
	v_mfma_f32_16x16x128_f8f6f4 v[40:43], v[8:15], v[210:217], v[40:43]
	v_mfma_f32_16x16x128_f8f6f4 v[32:35], v[0:7], v[210:217], v[32:35]
	s_barrier
	s_add_i32 s75, 0, 0x18000
	s_add_i32 s76, 0, 0x1c000
	v_add_u32_e32 v12, s75, v180
	v_add_u32_e32 v28, s76, v180
	ds_read_b128 v[0:3], v12
	ds_read_b128 v[4:7], v12 offset:1024
	ds_read_b128 v[8:11], v12 offset:2048
	ds_read_b128 v[12:15], v12 offset:3072
	ds_read_b128 v[16:19], v28
	ds_read_b128 v[20:23], v28 offset:1024
	ds_read_b128 v[24:27], v28 offset:2048
	ds_read_b128 v[28:31], v28 offset:3072
	s_add_u32 s36, s36, 0x20000
	s_addc_u32 s37, s37, 0
	s_mov_b32 m0, s43
	v_lshl_add_u64 v[218:219], s[36:37], 0, v[162:163]
	ds_read_b128 v[186:189], v183 offset:32768
	ds_read_b128 v[190:193], v183 offset:33792
	ds_read_b128 v[194:197], v183 offset:34816
	ds_read_b128 v[198:201], v183 offset:35840
	ds_read_b128 v[202:205], v183 offset:36864
	ds_read_b128 v[206:209], v183 offset:37888
	ds_read_b128 v[210:213], v183 offset:38912
	ds_read_b128 v[214:217], v183 offset:39936
	global_load_lds_dwordx4 v[218:219], off
	v_lshl_add_u64 v[218:219], s[36:37], 0, v[164:165]
	s_mov_b32 m0, s44
	s_nop 0
	global_load_lds_dwordx4 v[218:219], off
	s_waitcnt vmcnt(8)
	s_waitcnt lgkmcnt(0)
	s_barrier
	s_waitcnt lgkmcnt(0)
	v_mfma_f32_16x16x128_f8f6f4 v[156:159], v[0:7], v[186:193], v[156:159]
	v_lshl_add_u64 v[222:223], v[222:223], 0, s[8:9]
	v_mfma_f32_16x16x128_f8f6f4 v[148:151], v[8:15], v[186:193], v[148:151]
	v_lshl_add_u64 v[224:225], v[224:225], 0, s[8:9]
	v_mfma_f32_16x16x128_f8f6f4 v[140:143], v[0:7], v[194:201], v[140:143]
	v_lshl_add_u64 v[226:227], v[226:227], 0, s[8:9]
	v_mfma_f32_16x16x128_f8f6f4 v[132:135], v[8:15], v[194:201], v[132:135]
	v_lshl_add_u64 v[228:229], v[228:229], 0, s[8:9]
	v_mfma_f32_16x16x128_f8f6f4 v[124:127], v[0:7], v[202:209], v[124:127]
	v_lshl_add_u64 v[230:231], v[230:231], 0, s[8:9]
	v_mfma_f32_16x16x128_f8f6f4 v[116:119], v[8:15], v[202:209], v[116:119]
	v_lshl_add_u64 v[232:233], v[232:233], 0, s[8:9]
	v_mfma_f32_16x16x128_f8f6f4 v[108:111], v[0:7], v[210:217], v[108:111]
	v_mfma_f32_16x16x128_f8f6f4 v[100:103], v[8:15], v[210:217], v[100:103]
	v_mfma_f32_16x16x128_f8f6f4 v[152:155], v[16:23], v[186:193], v[152:155]
	v_mfma_f32_16x16x128_f8f6f4 v[144:147], v[24:31], v[186:193], v[144:147]
	v_mfma_f32_16x16x128_f8f6f4 v[136:139], v[16:23], v[194:201], v[136:139]
	v_mfma_f32_16x16x128_f8f6f4 v[128:131], v[24:31], v[194:201], v[128:131]
	v_mfma_f32_16x16x128_f8f6f4 v[120:123], v[16:23], v[202:209], v[120:123]
	v_mfma_f32_16x16x128_f8f6f4 v[112:115], v[24:31], v[202:209], v[112:115]
	v_mfma_f32_16x16x128_f8f6f4 v[104:107], v[16:23], v[210:217], v[104:107]
	v_mfma_f32_16x16x128_f8f6f4 v[96:99], v[24:31], v[210:217], v[96:99]
	s_barrier
	s_add_i32 s36, s75, s39
	s_mov_b32 m0, s36
	ds_read_b128 v[186:189], v183 offset:49152
	ds_read_b128 v[190:193], v183 offset:50176
	ds_read_b128 v[194:197], v183 offset:51200
	ds_read_b128 v[198:201], v183 offset:52224
	ds_read_b128 v[202:205], v183 offset:53248
	ds_read_b128 v[206:209], v183 offset:54272
	ds_read_b128 v[210:213], v183 offset:55296
	ds_read_b128 v[214:217], v183 offset:56320
	global_load_lds_dwordx4 v[222:223], off
	s_add_i32 m0, s36, 0x2000
	s_add_u32 s34, s34, 0x20080
	s_addc_u32 s35, s35, 0
	s_add_i32 s36, s76, s39
	global_load_lds_dwordx4 v[224:225], off
	s_mov_b32 m0, s36
	s_nop 0
	global_load_lds_dwordx4 v[226:227], off
	s_add_i32 m0, s36, 0x2000
	s_nop 0
	global_load_lds_dwordx4 v[228:229], off
	s_mov_b32 m0, s48
	s_nop 0
	global_load_lds_dwordx4 v[230:231], off
	s_mov_b32 m0, s49
	s_nop 0
	global_load_lds_dwordx4 v[232:233], off
	s_waitcnt vmcnt(8)
	s_waitcnt lgkmcnt(0)
	s_barrier
	s_waitcnt lgkmcnt(0)
	v_mfma_f32_16x16x128_f8f6f4 v[92:95], v[0:7], v[186:193], v[92:95]
	v_mfma_f32_16x16x128_f8f6f4 v[84:87], v[8:15], v[186:193], v[84:87]
	v_mfma_f32_16x16x128_f8f6f4 v[76:79], v[0:7], v[194:201], v[76:79]
	v_mfma_f32_16x16x128_f8f6f4 v[68:71], v[8:15], v[194:201], v[68:71]
	v_mfma_f32_16x16x128_f8f6f4 v[60:63], v[0:7], v[202:209], v[60:63]
	v_mfma_f32_16x16x128_f8f6f4 v[52:55], v[8:15], v[202:209], v[52:55]
	v_mfma_f32_16x16x128_f8f6f4 v[44:47], v[0:7], v[210:217], v[44:47]
	v_mfma_f32_16x16x128_f8f6f4 v[36:39], v[8:15], v[210:217], v[36:39]
	v_mfma_f32_16x16x128_f8f6f4 v[88:91], v[16:23], v[186:193], v[88:91]
	v_mfma_f32_16x16x128_f8f6f4 v[80:83], v[24:31], v[186:193], v[80:83]
	v_mfma_f32_16x16x128_f8f6f4 v[72:75], v[16:23], v[194:201], v[72:75]
	v_mfma_f32_16x16x128_f8f6f4 v[64:67], v[24:31], v[194:201], v[64:67]
	v_mfma_f32_16x16x128_f8f6f4 v[56:59], v[16:23], v[202:209], v[56:59]
	v_mfma_f32_16x16x128_f8f6f4 v[48:51], v[24:31], v[202:209], v[48:51]
	v_mfma_f32_16x16x128_f8f6f4 v[40:43], v[16:23], v[210:217], v[40:43]
	v_mfma_f32_16x16x128_f8f6f4 v[32:35], v[24:31], v[210:217], v[32:35]
	s_add_i32 s74, s74, 2
	s_add_u32 s30, s30, 0x100
	s_addc_u32 s31, s31, 0
	s_add_u32 s72, s72, 0x100
	s_addc_u32 s73, s73, 0
	s_cmp_gt_u32 s74, 5
	s_barrier
	s_cbranch_scc0 .LBB0_1540
	s_and_b64 vcc, exec, s[10:11]
	s_cbranch_vccz .LBB0_1543
	s_barrier

; #define PG8_BAR __builtin_amdgcn_s_barrier()
; template <class Epi, class Sched, bool ALIGN_EPI = false, bool SP2 = false, bool F8 = false, bool I8 = false, bool PF = false>
; __device__ __forceinline__ void gemm_phase(PG8_LAS unsigned char* lds, const Gemm g, const Sched& S, const Epi& E, const int wave_) {
;     ...
;         for (int t = 0; t < nt; t += 2) {
;             const bool last = (t == nt - 2);
;             const char* a1 = cA + (size_t)(t + 1) * kstep;
;             const char* a2 = last ? nA : cA + (size_t)(t + 2) * kstep; const char* b2 = last ? nB : cB + (size_t)(t + 2) * kstep;
;             const char* a3 = a2 + kstep; const char* b3 = b2 + kstep;
;             if (last && has_next) S.a_ready(nxt);
;             if constexpr (PF) {
;             PG8_STAGE(wr ? PG8_SA(0, 0) : PG8_SA(1, 1), wr ? a2 : a1 + hstep, voffA); PG8_STAGE(wr ? PG8_SB(0, 0) : PG8_SB(1, 1), wr ? b2 : cB + (size_t)(t + 1) * kstep + hstep, voffB);
;             PG8_WAIT_V(8); PG8_BAR;
;             PG8_X1(0); __builtin_amdgcn_s_waitcnt(0xC07F); PG8_BAR; PG8_SCHED;
;             PG8_STAGE(wr ? PG8_SA(0, 1) : PG8_SA(0, 0), wr ? a2 + hstep : a2, voffA); PG8_STAGE(wr ? PG8_SB(0, 1) : PG8_SB(0, 0), wr ? b2 + hstep : b2, voffB);
;             PG8_WAIT_V(8); PG8_BAR;
;             PG8_X2(0); __builtin_amdgcn_s_waitcnt(0xC07F); PG8_BAR; PG8_SCHED;
;             PG8_STAGE(wr ? PG8_SA(1, 0) : PG8_SA(0, 1), wr ? a3 : a2 + hstep, voffA); PG8_STAGE(wr ? PG8_SB(1, 0) : PG8_SB(0, 1), wr ? b3 : b2 + hstep, voffB);
;             PG8_WAIT_V(8); PG8_BAR;
;             PG8_X1(1); __builtin_amdgcn_s_waitcnt(0xC07F); PG8_BAR; PG8_SCHED;
;             PG8_STAGE(wr ? PG8_SA(1, 1) : PG8_SA(1, 0), wr ? a3 + hstep : a3, voffA); PG8_STAGE(wr ? PG8_SB(1, 1) : PG8_SB(1, 0), wr ? b3 + hstep : b3, voffB);
;             PG8_WAIT_V(8); PG8_BAR;
;             PG8_X2(1); __builtin_amdgcn_s_waitcnt(0xC07F); PG8_BAR; PG8_SCHED;
;             } else
;             if constexpr (SP2) {
;             PG8_LDB(B0, 0, 0); PG8_LDB(B1, 0, 1); PG8_SCHED; PG8_LDA(At, 0, 0); PG8_STAGE(PG8_SA(1, 1), a1 + hstep, voffA);
;     ...
; #pragma unroll
;         for (int a = 0; a < 2; ++a)
; #pragma unroll
;             for (int b = 0; b < 2; ++b)
; #pragma unroll
;                 for (int m = 0; m < 4; ++m)
; #pragma unroll
;                     for (int n = 0; n < 2; ++n) acc[a][b][m][n] = (f32x4){0.f, 0.f, 0.f, 0.f};
.LBB0_1620:
	s_add_u32 s71, s30, 0x100
	v_mov_b32_e32 v32, 0
	s_addc_u32 s72, s31, 0
	s_mov_b32 s73, -2
	v_mov_b32_e32 v33, v32
	v_pk_mov_b32 v[34:35], 0, 0
	v_pk_mov_b32 v[36:37], 0, 0
	v_pk_mov_b32 v[38:39], 0, 0
	v_pk_mov_b32 v[44:45], 0, 0
	v_pk_mov_b32 v[46:47], 0, 0
	v_pk_mov_b32 v[52:53], 0, 0
	v_pk_mov_b32 v[54:55], 0, 0
	v_pk_mov_b32 v[60:61], 0, 0
	v_pk_mov_b32 v[62:63], 0, 0
	v_pk_mov_b32 v[68:69], 0, 0
	v_pk_mov_b32 v[70:71], 0, 0
	v_pk_mov_b32 v[76:77], 0, 0
	v_pk_mov_b32 v[78:79], 0, 0
	v_pk_mov_b32 v[84:85], 0, 0
	v_pk_mov_b32 v[86:87], 0, 0
	v_pk_mov_b32 v[40:41], 0, 0
	v_pk_mov_b32 v[42:43], 0, 0
	v_pk_mov_b32 v[48:49], 0, 0
	v_pk_mov_b32 v[50:51], 0, 0
	v_pk_mov_b32 v[56:57], 0, 0
	v_pk_mov_b32 v[58:59], 0, 0
	v_pk_mov_b32 v[64:65], 0, 0
	v_pk_mov_b32 v[66:67], 0, 0
	v_pk_mov_b32 v[72:73], 0, 0
	v_pk_mov_b32 v[74:75], 0, 0
	v_pk_mov_b32 v[80:81], 0, 0
	v_pk_mov_b32 v[82:83], 0, 0
	v_pk_mov_b32 v[88:89], 0, 0
	v_pk_mov_b32 v[90:91], 0, 0
	v_pk_mov_b32 v[92:93], 0, 0
	v_pk_mov_b32 v[94:95], 0, 0
	v_pk_mov_b32 v[96:97], 0, 0
	v_pk_mov_b32 v[98:99], 0, 0
	v_pk_mov_b32 v[100:101], 0, 0
	v_pk_mov_b32 v[102:103], 0, 0
	v_pk_mov_b32 v[108:109], 0, 0
	v_pk_mov_b32 v[110:111], 0, 0
	v_pk_mov_b32 v[116:117], 0, 0
	v_pk_mov_b32 v[118:119], 0, 0
	v_pk_mov_b32 v[124:125], 0, 0
	v_pk_mov_b32 v[126:127], 0, 0
	v_pk_mov_b32 v[132:133], 0, 0
	v_pk_mov_b32 v[134:135], 0, 0
	v_pk_mov_b32 v[140:141], 0, 0
	v_pk_mov_b32 v[142:143], 0, 0
	v_pk_mov_b32 v[148:149], 0, 0
	v_pk_mov_b32 v[150:151], 0, 0
	v_pk_mov_b32 v[104:105], 0, 0
	v_pk_mov_b32 v[106:107], 0, 0
	v_pk_mov_b32 v[112:113], 0, 0
	v_pk_mov_b32 v[114:115], 0, 0
	v_pk_mov_b32 v[120:121], 0, 0
	v_pk_mov_b32 v[122:123], 0, 0
	v_pk_mov_b32 v[128:129], 0, 0
	v_pk_mov_b32 v[130:131], 0, 0
	v_pk_mov_b32 v[136:137], 0, 0
	v_pk_mov_b32 v[138:139], 0, 0
	v_pk_mov_b32 v[144:145], 0, 0
	v_pk_mov_b32 v[146:147], 0, 0
	v_pk_mov_b32 v[152:153], 0, 0
	v_pk_mov_b32 v[154:155], 0, 0
	v_pk_mov_b32 v[156:157], 0, 0
	v_pk_mov_b32 v[158:159], 0, 0
.LBB0_1621:
	ds_read_b128 v[24:27], v181
	ds_read_b128 v[28:31], v181 offset:1024
	ds_read_b128 v[16:19], v181 offset:2048
	ds_read_b128 v[20:23], v181 offset:3072
	ds_read_b128 v[8:11], v182
	ds_read_b128 v[12:15], v182 offset:1024
	ds_read_b128 v[0:3], v182 offset:2048
	ds_read_b128 v[4:7], v182 offset:3072
	s_add_u32 s30, s34, 0x100
	s_addc_u32 s31, s35, 0
	s_cmp_eq_u32 s73, 24
	s_cselect_b32 s39, s25, s31
	s_cselect_b32 s38, s24, s30
	s_cselect_b32 s37, s27, s72
	s_cselect_b32 s36, s26, s71
	v_lshl_add_u64 v[208:209], s[34:35], 0, v[168:169]
	s_add_i32 m0, s29, 0xc000
	ds_read_b128 v[172:175], v183
	ds_read_b128 v[176:179], v183 offset:1024
	ds_read_b128 v[184:187], v183 offset:2048
	ds_read_b128 v[188:191], v183 offset:3072
	ds_read_b128 v[192:195], v183 offset:4096
	ds_read_b128 v[196:199], v183 offset:5120
	ds_read_b128 v[200:203], v183 offset:6144
	ds_read_b128 v[204:207], v183 offset:7168
	global_load_lds_dwordx4 v[208:209], off
	v_lshl_add_u64 v[208:209], s[34:35], 0, v[170:171]
	s_add_i32 m0, s29, 0xe000
	s_nop 0
	global_load_lds_dwordx4 v[208:209], off
	s_waitcnt vmcnt(8)
	s_waitcnt lgkmcnt(0)
	s_barrier
	s_waitcnt lgkmcnt(0)
	v_mfma_f32_16x16x128_f8f6f4 v[156:159], v[24:31], v[172:179], v[156:159]
	v_mfma_f32_16x16x128_f8f6f4 v[152:155], v[16:23], v[172:179], v[152:155]
	v_mfma_f32_16x16x128_f8f6f4 v[144:147], v[24:31], v[184:191], v[144:147]
	v_mfma_f32_16x16x128_f8f6f4 v[136:139], v[16:23], v[184:191], v[136:139]
	v_mfma_f32_16x16x128_f8f6f4 v[128:131], v[24:31], v[192:199], v[128:131]
	v_mfma_f32_16x16x128_f8f6f4 v[120:123], v[16:23], v[192:199], v[120:123]
	v_mfma_f32_16x16x128_f8f6f4 v[112:115], v[24:31], v[200:207], v[112:115]
	v_mfma_f32_16x16x128_f8f6f4 v[104:107], v[16:23], v[200:207], v[104:107]
	v_mfma_f32_16x16x128_f8f6f4 v[148:151], v[8:15], v[172:179], v[148:151]
	v_mfma_f32_16x16x128_f8f6f4 v[140:143], v[0:7], v[172:179], v[140:143]
	v_mfma_f32_16x16x128_f8f6f4 v[132:135], v[8:15], v[184:191], v[132:135]
	v_mfma_f32_16x16x128_f8f6f4 v[124:127], v[0:7], v[184:191], v[124:127]
	v_mfma_f32_16x16x128_f8f6f4 v[116:119], v[8:15], v[192:199], v[116:119]
	v_mfma_f32_16x16x128_f8f6f4 v[108:111], v[0:7], v[192:199], v[108:111]
	v_mfma_f32_16x16x128_f8f6f4 v[100:103], v[8:15], v[200:207], v[100:103]
	v_mfma_f32_16x16x128_f8f6f4 v[96:99], v[0:7], v[200:207], v[96:99]
	s_barrier
	s_add_i32 s34, s53, s42
	v_lshl_add_u64 v[172:173], s[36:37], 0, v[160:161]
	s_mov_b32 m0, s34
	ds_read_b128 v[184:187], v183 offset:16384
	ds_read_b128 v[188:191], v183 offset:17408
	ds_read_b128 v[192:195], v183 offset:18432
	ds_read_b128 v[196:199], v183 offset:19456
	ds_read_b128 v[200:203], v183 offset:20480
	ds_read_b128 v[204:207], v183 offset:21504
	ds_read_b128 v[208:211], v183 offset:22528
	ds_read_b128 v[212:215], v183 offset:23552
	global_load_lds_dwordx4 v[172:173], off
	s_add_i32 m0, s34, 0x2000
	s_add_u32 s34, s36, 0x70000
	v_lshl_add_u64 v[174:175], s[36:37], 0, v[166:167]
	s_addc_u32 s35, s37, 0
	s_add_i32 s74, s54, s42
	global_load_lds_dwordx4 v[174:175], off
	v_lshl_add_u64 v[176:177], s[34:35], 0, v[160:161]
	s_mov_b32 m0, s74
	v_lshl_add_u64 v[178:179], s[38:39], 0, v[164:165]
	global_load_lds_dwordx4 v[176:177], off
	v_lshl_add_u64 v[176:177], s[34:35], 0, v[166:167]
	s_add_i32 m0, s74, 0x2000
	s_nop 0
	global_load_lds_dwordx4 v[176:177], off
	v_lshl_add_u64 v[176:177], s[38:39], 0, v[162:163]
	s_mov_b32 m0, s29
	s_nop 0
	global_load_lds_dwordx4 v[176:177], off
	s_mov_b32 m0, s45
	s_nop 0
	global_load_lds_dwordx4 v[178:179], off
	s_waitcnt vmcnt(8)
	s_waitcnt lgkmcnt(0)
	s_barrier
; #define PG8_LDA(dst, b, h) do { _Pragma("unroll") for (int m = 0; m < 4; ++m) _Pragma("unroll") for (int k = 0; k < 2; ++k) dst[m][k] = *(const PG8_LAS bf16x8*)(lds + PG8_SA(b, h) + aoff + m * 2048 + k * 1024); } while (0)
; #define PG8_LDB(dst, b, h) do { _Pragma("unroll") for (int n = 0; n < 2; ++n) _Pragma("unroll") for (int k = 0; k < 2; ++k) dst[n][k] = *(const PG8_LAS bf16x8*)(lds + PG8_SB(b, h) + boff + n * 2048 + k * 1024); } while (0)
; #define PG8_WAIT_V(n) asm volatile("s_waitcnt vmcnt(" #n ")" ::: "memory")
; #define PG8_WAIT_L(n) asm volatile("s_waitcnt lgkmcnt(" #n ")" ::: "memory")
; #define PG8_BAR __builtin_amdgcn_s_barrier()
; #define PG8_SCHED __builtin_amdgcn_sched_barrier(0)
; template <class Epi, class Sched, bool ALIGN_EPI = false, bool SP2 = false, bool F8 = false, bool I8 = false, bool PF = false>
; __device__ __forceinline__ void gemm_phase(PG8_LAS unsigned char* lds, const Gemm g, const Sched& S, const Epi& E, const int wave_) {
;     ...
;             PG8_WAIT_V(8); PG8_WAIT_L(0); PG8_BAR; PG8_MMA(1, 0, At, B0); PG8_MMA(1, 1, At, B1); PG8_BAR; PG8_SCHED;
;             PG8_LDB(B0, 1, 0); PG8_LDB(B1, 1, 1); PG8_SCHED; PG8_LDA(At, 1, 0); PG8_STAGE(PG8_SA(0, 1), a2 + hstep, voffA);
;             PG8_WAIT_V(8); PG8_WAIT_L(0); PG8_BAR; PG8_MMA(0, 0, At, B0); PG8_MMA(0, 1, At, B1); PG8_BAR; PG8_SCHED;
;             PG8_LDA(At, 1, 1); PG8_STAGE(PG8_SB(1, 0), b3, voffB); PG8_STAGE(PG8_SB(1, 1), b3 + hstep, voffB); PG8_STAGE(PG8_SA(1, 0), a3, voffA);
;             PG8_WAIT_V(8); PG8_WAIT_L(0); PG8_BAR; PG8_MMA(1, 0, At, B0); PG8_MMA(1, 1, At, B1); PG8_BAR; PG8_SCHED;
	s_waitcnt lgkmcnt(0)
	v_mfma_f32_16x16x128_f8f6f4 v[92:95], v[24:31], v[184:191], v[92:95]
	v_mfma_f32_16x16x128_f8f6f4 v[88:91], v[16:23], v[184:191], v[88:91]
	v_mfma_f32_16x16x128_f8f6f4 v[80:83], v[24:31], v[192:199], v[80:83]
	v_mfma_f32_16x16x128_f8f6f4 v[72:75], v[16:23], v[192:199], v[72:75]
	v_mfma_f32_16x16x128_f8f6f4 v[64:67], v[24:31], v[200:207], v[64:67]
	v_mfma_f32_16x16x128_f8f6f4 v[56:59], v[16:23], v[200:207], v[56:59]
	v_mfma_f32_16x16x128_f8f6f4 v[48:51], v[24:31], v[208:215], v[48:51]
	v_mfma_f32_16x16x128_f8f6f4 v[40:43], v[16:23], v[208:215], v[40:43]
	v_mfma_f32_16x16x128_f8f6f4 v[84:87], v[8:15], v[184:191], v[84:87]
	v_mfma_f32_16x16x128_f8f6f4 v[76:79], v[0:7], v[184:191], v[76:79]
	v_mfma_f32_16x16x128_f8f6f4 v[68:71], v[8:15], v[192:199], v[68:71]
	v_mfma_f32_16x16x128_f8f6f4 v[60:63], v[0:7], v[192:199], v[60:63]
	v_mfma_f32_16x16x128_f8f6f4 v[52:55], v[8:15], v[200:207], v[52:55]
	v_mfma_f32_16x16x128_f8f6f4 v[44:47], v[0:7], v[200:207], v[44:47]
	v_mfma_f32_16x16x128_f8f6f4 v[36:39], v[8:15], v[208:215], v[36:39]
	v_mfma_f32_16x16x128_f8f6f4 v[32:35], v[0:7], v[208:215], v[32:35]
	s_barrier
	s_add_i32 s74, 0, 0x18000
	s_add_i32 s75, 0, 0x1c000
	v_add_u32_e32 v12, s74, v180
	v_add_u32_e32 v28, s75, v180
	ds_read_b128 v[0:3], v12
	ds_read_b128 v[4:7], v12 offset:1024
	ds_read_b128 v[8:11], v12 offset:2048
	ds_read_b128 v[12:15], v12 offset:3072
	ds_read_b128 v[16:19], v28
	ds_read_b128 v[20:23], v28 offset:1024
	ds_read_b128 v[24:27], v28 offset:2048
	ds_read_b128 v[28:31], v28 offset:3072
	s_add_u32 s34, s38, 0x70000
	s_addc_u32 s35, s39, 0
	s_mov_b32 m0, s46
	v_lshl_add_u64 v[216:217], s[34:35], 0, v[162:163]
	ds_read_b128 v[184:187], v183 offset:32768
	ds_read_b128 v[188:191], v183 offset:33792
	ds_read_b128 v[192:195], v183 offset:34816
	ds_read_b128 v[196:199], v183 offset:35840
	ds_read_b128 v[200:203], v183 offset:36864
	ds_read_b128 v[204:207], v183 offset:37888
	ds_read_b128 v[208:211], v183 offset:38912
	ds_read_b128 v[212:215], v183 offset:39936
	global_load_lds_dwordx4 v[216:217], off
	v_lshl_add_u64 v[216:217], s[34:35], 0, v[164:165]
	s_mov_b32 m0, s47
	s_nop 0
	global_load_lds_dwordx4 v[216:217], off
	s_waitcnt vmcnt(8)
	s_waitcnt lgkmcnt(0)
	s_barrier
	s_waitcnt lgkmcnt(0)
	v_mfma_f32_16x16x128_f8f6f4 v[156:159], v[0:7], v[184:191], v[156:159]
	v_mfma_f32_16x16x128_f8f6f4 v[152:155], v[8:15], v[184:191], v[152:155]
	v_mfma_f32_16x16x128_f8f6f4 v[144:147], v[0:7], v[192:199], v[144:147]
	v_mfma_f32_16x16x128_f8f6f4 v[136:139], v[8:15], v[192:199], v[136:139]
	v_mfma_f32_16x16x128_f8f6f4 v[128:131], v[0:7], v[200:207], v[128:131]
	v_mfma_f32_16x16x128_f8f6f4 v[120:123], v[8:15], v[200:207], v[120:123]
	v_mfma_f32_16x16x128_f8f6f4 v[112:115], v[0:7], v[208:215], v[112:115]
	v_mfma_f32_16x16x128_f8f6f4 v[104:107], v[8:15], v[208:215], v[104:107]
	v_mfma_f32_16x16x128_f8f6f4 v[148:151], v[16:23], v[184:191], v[148:151]
	v_mfma_f32_16x16x128_f8f6f4 v[140:143], v[24:31], v[184:191], v[140:143]
	v_mfma_f32_16x16x128_f8f6f4 v[132:135], v[16:23], v[192:199], v[132:135]
	v_mfma_f32_16x16x128_f8f6f4 v[124:127], v[24:31], v[192:199], v[124:127]
	v_mfma_f32_16x16x128_f8f6f4 v[116:119], v[16:23], v[200:207], v[116:119]
	v_mfma_f32_16x16x128_f8f6f4 v[108:111], v[24:31], v[200:207], v[108:111]
	v_mfma_f32_16x16x128_f8f6f4 v[100:103], v[16:23], v[208:215], v[100:103]
	v_mfma_f32_16x16x128_f8f6f4 v[96:99], v[24:31], v[208:215], v[96:99]
	s_barrier
	s_add_i32 s34, s74, s42
	v_lshl_add_u64 v[172:173], v[172:173], 0, s[8:9]
	s_mov_b32 m0, s34
	ds_read_b128 v[184:187], v183 offset:49152
	ds_read_b128 v[188:191], v183 offset:50176
	ds_read_b128 v[192:195], v183 offset:51200
	ds_read_b128 v[196:199], v183 offset:52224
	ds_read_b128 v[200:203], v183 offset:53248
	ds_read_b128 v[204:207], v183 offset:54272
	ds_read_b128 v[208:211], v183 offset:55296
	ds_read_b128 v[212:215], v183 offset:56320
	global_load_lds_dwordx4 v[172:173], off
	s_add_i32 m0, s34, 0x2000
	s_add_u32 s34, s36, 0x70080
	v_lshl_add_u64 v[172:173], v[174:175], 0, s[8:9]
	s_addc_u32 s35, s37, 0
	s_add_i32 s36, s75, s42
	global_load_lds_dwordx4 v[172:173], off
	v_lshl_add_u64 v[172:173], s[34:35], 0, v[160:161]
	s_mov_b32 m0, s36
	s_nop 0
	global_load_lds_dwordx4 v[172:173], off
	v_lshl_add_u64 v[172:173], s[34:35], 0, v[166:167]
	s_add_i32 m0, s36, 0x2000
	s_nop 0
	global_load_lds_dwordx4 v[172:173], off
	v_lshl_add_u64 v[172:173], v[176:177], 0, s[8:9]
	s_mov_b32 m0, s51
	s_nop 0
	global_load_lds_dwordx4 v[172:173], off
	v_lshl_add_u64 v[172:173], v[178:179], 0, s[8:9]
	s_mov_b32 m0, s52
	s_nop 0
	global_load_lds_dwordx4 v[172:173], off
	s_waitcnt vmcnt(8)
	s_waitcnt lgkmcnt(0)
	s_barrier
	s_waitcnt lgkmcnt(0)
	v_mfma_f32_16x16x128_f8f6f4 v[92:95], v[0:7], v[184:191], v[92:95]
	v_mfma_f32_16x16x128_f8f6f4 v[88:91], v[8:15], v[184:191], v[88:91]
	v_mfma_f32_16x16x128_f8f6f4 v[80:83], v[0:7], v[192:199], v[80:83]
	v_mfma_f32_16x16x128_f8f6f4 v[72:75], v[8:15], v[192:199], v[72:75]
	v_mfma_f32_16x16x128_f8f6f4 v[64:67], v[0:7], v[200:207], v[64:67]
	v_mfma_f32_16x16x128_f8f6f4 v[56:59], v[8:15], v[200:207], v[56:59]
	v_mfma_f32_16x16x128_f8f6f4 v[48:51], v[0:7], v[208:215], v[48:51]
	v_mfma_f32_16x16x128_f8f6f4 v[40:43], v[8:15], v[208:215], v[40:43]
	v_mfma_f32_16x16x128_f8f6f4 v[84:87], v[16:23], v[184:191], v[84:87]
	v_mfma_f32_16x16x128_f8f6f4 v[76:79], v[24:31], v[184:191], v[76:79]
	v_mfma_f32_16x16x128_f8f6f4 v[68:71], v[16:23], v[192:199], v[68:71]
	v_mfma_f32_16x16x128_f8f6f4 v[60:63], v[24:31], v[192:199], v[60:63]
	v_mfma_f32_16x16x128_f8f6f4 v[52:55], v[16:23], v[200:207], v[52:55]
	v_mfma_f32_16x16x128_f8f6f4 v[44:47], v[24:31], v[200:207], v[44:47]
	v_mfma_f32_16x16x128_f8f6f4 v[36:39], v[16:23], v[208:215], v[36:39]
	v_mfma_f32_16x16x128_f8f6f4 v[32:35], v[24:31], v[208:215], v[32:35]
	s_add_i32 s73, s73, 2
	s_add_u32 s71, s71, 0x100
	s_addc_u32 s72, s72, 0
	s_cmp_gt_u32 s73, 25
	s_mov_b64 s[34:35], s[30:31]
	s_barrier
	s_cbranch_scc0 .LBB0_1621
	s_and_b64 vcc, exec, s[10:11]
	s_cbranch_vccz .LBB0_1624
	s_barrier

; #define PG8_LDA(dst, b, h) do { _Pragma("unroll") for (int m = 0; m < 4; ++m) _Pragma("unroll") for (int k = 0; k < 2; ++k) dst[m][k] = *(const PG8_LAS bf16x8*)(lds + PG8_SA(b, h) + aoff + m * 2048 + k * 1024); } while (0)
; #define PG8_LDB(dst, b, h) do { _Pragma("unroll") for (int n = 0; n < 2; ++n) _Pragma("unroll") for (int k = 0; k < 2; ++k) dst[n][k] = *(const PG8_LAS bf16x8*)(lds + PG8_SB(b, h) + boff + n * 2048 + k * 1024); } while (0)
; #define PG8_WAIT_V(n) asm volatile("s_waitcnt vmcnt(" #n ")" ::: "memory")
; #define PG8_WAIT_L(n) asm volatile("s_waitcnt lgkmcnt(" #n ")" ::: "memory")
; #define PG8_BAR __builtin_amdgcn_s_barrier()
; #define PG8_SCHED __builtin_amdgcn_sched_barrier(0)
; template <class Epi, class Sched, bool ALIGN_EPI = false, bool SP2 = false, bool F8 = false, bool I8 = false, bool PF = false>
; __device__ __forceinline__ void gemm_phase(PG8_LAS unsigned char* lds, const Gemm g, const Sched& S, const Epi& E, const int wave_) {
;     ...
;             PG8_LDB(B0, 0, 0); PG8_LDB(B1, 0, 1); PG8_SCHED; PG8_LDA(At, 0, 0); PG8_STAGE(PG8_SA(1, 1), a1 + hstep, voffA);
;             PG8_WAIT_V(8); PG8_WAIT_L(0); PG8_BAR; PG8_MMA(0, 0, At, B0); PG8_MMA(0, 1, At, B1); PG8_BAR; PG8_SCHED;
;             PG8_LDA(At, 0, 1); PG8_STAGE(PG8_SB(0, 0), b2, voffB); PG8_STAGE(PG8_SB(0, 1), b2 + hstep, voffB); PG8_STAGE(PG8_SA(0, 0), a2, voffA);
;             PG8_WAIT_V(8); PG8_WAIT_L(0); PG8_BAR; PG8_MMA(1, 0, At, B0); PG8_MMA(1, 1, At, B1); PG8_BAR; PG8_SCHED;
.LBB0_1718:
	ds_read_b128 v[24:27], v181
	ds_read_b128 v[28:31], v181 offset:1024
	ds_read_b128 v[16:19], v181 offset:2048
	ds_read_b128 v[20:23], v181 offset:3072
	ds_read_b128 v[8:11], v182
	ds_read_b128 v[12:15], v182 offset:1024
	ds_read_b128 v[0:3], v182 offset:2048
	ds_read_b128 v[4:7], v182 offset:3072
	s_add_u32 s30, s34, 0x100
	s_addc_u32 s31, s35, 0
	s_cmp_eq_u32 s73, 24
	s_cselect_b32 s39, s25, s31
	s_cselect_b32 s38, s24, s30
	s_cselect_b32 s37, s27, s72
	s_cselect_b32 s36, s26, s71
	v_lshl_add_u64 v[208:209], s[34:35], 0, v[168:169]
	s_add_i32 m0, s29, 0xc000
	ds_read_b128 v[172:175], v183
	ds_read_b128 v[176:179], v183 offset:1024
	ds_read_b128 v[184:187], v183 offset:2048
	ds_read_b128 v[188:191], v183 offset:3072
	ds_read_b128 v[192:195], v183 offset:4096
	ds_read_b128 v[196:199], v183 offset:5120
	ds_read_b128 v[200:203], v183 offset:6144
	ds_read_b128 v[204:207], v183 offset:7168
	global_load_lds_dwordx4 v[208:209], off
	v_lshl_add_u64 v[208:209], s[34:35], 0, v[170:171]
	s_add_i32 m0, s29, 0xe000
	s_nop 0
	global_load_lds_dwordx4 v[208:209], off
	s_waitcnt vmcnt(8)
	s_waitcnt lgkmcnt(0)
	s_barrier
	s_waitcnt lgkmcnt(0)
	v_mfma_f32_16x16x128_f8f6f4 v[156:159], v[24:31], v[172:179], v[156:159]
	v_mfma_f32_16x16x128_f8f6f4 v[152:155], v[16:23], v[172:179], v[152:155]
	v_mfma_f32_16x16x128_f8f6f4 v[144:147], v[24:31], v[184:191], v[144:147]
	v_mfma_f32_16x16x128_f8f6f4 v[136:139], v[16:23], v[184:191], v[136:139]
	v_mfma_f32_16x16x128_f8f6f4 v[128:131], v[24:31], v[192:199], v[128:131]
	v_mfma_f32_16x16x128_f8f6f4 v[120:123], v[16:23], v[192:199], v[120:123]
	v_mfma_f32_16x16x128_f8f6f4 v[112:115], v[24:31], v[200:207], v[112:115]
	v_mfma_f32_16x16x128_f8f6f4 v[104:107], v[16:23], v[200:207], v[104:107]
	v_mfma_f32_16x16x128_f8f6f4 v[148:151], v[8:15], v[172:179], v[148:151]
	v_mfma_f32_16x16x128_f8f6f4 v[140:143], v[0:7], v[172:179], v[140:143]
	v_mfma_f32_16x16x128_f8f6f4 v[132:135], v[8:15], v[184:191], v[132:135]
	v_mfma_f32_16x16x128_f8f6f4 v[124:127], v[0:7], v[184:191], v[124:127]
	v_mfma_f32_16x16x128_f8f6f4 v[116:119], v[8:15], v[192:199], v[116:119]
	v_mfma_f32_16x16x128_f8f6f4 v[108:111], v[0:7], v[192:199], v[108:111]
	v_mfma_f32_16x16x128_f8f6f4 v[100:103], v[8:15], v[200:207], v[100:103]
	v_mfma_f32_16x16x128_f8f6f4 v[96:99], v[0:7], v[200:207], v[96:99]
	s_barrier
	s_add_i32 s34, s53, s43
	v_lshl_add_u64 v[172:173], s[36:37], 0, v[160:161]
	s_mov_b32 m0, s34
	ds_read_b128 v[184:187], v183 offset:16384
	ds_read_b128 v[188:191], v183 offset:17408
	ds_read_b128 v[192:195], v183 offset:18432
	ds_read_b128 v[196:199], v183 offset:19456
	ds_read_b128 v[200:203], v183 offset:20480
	ds_read_b128 v[204:207], v183 offset:21504
	ds_read_b128 v[208:211], v183 offset:22528
	ds_read_b128 v[212:215], v183 offset:23552
	global_load_lds_dwordx4 v[172:173], off
	s_add_i32 m0, s34, 0x2000
	s_add_u32 s34, s36, 0x70000
	v_lshl_add_u64 v[174:175], s[36:37], 0, v[162:163]
	s_addc_u32 s35, s37, 0
	s_add_i32 s74, s54, s43
	global_load_lds_dwordx4 v[174:175], off
	v_lshl_add_u64 v[176:177], s[34:35], 0, v[160:161]
	s_mov_b32 m0, s74
	v_lshl_add_u64 v[178:179], s[38:39], 0, v[164:165]
	global_load_lds_dwordx4 v[176:177], off
	v_lshl_add_u64 v[176:177], s[34:35], 0, v[162:163]
	s_add_i32 m0, s74, 0x2000
	s_nop 0
	global_load_lds_dwordx4 v[176:177], off
	v_lshl_add_u64 v[176:177], s[38:39], 0, v[166:167]
	s_mov_b32 m0, s29
	s_nop 0
	global_load_lds_dwordx4 v[176:177], off
	s_mov_b32 m0, s45
	s_nop 0
	global_load_lds_dwordx4 v[178:179], off
	s_waitcnt vmcnt(8)
	s_waitcnt lgkmcnt(0)
	s_barrier
	s_waitcnt lgkmcnt(0)
	v_mfma_f32_16x16x128_f8f6f4 v[92:95], v[24:31], v[184:191], v[92:95]
	v_mfma_f32_16x16x128_f8f6f4 v[88:91], v[16:23], v[184:191], v[88:91]
	v_mfma_f32_16x16x128_f8f6f4 v[80:83], v[24:31], v[192:199], v[80:83]
	v_mfma_f32_16x16x128_f8f6f4 v[72:75], v[16:23], v[192:199], v[72:75]
	v_mfma_f32_16x16x128_f8f6f4 v[64:67], v[24:31], v[200:207], v[64:67]
	v_mfma_f32_16x16x128_f8f6f4 v[56:59], v[16:23], v[200:207], v[56:59]
	v_mfma_f32_16x16x128_f8f6f4 v[48:51], v[24:31], v[208:215], v[48:51]
	v_mfma_f32_16x16x128_f8f6f4 v[40:43], v[16:23], v[208:215], v[40:43]
	v_mfma_f32_16x16x128_f8f6f4 v[84:87], v[8:15], v[184:191], v[84:87]
	v_mfma_f32_16x16x128_f8f6f4 v[76:79], v[0:7], v[184:191], v[76:79]
	v_mfma_f32_16x16x128_f8f6f4 v[68:71], v[8:15], v[192:199], v[68:71]
	v_mfma_f32_16x16x128_f8f6f4 v[60:63], v[0:7], v[192:199], v[60:63]
	v_mfma_f32_16x16x128_f8f6f4 v[52:55], v[8:15], v[200:207], v[52:55]
	v_mfma_f32_16x16x128_f8f6f4 v[44:47], v[0:7], v[200:207], v[44:47]
	v_mfma_f32_16x16x128_f8f6f4 v[36:39], v[8:15], v[208:215], v[36:39]
	v_mfma_f32_16x16x128_f8f6f4 v[32:35], v[0:7], v[208:215], v[32:35]
	s_barrier
; #define PG8_LDA(dst, b, h) do { _Pragma("unroll") for (int m = 0; m < 4; ++m) _Pragma("unroll") for (int k = 0; k < 2; ++k) dst[m][k] = *(const PG8_LAS bf16x8*)(lds + PG8_SA(b, h) + aoff + m * 2048 + k * 1024); } while (0)
; #define PG8_LDB(dst, b, h) do { _Pragma("unroll") for (int n = 0; n < 2; ++n) _Pragma("unroll") for (int k = 0; k < 2; ++k) dst[n][k] = *(const PG8_LAS bf16x8*)(lds + PG8_SB(b, h) + boff + n * 2048 + k * 1024); } while (0)
; #define PG8_WAIT_V(n) asm volatile("s_waitcnt vmcnt(" #n ")" ::: "memory")
; #define PG8_WAIT_L(n) asm volatile("s_waitcnt lgkmcnt(" #n ")" ::: "memory")
; #define PG8_BAR __builtin_amdgcn_s_barrier()
; #define PG8_SCHED __builtin_amdgcn_sched_barrier(0)
; template <class Epi, class Sched, bool ALIGN_EPI = false, bool SP2 = false, bool F8 = false, bool I8 = false, bool PF = false>
; __device__ __forceinline__ void gemm_phase(PG8_LAS unsigned char* lds, const Gemm g, const Sched& S, const Epi& E, const int wave_) {
;     ...
;             PG8_LDB(B0, 1, 0); PG8_LDB(B1, 1, 1); PG8_SCHED; PG8_LDA(At, 1, 0); PG8_STAGE(PG8_SA(0, 1), a2 + hstep, voffA);
;             PG8_WAIT_V(8); PG8_WAIT_L(0); PG8_BAR; PG8_MMA(0, 0, At, B0); PG8_MMA(0, 1, At, B1); PG8_BAR; PG8_SCHED;
;             PG8_LDA(At, 1, 1); PG8_STAGE(PG8_SB(1, 0), b3, voffB); PG8_STAGE(PG8_SB(1, 1), b3 + hstep, voffB); PG8_STAGE(PG8_SA(1, 0), a3, voffA);
;             PG8_WAIT_V(8); PG8_WAIT_L(0); PG8_BAR; PG8_MMA(1, 0, At, B0); PG8_MMA(1, 1, At, B1); PG8_BAR; PG8_SCHED;
	s_add_i32 s74, 0, 0x18000
	s_add_i32 s75, 0, 0x1c000
	v_add_u32_e32 v12, s74, v180
	v_add_u32_e32 v28, s75, v180
	ds_read_b128 v[0:3], v12
	ds_read_b128 v[4:7], v12 offset:1024
	ds_read_b128 v[8:11], v12 offset:2048
	ds_read_b128 v[12:15], v12 offset:3072
	ds_read_b128 v[16:19], v28
	ds_read_b128 v[20:23], v28 offset:1024
	ds_read_b128 v[24:27], v28 offset:2048
	ds_read_b128 v[28:31], v28 offset:3072
	s_add_u32 s34, s38, 0x70000
	s_addc_u32 s35, s39, 0
	s_mov_b32 m0, s46
	v_lshl_add_u64 v[216:217], s[34:35], 0, v[166:167]
	ds_read_b128 v[184:187], v183 offset:32768
	ds_read_b128 v[188:191], v183 offset:33792
	ds_read_b128 v[192:195], v183 offset:34816
	ds_read_b128 v[196:199], v183 offset:35840
	ds_read_b128 v[200:203], v183 offset:36864
	ds_read_b128 v[204:207], v183 offset:37888
	ds_read_b128 v[208:211], v183 offset:38912
	ds_read_b128 v[212:215], v183 offset:39936
	global_load_lds_dwordx4 v[216:217], off
	v_lshl_add_u64 v[216:217], s[34:35], 0, v[164:165]
	s_mov_b32 m0, s47
	s_nop 0
	global_load_lds_dwordx4 v[216:217], off
	s_waitcnt vmcnt(8)
	s_waitcnt lgkmcnt(0)
	s_barrier
	s_waitcnt lgkmcnt(0)
	v_mfma_f32_16x16x128_f8f6f4 v[156:159], v[0:7], v[184:191], v[156:159]
	v_mfma_f32_16x16x128_f8f6f4 v[152:155], v[8:15], v[184:191], v[152:155]
	v_mfma_f32_16x16x128_f8f6f4 v[144:147], v[0:7], v[192:199], v[144:147]
	v_mfma_f32_16x16x128_f8f6f4 v[136:139], v[8:15], v[192:199], v[136:139]
	v_mfma_f32_16x16x128_f8f6f4 v[128:131], v[0:7], v[200:207], v[128:131]
	v_mfma_f32_16x16x128_f8f6f4 v[120:123], v[8:15], v[200:207], v[120:123]
	v_mfma_f32_16x16x128_f8f6f4 v[112:115], v[0:7], v[208:215], v[112:115]
	v_mfma_f32_16x16x128_f8f6f4 v[104:107], v[8:15], v[208:215], v[104:107]
	v_mfma_f32_16x16x128_f8f6f4 v[148:151], v[16:23], v[184:191], v[148:151]
	v_mfma_f32_16x16x128_f8f6f4 v[140:143], v[24:31], v[184:191], v[140:143]
	v_mfma_f32_16x16x128_f8f6f4 v[132:135], v[16:23], v[192:199], v[132:135]
	v_mfma_f32_16x16x128_f8f6f4 v[124:127], v[24:31], v[192:199], v[124:127]
	v_mfma_f32_16x16x128_f8f6f4 v[116:119], v[16:23], v[200:207], v[116:119]
	v_mfma_f32_16x16x128_f8f6f4 v[108:111], v[24:31], v[200:207], v[108:111]
	v_mfma_f32_16x16x128_f8f6f4 v[100:103], v[16:23], v[208:215], v[100:103]
	v_mfma_f32_16x16x128_f8f6f4 v[96:99], v[24:31], v[208:215], v[96:99]
	s_barrier
	s_add_i32 s34, s74, s43
	v_lshl_add_u64 v[172:173], v[172:173], 0, s[8:9]
	s_mov_b32 m0, s34
	ds_read_b128 v[184:187], v183 offset:49152
	ds_read_b128 v[188:191], v183 offset:50176
	ds_read_b128 v[192:195], v183 offset:51200
	ds_read_b128 v[196:199], v183 offset:52224
	ds_read_b128 v[200:203], v183 offset:53248
	ds_read_b128 v[204:207], v183 offset:54272
	ds_read_b128 v[208:211], v183 offset:55296
	ds_read_b128 v[212:215], v183 offset:56320
	global_load_lds_dwordx4 v[172:173], off
	s_add_i32 m0, s34, 0x2000
	s_add_u32 s34, s36, 0x70080
	v_lshl_add_u64 v[172:173], v[174:175], 0, s[8:9]
	s_addc_u32 s35, s37, 0
	s_add_i32 s36, s75, s43
	global_load_lds_dwordx4 v[172:173], off
	v_lshl_add_u64 v[172:173], s[34:35], 0, v[160:161]
	s_mov_b32 m0, s36
	s_nop 0
	global_load_lds_dwordx4 v[172:173], off
	v_lshl_add_u64 v[172:173], s[34:35], 0, v[162:163]
	s_add_i32 m0, s36, 0x2000
	s_nop 0
	global_load_lds_dwordx4 v[172:173], off
	v_lshl_add_u64 v[172:173], v[176:177], 0, s[8:9]
	s_mov_b32 m0, s51
	s_nop 0
	global_load_lds_dwordx4 v[172:173], off
	v_lshl_add_u64 v[172:173], v[178:179], 0, s[8:9]
	s_mov_b32 m0, s52
	s_nop 0
	global_load_lds_dwordx4 v[172:173], off
	s_waitcnt vmcnt(8)
	s_waitcnt lgkmcnt(0)
	s_barrier
	s_waitcnt lgkmcnt(0)
	v_mfma_f32_16x16x128_f8f6f4 v[92:95], v[0:7], v[184:191], v[92:95]
	v_mfma_f32_16x16x128_f8f6f4 v[88:91], v[8:15], v[184:191], v[88:91]
	v_mfma_f32_16x16x128_f8f6f4 v[80:83], v[0:7], v[192:199], v[80:83]
	v_mfma_f32_16x16x128_f8f6f4 v[72:75], v[8:15], v[192:199], v[72:75]
	v_mfma_f32_16x16x128_f8f6f4 v[64:67], v[0:7], v[200:207], v[64:67]
	v_mfma_f32_16x16x128_f8f6f4 v[56:59], v[8:15], v[200:207], v[56:59]
	v_mfma_f32_16x16x128_f8f6f4 v[48:51], v[0:7], v[208:215], v[48:51]
	v_mfma_f32_16x16x128_f8f6f4 v[40:43], v[8:15], v[208:215], v[40:43]
	v_mfma_f32_16x16x128_f8f6f4 v[84:87], v[16:23], v[184:191], v[84:87]
	v_mfma_f32_16x16x128_f8f6f4 v[76:79], v[24:31], v[184:191], v[76:79]
	v_mfma_f32_16x16x128_f8f6f4 v[68:71], v[16:23], v[192:199], v[68:71]
	v_mfma_f32_16x16x128_f8f6f4 v[60:63], v[24:31], v[192:199], v[60:63]
	v_mfma_f32_16x16x128_f8f6f4 v[52:55], v[16:23], v[200:207], v[52:55]
	v_mfma_f32_16x16x128_f8f6f4 v[44:47], v[24:31], v[200:207], v[44:47]
	v_mfma_f32_16x16x128_f8f6f4 v[36:39], v[16:23], v[208:215], v[36:39]
	v_mfma_f32_16x16x128_f8f6f4 v[32:35], v[24:31], v[208:215], v[32:35]
	s_add_i32 s73, s73, 2
	s_add_u32 s71, s71, 0x100
	s_addc_u32 s72, s72, 0
	s_cmp_gt_u32 s73, 25
	s_mov_b64 s[34:35], s[30:31]
	s_barrier
	s_cbranch_scc0 .LBB0_1718
	s_and_b64 vcc, exec, s[10:11]
	s_cbranch_vccz .LBB0_1721
	s_barrier
